# plus P2: relaxed first-iteration waits per epilogue branch and post-loop vmcnt(0)->vmcnt(8)
# baseline (speedup 1.0000x reference)
; #define PHASE_BASES() const KAS char* KA = (const KAS char*)__builtin_amdgcn_kernarg_segment_ptr(); asm volatile("" : "+s"(KA)); unsigned char* const ws = *(unsigned char* const KAS*)(KA + 8 * 27)
; #define w_in KARG(8)
; __global__ void __launch_bounds__(NWAVES * 64, 2) mk_fwd(Args args) {
;     ...
;     if (IN(2)) { PHASE_BASES();
;         if ((((bx >> 3) & 15) < 3) || (bx >> 3) == 8) {
;             { constexpr int I_IN = 32 * (PROJ_COLS / 64), NIT = I_IN + 3 * 32 * 32;
;               const MixerCopy Xm{w_in, w_ssd_out, w_sc_out, w_o, ssd_norm_w, WIN, WSSD, WSC, WO};
; #pragma unroll 1
;               for (;;) { int g0 = 0; if (lane == 0) g0 = I_IN + (int)__hip_atomic_fetch_add(ctl + CW_Q4, 8u, __ATOMIC_RELAXED, __HIP_MEMORY_SCOPE_AGENT);
;                   g0 = __builtin_amdgcn_readfirstlane(g0); if (g0 >= NIT) break;
; #pragma unroll 1
;                   for (int k = 0; k < 8; k += 2) wtile_copy_pair(mixer_tile_addr(Xm, g0 + k), mixer_tile_addr(Xm, g0 + k + 1), lane); } }
;             const ExpertCopy X{w_e1, w_e3, w_e2, W13, W2}; expert_copy_share(X, ctl + CW_Q1, lane); }
.LBB0_209:
	s_mov_b32 s98, 0
	s_cmp_lt_i32 s78, 3
	s_cselect_b64 s[0:1], -1, 0
	s_cmp_gt_i32 s79, 2
	s_cselect_b64 s[2:3], -1, 0
	s_and_b64 s[0:1], s[0:1], s[2:3]
	s_andn2_b64 vcc, exec, s[0:1]
	s_cbranch_vccnz .LBB0_539
	s_and_b32 s4, s88, 0x78
	s_mov_b64 s[2:3], s[74:75]
	s_cmp_gt_u32 s4, 23
	s_load_dwordx2 s[0:1], s[2:3], 0xd8
	s_cselect_b64 s[4:5], -1, 0
	s_and_b32 s6, s88, -8
	s_cmp_lg_u32 s6, 64
	s_cselect_b64 s[6:7], -1, 0
	s_and_b64 s[4:5], s[4:5], s[6:7]
	s_and_b64 vcc, exec, s[4:5]
	v_and_b32_e32 v130, 48, v0
	s_cbranch_vccnz .LBB0_305
	s_waitcnt lgkmcnt(0)
	s_add_u32 s18, s0, 0x1d200000
	s_load_dwordx2 s[4:5], s[2:3], 0x40
	s_load_dwordx4 s[12:15], s[2:3], 0x70
	s_load_dwordx2 s[10:11], s[2:3], 0x88
	s_load_dwordx2 s[16:17], s[2:3], 0x98
	s_addc_u32 s19, s1, 0
	s_add_u32 s6, s0, 0x1000000
	s_addc_u32 s7, s1, 0
	s_add_u32 s33, s0, 0x1800000
	s_addc_u32 s38, s1, 0
	v_lshlrev_b32_e32 v1, 2, v0
	s_add_u32 s39, s0, 0x2000000
	v_and_b32_e32 v132, 60, v1
	v_lshlrev_b32_e32 v1, 3, v0
	s_addc_u32 s40, s1, 0
	s_mov_b32 s21, 0
	v_cmp_eq_u32_e64 s[8:9], 0, v186
	v_mov_b32_e32 v135, 0
	v_and_b32_e32 v1, 0x78, v1
	v_or_b32_e32 v136, 15, v186
	s_movk_i32 s41, 0x1000
	s_movk_i32 s42, 0x2000
	s_branch .LBB0_214

;     __device__ __forceinline__ unsigned claim_issue(int wid, int lane) const { unsigned r = 0u; if (wid == 0 && lane == 0) { unsigned z; asm volatile("v_mov_b32 %0, 0" : "=v"(z)); r = __hip_atomic_fetch_add(q + z, 1u, __ATOMIC_RELAXED, __HIP_MEMORY_SCOPE_AGENT); } return r; }
;     __device__ __forceinline__ bool next(int i, pg8::Unit& u) const { const int s = i >= R ? 1 : 0; const bool ok = so.next(i - s * R, u); u.sel = s; return ok && i < 2 * R; }
; template <class Epi, class Sched, bool ALIGN_EPI = false, bool SP2 = false>
; __device__ __forceinline__ void gemm_phase(PG8_LAS unsigned char* lds, const Gemm g, const Sched& S, const Epi& E) {
;     ...
;     for (;;) {
;         const bool has_next = S.next(ui + 1, nxt);
;         unsigned pend = 0u; if constexpr (Sched::DYNAMIC) pend = S.claim_issue(wid, lane);
;         const char* nA = has_next ? (const char*)(nxt.sel ? g.A2 : g.A) + (size_t)nxt.pm * tstep : cA; const char* nB = has_next ? (const char*)(nxt.sel ? g.Bt2 : g.Bt) + (size_t)nxt.pn * tstep : cB;
;         for (int t = 0; t < nt; t += 2) {
;             const bool last = (t == nt - 2);
;             const char* a1 = cA + (size_t)(t + 1) * kstep;
;             const char* a2 = last ? nA : cA + (size_t)(t + 2) * kstep; const char* b2 = last ? nB : cB + (size_t)(t + 2) * kstep;
;             const char* a3 = a2 + kstep; const char* b3 = b2 + kstep;
;             if (last && has_next) S.a_ready(nxt);
;     ...
; #pragma unroll
;         for (int a = 0; a < 2; ++a)
; #pragma unroll
;             for (int b = 0; b < 2; ++b)
; #pragma unroll
;                 for (int m = 0; m < 4; ++m)
; #pragma unroll
;                     for (int n = 0; n < 2; ++n) acc[a][b][m][n] = (f32x4){0.f, 0.f, 0.f, 0.f};
;         cur = nxt; cA = nA; cB = nB; ++ui;
.LBB0_331:
	s_or_b64 exec, exec, s[0:1]
	s_ashr_i32 s53, s52, 31
	s_lshl_b64 s[0:1], s[52:53], 20
	s_add_u32 s58, s67, s0
	s_addc_u32 s59, s68, s1
	s_and_b64 s[0:1], s[56:57], exec
	s_cselect_b32 s7, s59, s5
	s_cselect_b32 s33, s58, s4
	s_ashr_i32 s55, s54, 31
	s_lshl_b64 s[0:1], s[54:55], 20
	s_add_u32 s60, s69, s0
	s_addc_u32 s61, s70, s1
	s_and_b64 s[0:1], s[56:57], exec
	s_cselect_b32 s53, s61, s3
	s_cselect_b32 s55, s60, s2
	s_add_u32 s0, s4, 0x80080
	s_addc_u32 s1, s5, 0
	s_add_u32 s84, s2, 0x100
	s_addc_u32 s85, s3, 0
	s_mov_b32 s95, -2
	v_mov_b32_e32 v3, v2
	v_mov_b32_e32 v4, v2
	v_mov_b32_e32 v5, v2
	v_mov_b32_e32 v6, v2
	v_mov_b32_e32 v7, v2
	v_mov_b32_e32 v8, v2
	v_mov_b32_e32 v9, v2
	v_mov_b32_e32 v10, v2
	v_mov_b32_e32 v11, v2
	v_mov_b32_e32 v12, v2
	v_mov_b32_e32 v13, v2
	v_mov_b32_e32 v18, v2
	v_mov_b32_e32 v19, v2
	v_mov_b32_e32 v20, v2
	v_mov_b32_e32 v21, v2
	v_mov_b32_e32 v26, v2
	v_mov_b32_e32 v27, v2
	v_mov_b32_e32 v28, v2
	v_mov_b32_e32 v29, v2
	v_mov_b32_e32 v34, v2
	v_mov_b32_e32 v35, v2
	v_mov_b32_e32 v36, v2
	v_mov_b32_e32 v37, v2
	v_mov_b32_e32 v42, v2
	v_mov_b32_e32 v43, v2
	v_mov_b32_e32 v44, v2
	v_mov_b32_e32 v45, v2
	v_mov_b32_e32 v50, v2
	v_mov_b32_e32 v51, v2
	v_mov_b32_e32 v52, v2
	v_mov_b32_e32 v53, v2
	v_mov_b32_e32 v14, v2
	v_mov_b32_e32 v15, v2
	v_mov_b32_e32 v16, v2
	v_mov_b32_e32 v17, v2
	v_mov_b32_e32 v22, v2
	v_mov_b32_e32 v23, v2
	v_mov_b32_e32 v24, v2
	v_mov_b32_e32 v25, v2
	v_mov_b32_e32 v30, v2
	v_mov_b32_e32 v31, v2
	v_mov_b32_e32 v32, v2
	v_mov_b32_e32 v33, v2
	v_mov_b32_e32 v38, v2
	v_mov_b32_e32 v39, v2
	v_mov_b32_e32 v40, v2
	v_mov_b32_e32 v41, v2
	v_mov_b32_e32 v46, v2
	v_mov_b32_e32 v47, v2
	v_mov_b32_e32 v48, v2
	v_mov_b32_e32 v49, v2
	v_mov_b32_e32 v54, v2
	v_mov_b32_e32 v55, v2
	v_mov_b32_e32 v56, v2
	v_mov_b32_e32 v57, v2
	v_mov_b32_e32 v58, v2
	v_mov_b32_e32 v59, v2
	v_mov_b32_e32 v60, v2
	v_mov_b32_e32 v61, v2
	v_mov_b32_e32 v62, v2
	v_mov_b32_e32 v63, v2
	v_mov_b32_e32 v64, v2
	v_mov_b32_e32 v65, v2
	v_mov_b32_e32 v66, v2
	v_mov_b32_e32 v67, v2
	v_mov_b32_e32 v68, v2
	v_mov_b32_e32 v69, v2
	v_mov_b32_e32 v70, v2
	v_mov_b32_e32 v71, v2
	v_mov_b32_e32 v72, v2
	v_mov_b32_e32 v73, v2
	v_mov_b32_e32 v74, v2
	v_mov_b32_e32 v75, v2
	v_mov_b32_e32 v76, v2
	v_mov_b32_e32 v77, v2
	v_mov_b32_e32 v82, v2
	v_mov_b32_e32 v83, v2
	v_mov_b32_e32 v84, v2
	v_mov_b32_e32 v85, v2
	v_mov_b32_e32 v90, v2
	v_mov_b32_e32 v91, v2
	v_mov_b32_e32 v92, v2
	v_mov_b32_e32 v93, v2
	v_mov_b32_e32 v98, v2
	v_mov_b32_e32 v99, v2
	v_mov_b32_e32 v100, v2
	v_mov_b32_e32 v101, v2
	v_mov_b32_e32 v106, v2
	v_mov_b32_e32 v107, v2
	v_mov_b32_e32 v108, v2
	v_mov_b32_e32 v109, v2
	v_mov_b32_e32 v114, v2
	v_mov_b32_e32 v115, v2
	v_mov_b32_e32 v116, v2
	v_mov_b32_e32 v117, v2
	v_mov_b32_e32 v78, v2
	v_mov_b32_e32 v79, v2
	v_mov_b32_e32 v80, v2
	v_mov_b32_e32 v81, v2
	v_mov_b32_e32 v86, v2
	v_mov_b32_e32 v87, v2
	v_mov_b32_e32 v88, v2
	v_mov_b32_e32 v89, v2
	v_mov_b32_e32 v94, v2
	v_mov_b32_e32 v95, v2
	v_mov_b32_e32 v96, v2
	v_mov_b32_e32 v97, v2
	v_mov_b32_e32 v102, v2
	v_mov_b32_e32 v103, v2
	v_mov_b32_e32 v104, v2
	v_mov_b32_e32 v105, v2
	v_mov_b32_e32 v110, v2
	v_mov_b32_e32 v111, v2
	v_mov_b32_e32 v112, v2
	v_mov_b32_e32 v113, v2
	v_mov_b32_e32 v118, v2
	v_mov_b32_e32 v119, v2
	v_mov_b32_e32 v120, v2
	v_mov_b32_e32 v121, v2
	v_mov_b32_e32 v122, v2
	v_mov_b32_e32 v123, v2
	v_mov_b32_e32 v124, v2
	v_mov_b32_e32 v125, v2
	v_mov_b32_e32 v126, v2
	v_mov_b32_e32 v127, v2
	v_mov_b32_e32 v128, v2
	v_mov_b32_e32 v129, v2
	s_cmp_lg_u32 s98, 0
	s_cselect_b32 s99, -2, 0x7ffffff0
	s_branch .LBB0_332

; #define PG8_STAGE(bufoff, gbase, voff) do { _Pragma("unroll") for (int _i = 0; _i < 2; ++_i) \
;         __builtin_amdgcn_global_load_lds((const unsigned*)((const char*)(gbase) + (voff)[_i]), (PG8_LAS unsigned*)(lds + (bufoff) + ldsw + _i * 8192), 16, 0, 0); } while (0)
; #define PG8_LDA(dst, b, h) do { _Pragma("unroll") for (int m = 0; m < 4; ++m) _Pragma("unroll") for (int k = 0; k < 2; ++k) dst[m][k] = *(const PG8_LAS bf16x8*)(lds + PG8_SA(b, h) + aoff + m * 2048 + k * 1024); } while (0)
; #define PG8_LDB(dst, b, h) do { _Pragma("unroll") for (int n = 0; n < 2; ++n) _Pragma("unroll") for (int k = 0; k < 2; ++k) dst[n][k] = *(const PG8_LAS bf16x8*)(lds + PG8_SB(b, h) + boff + n * 2048 + k * 1024); } while (0)
; #define PG8_MMA(ai, bj, At, Bt) do { __builtin_amdgcn_s_setprio(1); _Pragma("unroll") for (int m = 0; m < 4; ++m) _Pragma("unroll") for (int n = 0; n < 2; ++n) _Pragma("unroll") for (int k = 0; k < 2; ++k) \
;         acc[ai][bj][m][n] = __builtin_amdgcn_mfma_f32_16x16x32_bf16(Bt[n][k], At[m][k], acc[ai][bj][m][n], 0, 0, 0); __builtin_amdgcn_s_setprio(0); } while (0)
; #define PG8_WAIT_V(n) asm volatile("s_waitcnt vmcnt(" #n ")" ::: "memory")
; #define PG8_WAIT_L(n) asm volatile("s_waitcnt lgkmcnt(" #n ")" ::: "memory")
; #define PG8_BAR __builtin_amdgcn_s_barrier()
; #define PG8_SCHED __builtin_amdgcn_sched_barrier(0)
; #define PG8_STAGE(bufoff, gbase, voff) do { _Pragma("unroll") for (int _i = 0; _i < 2; ++_i) \
;         __builtin_amdgcn_global_load_lds((const unsigned*)((const char*)(gbase) + (voff)[_i]), (PG8_LAS unsigned*)(lds + (bufoff) + ldsw + _i * 8192), 16, 0, 0); } while (0)
; #define PG8_WAIT_V(n) asm volatile("s_waitcnt vmcnt(" #n ")" ::: "memory")
; #define PG8_BAR __builtin_amdgcn_s_barrier()
; template <class Epi, class Sched, bool ALIGN_EPI = false, bool SP2 = false>
; __device__ __forceinline__ void gemm_phase(PG8_LAS unsigned char* lds, const Gemm g, const Sched& S, const Epi& E) {
;     ...
;             if constexpr (SP2) {
;             PG8_LDB(B0, 0, 0); PG8_LDB(B1, 0, 1); PG8_SCHED; PG8_LDA(At, 0, 0); PG8_STAGE(PG8_SA(1, 1), a1 + hstep, voffA);
;             PG8_WAIT_V(8); PG8_WAIT_L(0); PG8_BAR; PG8_MMA(0, 0, At, B0); PG8_MMA(0, 1, At, B1); PG8_BAR; PG8_SCHED;
;             PG8_LDA(At, 0, 1); PG8_STAGE(PG8_SB(0, 0), b2, voffB); PG8_STAGE(PG8_SB(0, 1), b2 + hstep, voffB); PG8_STAGE(PG8_SA(0, 0), a2, voffA);
.LBB0_332:
	ds_read_b128 v[132:135], v213
	ds_read_b128 v[136:139], v213 offset:1024
	ds_read_b128 v[140:143], v213 offset:2048
	ds_read_b128 v[144:147], v213 offset:3072
	ds_read_b128 v[148:151], v214
	ds_read_b128 v[152:155], v214 offset:1024
	ds_read_b128 v[156:159], v214 offset:2048
	ds_read_b128 v[178:181], v214 offset:3072
	s_add_u32 s2, s0, 0xfff80080
	s_addc_u32 s3, s1, -1
	s_cmp_eq_u32 s95, 28
	s_cselect_b32 s5, s7, s3
	s_cselect_b32 s4, s33, s2
	s_cselect_b32 s3, s53, s85
	s_cselect_b32 s2, s55, s84
	v_lshl_add_u64 v[160:161], s[0:1], 0, v[172:173]
	s_add_i32 m0, s63, 0xc000
	ds_read_b128 v[182:185], v215
	ds_read_b128 v[188:191], v215 offset:1024
	ds_read_b128 v[192:195], v215 offset:2048
	ds_read_b128 v[196:199], v215 offset:3072
	ds_read_b128 v[200:203], v215 offset:4096
	ds_read_b128 v[204:207], v215 offset:5120
	ds_read_b128 v[218:221], v215 offset:6144
	ds_read_b128 v[222:225], v215 offset:7168
	global_load_lds_dwordx4 v[160:161], off
	v_lshl_add_u64 v[160:161], s[0:1], 0, v[174:175]
	s_add_i32 m0, s63, 0xe000
	s_nop 0
	global_load_lds_dwordx4 v[160:161], off
	s_cmp_eq_u32 s95, s99
	s_cbranch_scc1 .Lrx2_a
	s_waitcnt vmcnt(8)
.Lrx2_a_done:
	s_waitcnt lgkmcnt(0)
	s_barrier
	s_setprio 1
	s_waitcnt lgkmcnt(0)
	v_mfma_f32_16x16x32_bf16 v[126:129], v[132:135], v[182:185], v[126:129]
	v_mfma_f32_16x16x32_bf16 v[122:125], v[140:143], v[182:185], v[122:125]
	v_mfma_f32_16x16x32_bf16 v[118:121], v[132:135], v[192:195], v[118:121]
	v_mfma_f32_16x16x32_bf16 v[110:113], v[140:143], v[192:195], v[110:113]
	v_mfma_f32_16x16x32_bf16 v[102:105], v[132:135], v[200:203], v[102:105]
	v_mfma_f32_16x16x32_bf16 v[94:97], v[140:143], v[200:203], v[94:97]
	v_mfma_f32_16x16x32_bf16 v[86:89], v[132:135], v[218:221], v[86:89]
	v_mfma_f32_16x16x32_bf16 v[78:81], v[140:143], v[218:221], v[78:81]
	v_mfma_f32_16x16x32_bf16 v[126:129], v[136:139], v[188:191], v[126:129]
	v_mfma_f32_16x16x32_bf16 v[122:125], v[144:147], v[188:191], v[122:125]
	v_mfma_f32_16x16x32_bf16 v[118:121], v[136:139], v[196:199], v[118:121]
	v_mfma_f32_16x16x32_bf16 v[110:113], v[144:147], v[196:199], v[110:113]
	v_mfma_f32_16x16x32_bf16 v[102:105], v[136:139], v[204:207], v[102:105]
	v_mfma_f32_16x16x32_bf16 v[94:97], v[144:147], v[204:207], v[94:97]
	v_mfma_f32_16x16x32_bf16 v[86:89], v[136:139], v[222:225], v[86:89]
	v_mfma_f32_16x16x32_bf16 v[78:81], v[144:147], v[222:225], v[78:81]
	s_setprio 0
	s_setprio 1
	v_mfma_f32_16x16x32_bf16 v[114:117], v[148:151], v[182:185], v[114:117]
	v_mfma_f32_16x16x32_bf16 v[106:109], v[156:159], v[182:185], v[106:109]
	v_mfma_f32_16x16x32_bf16 v[98:101], v[148:151], v[192:195], v[98:101]
	v_mfma_f32_16x16x32_bf16 v[90:93], v[156:159], v[192:195], v[90:93]
	v_mfma_f32_16x16x32_bf16 v[82:85], v[148:151], v[200:203], v[82:85]
	v_mfma_f32_16x16x32_bf16 v[74:77], v[156:159], v[200:203], v[74:77]
	v_mfma_f32_16x16x32_bf16 v[70:73], v[148:151], v[218:221], v[70:73]
	v_mfma_f32_16x16x32_bf16 v[66:69], v[156:159], v[218:221], v[66:69]
	v_mfma_f32_16x16x32_bf16 v[114:117], v[152:155], v[188:191], v[114:117]
	v_mfma_f32_16x16x32_bf16 v[106:109], v[178:181], v[188:191], v[106:109]
	v_mfma_f32_16x16x32_bf16 v[98:101], v[152:155], v[196:199], v[98:101]
	v_mfma_f32_16x16x32_bf16 v[90:93], v[178:181], v[196:199], v[90:93]
	v_mfma_f32_16x16x32_bf16 v[82:85], v[152:155], v[204:207], v[82:85]
	v_mfma_f32_16x16x32_bf16 v[74:77], v[178:181], v[204:207], v[74:77]
	v_mfma_f32_16x16x32_bf16 v[70:73], v[152:155], v[222:225], v[70:73]
	v_mfma_f32_16x16x32_bf16 v[66:69], v[178:181], v[222:225], v[66:69]
	s_setprio 0
	s_barrier
	s_add_i32 s96, s81, s66
	v_lshl_add_u64 v[160:161], s[2:3], 0, v[164:165]
	s_mov_b32 m0, s96
	ds_read_b128 v[182:185], v215 offset:16384
	ds_read_b128 v[188:191], v215 offset:17408
	ds_read_b128 v[192:195], v215 offset:18432
	ds_read_b128 v[196:199], v215 offset:19456
	ds_read_b128 v[200:203], v215 offset:20480
	ds_read_b128 v[204:207], v215 offset:21504
	ds_read_b128 v[218:221], v215 offset:22528
	ds_read_b128 v[222:225], v215 offset:23552
	global_load_lds_dwordx4 v[160:161], off
	s_add_i32 m0, s96, 0x2000
	s_add_u32 s96, s2, 0x80000
	v_lshl_add_u64 v[208:209], s[2:3], 0, v[168:169]
	s_addc_u32 s97, s3, 0
	s_add_i32 vcc_lo, s82, s66
	global_load_lds_dwordx4 v[208:209], off
	v_lshl_add_u64 v[226:227], s[96:97], 0, v[164:165]
	s_mov_b32 m0, vcc_lo
	v_lshl_add_u64 v[228:229], s[4:5], 0, v[166:167]
	global_load_lds_dwordx4 v[226:227], off
	v_lshl_add_u64 v[226:227], s[96:97], 0, v[168:169]
	s_add_i32 m0, vcc_lo, 0x2000
	s_nop 0
	global_load_lds_dwordx4 v[226:227], off
	v_lshl_add_u64 v[226:227], s[4:5], 0, v[162:163]
	s_mov_b32 m0, s63
	s_nop 0
	global_load_lds_dwordx4 v[226:227], off
	s_mov_b32 m0, s65
	s_nop 0
	global_load_lds_dwordx4 v[228:229], off
	s_cmp_eq_u32 s95, s99
	s_cbranch_scc1 .Lrx2_b
	s_waitcnt vmcnt(8)
; #define PG8_STAGE(bufoff, gbase, voff) do { _Pragma("unroll") for (int _i = 0; _i < 2; ++_i) \
;         __builtin_amdgcn_global_load_lds((const unsigned*)((const char*)(gbase) + (voff)[_i]), (PG8_LAS unsigned*)(lds + (bufoff) + ldsw + _i * 8192), 16, 0, 0); } while (0)
; #define PG8_LDA(dst, b, h) do { _Pragma("unroll") for (int m = 0; m < 4; ++m) _Pragma("unroll") for (int k = 0; k < 2; ++k) dst[m][k] = *(const PG8_LAS bf16x8*)(lds + PG8_SA(b, h) + aoff + m * 2048 + k * 1024); } while (0)
; #define PG8_LDB(dst, b, h) do { _Pragma("unroll") for (int n = 0; n < 2; ++n) _Pragma("unroll") for (int k = 0; k < 2; ++k) dst[n][k] = *(const PG8_LAS bf16x8*)(lds + PG8_SB(b, h) + boff + n * 2048 + k * 1024); } while (0)
; #define PG8_MMA(ai, bj, At, Bt) do { __builtin_amdgcn_s_setprio(1); _Pragma("unroll") for (int m = 0; m < 4; ++m) _Pragma("unroll") for (int n = 0; n < 2; ++n) _Pragma("unroll") for (int k = 0; k < 2; ++k) \
;         acc[ai][bj][m][n] = __builtin_amdgcn_mfma_f32_16x16x32_bf16(Bt[n][k], At[m][k], acc[ai][bj][m][n], 0, 0, 0); __builtin_amdgcn_s_setprio(0); } while (0)
; #define PG8_WAIT_V(n) asm volatile("s_waitcnt vmcnt(" #n ")" ::: "memory")
; #define PG8_WAIT_L(n) asm volatile("s_waitcnt lgkmcnt(" #n ")" ::: "memory")
; #define PG8_BAR __builtin_amdgcn_s_barrier()
; #define PG8_SCHED __builtin_amdgcn_sched_barrier(0)
; #define PG8_STAGE(bufoff, gbase, voff) do { _Pragma("unroll") for (int _i = 0; _i < 2; ++_i) \
;         __builtin_amdgcn_global_load_lds((const unsigned*)((const char*)(gbase) + (voff)[_i]), (PG8_LAS unsigned*)(lds + (bufoff) + ldsw + _i * 8192), 16, 0, 0); } while (0)
; #define PG8_WAIT_V(n) asm volatile("s_waitcnt vmcnt(" #n ")" ::: "memory")
; #define PG8_WAIT_L(n) asm volatile("s_waitcnt lgkmcnt(" #n ")" ::: "memory")
; #define PG8_BAR __builtin_amdgcn_s_barrier()
; template <class Epi, class Sched, bool ALIGN_EPI = false, bool SP2 = false>
; __device__ __forceinline__ void gemm_phase(PG8_LAS unsigned char* lds, const Gemm g, const Sched& S, const Epi& E) {
;     ...
;             PG8_WAIT_V(8); PG8_WAIT_L(0); PG8_BAR; PG8_MMA(1, 0, At, B0); PG8_MMA(1, 1, At, B1); PG8_BAR; PG8_SCHED;
;             PG8_LDB(B0, 1, 0); PG8_LDB(B1, 1, 1); PG8_SCHED; PG8_LDA(At, 1, 0); PG8_STAGE(PG8_SA(0, 1), a2 + hstep, voffA);
;             PG8_WAIT_V(8); PG8_WAIT_L(0); PG8_BAR; PG8_MMA(0, 0, At, B0); PG8_MMA(0, 1, At, B1); PG8_BAR; PG8_SCHED;
.Lrx2_b_done:
	s_waitcnt lgkmcnt(0)
	s_barrier
	s_setprio 1
	s_waitcnt lgkmcnt(0)
	v_mfma_f32_16x16x32_bf16 v[62:65], v[132:135], v[182:185], v[62:65]
	v_mfma_f32_16x16x32_bf16 v[58:61], v[140:143], v[182:185], v[58:61]
	v_mfma_f32_16x16x32_bf16 v[54:57], v[132:135], v[192:195], v[54:57]
	v_mfma_f32_16x16x32_bf16 v[46:49], v[140:143], v[192:195], v[46:49]
	v_mfma_f32_16x16x32_bf16 v[38:41], v[132:135], v[200:203], v[38:41]
	v_mfma_f32_16x16x32_bf16 v[30:33], v[140:143], v[200:203], v[30:33]
	v_mfma_f32_16x16x32_bf16 v[22:25], v[132:135], v[218:221], v[22:25]
	v_mfma_f32_16x16x32_bf16 v[14:17], v[140:143], v[218:221], v[14:17]
	v_mfma_f32_16x16x32_bf16 v[62:65], v[136:139], v[188:191], v[62:65]
	v_mfma_f32_16x16x32_bf16 v[58:61], v[144:147], v[188:191], v[58:61]
	v_mfma_f32_16x16x32_bf16 v[54:57], v[136:139], v[196:199], v[54:57]
	v_mfma_f32_16x16x32_bf16 v[46:49], v[144:147], v[196:199], v[46:49]
	v_mfma_f32_16x16x32_bf16 v[38:41], v[136:139], v[204:207], v[38:41]
	v_mfma_f32_16x16x32_bf16 v[30:33], v[144:147], v[204:207], v[30:33]
	v_mfma_f32_16x16x32_bf16 v[22:25], v[136:139], v[222:225], v[22:25]
	v_mfma_f32_16x16x32_bf16 v[14:17], v[144:147], v[222:225], v[14:17]
	s_setprio 0
	s_setprio 1
	v_mfma_f32_16x16x32_bf16 v[50:53], v[148:151], v[182:185], v[50:53]
	v_mfma_f32_16x16x32_bf16 v[42:45], v[156:159], v[182:185], v[42:45]
	v_mfma_f32_16x16x32_bf16 v[34:37], v[148:151], v[192:195], v[34:37]
	v_mfma_f32_16x16x32_bf16 v[26:29], v[156:159], v[192:195], v[26:29]
	v_mfma_f32_16x16x32_bf16 v[18:21], v[148:151], v[200:203], v[18:21]
	v_mfma_f32_16x16x32_bf16 v[10:13], v[156:159], v[200:203], v[10:13]
	v_mfma_f32_16x16x32_bf16 v[6:9], v[148:151], v[218:221], v[6:9]
	v_mfma_f32_16x16x32_bf16 v[2:5], v[156:159], v[218:221], v[2:5]
	v_mfma_f32_16x16x32_bf16 v[50:53], v[152:155], v[188:191], v[50:53]
	v_mfma_f32_16x16x32_bf16 v[42:45], v[178:181], v[188:191], v[42:45]
	v_mfma_f32_16x16x32_bf16 v[34:37], v[152:155], v[196:199], v[34:37]
	v_mfma_f32_16x16x32_bf16 v[26:29], v[178:181], v[196:199], v[26:29]
	v_mfma_f32_16x16x32_bf16 v[18:21], v[152:155], v[204:207], v[18:21]
	v_mfma_f32_16x16x32_bf16 v[10:13], v[178:181], v[204:207], v[10:13]
	v_mfma_f32_16x16x32_bf16 v[6:9], v[152:155], v[222:225], v[6:9]
	v_mfma_f32_16x16x32_bf16 v[2:5], v[178:181], v[222:225], v[2:5]
	s_setprio 0
	s_barrier
	s_add_i32 s96, 0, 0x18000
	v_add_u32_e32 v131, s96, v211
	s_add_i32 s97, 0, 0x1c000
	ds_read_b128 v[132:135], v131
	ds_read_b128 v[136:139], v131 offset:1024
	ds_read_b128 v[140:143], v131 offset:2048
	ds_read_b128 v[144:147], v131 offset:3072
	v_add_u32_e32 v131, s97, v211
	ds_read_b128 v[148:151], v131
	ds_read_b128 v[152:155], v131 offset:1024
	ds_read_b128 v[156:159], v131 offset:2048
	ds_read_b128 v[178:181], v131 offset:3072
	s_add_u32 s4, s4, 0x80000
	s_addc_u32 s5, s5, 0
	s_mov_b32 m0, s71
	v_lshl_add_u64 v[230:231], s[4:5], 0, v[162:163]
	ds_read_b128 v[182:185], v215 offset:32768
	ds_read_b128 v[188:191], v215 offset:33792
	ds_read_b128 v[192:195], v215 offset:34816
	ds_read_b128 v[196:199], v215 offset:35840
	ds_read_b128 v[200:203], v215 offset:36864
	ds_read_b128 v[204:207], v215 offset:37888
	ds_read_b128 v[218:221], v215 offset:38912
	ds_read_b128 v[222:225], v215 offset:39936
	global_load_lds_dwordx4 v[230:231], off
	v_lshl_add_u64 v[230:231], s[4:5], 0, v[166:167]
	s_mov_b32 m0, s72
	s_nop 0
	global_load_lds_dwordx4 v[230:231], off
	s_waitcnt vmcnt(8)
	s_waitcnt lgkmcnt(0)
	s_barrier
	s_setprio 1
	s_waitcnt lgkmcnt(0)
	v_mfma_f32_16x16x32_bf16 v[126:129], v[132:135], v[182:185], v[126:129]
	v_mfma_f32_16x16x32_bf16 v[122:125], v[140:143], v[182:185], v[122:125]
	v_mfma_f32_16x16x32_bf16 v[118:121], v[132:135], v[192:195], v[118:121]
	v_mfma_f32_16x16x32_bf16 v[110:113], v[140:143], v[192:195], v[110:113]
	v_mfma_f32_16x16x32_bf16 v[102:105], v[132:135], v[200:203], v[102:105]
	v_mfma_f32_16x16x32_bf16 v[94:97], v[140:143], v[200:203], v[94:97]
	v_mfma_f32_16x16x32_bf16 v[86:89], v[132:135], v[218:221], v[86:89]
	v_mfma_f32_16x16x32_bf16 v[78:81], v[140:143], v[218:221], v[78:81]
	v_mfma_f32_16x16x32_bf16 v[126:129], v[136:139], v[188:191], v[126:129]
	v_mfma_f32_16x16x32_bf16 v[122:125], v[144:147], v[188:191], v[122:125]
	v_mfma_f32_16x16x32_bf16 v[118:121], v[136:139], v[196:199], v[118:121]
	v_mfma_f32_16x16x32_bf16 v[110:113], v[144:147], v[196:199], v[110:113]
	v_mfma_f32_16x16x32_bf16 v[102:105], v[136:139], v[204:207], v[102:105]
	v_mfma_f32_16x16x32_bf16 v[94:97], v[144:147], v[204:207], v[94:97]
	v_mfma_f32_16x16x32_bf16 v[86:89], v[136:139], v[222:225], v[86:89]
	v_mfma_f32_16x16x32_bf16 v[78:81], v[144:147], v[222:225], v[78:81]
	s_setprio 0
	s_setprio 1
	v_mfma_f32_16x16x32_bf16 v[114:117], v[148:151], v[182:185], v[114:117]
	v_mfma_f32_16x16x32_bf16 v[106:109], v[156:159], v[182:185], v[106:109]
	v_mfma_f32_16x16x32_bf16 v[98:101], v[148:151], v[192:195], v[98:101]
	v_mfma_f32_16x16x32_bf16 v[90:93], v[156:159], v[192:195], v[90:93]
	v_mfma_f32_16x16x32_bf16 v[82:85], v[148:151], v[200:203], v[82:85]
	v_mfma_f32_16x16x32_bf16 v[74:77], v[156:159], v[200:203], v[74:77]
	v_mfma_f32_16x16x32_bf16 v[70:73], v[148:151], v[218:221], v[70:73]
	v_mfma_f32_16x16x32_bf16 v[66:69], v[156:159], v[218:221], v[66:69]
	v_mfma_f32_16x16x32_bf16 v[114:117], v[152:155], v[188:191], v[114:117]
	v_mfma_f32_16x16x32_bf16 v[106:109], v[178:181], v[188:191], v[106:109]
	v_mfma_f32_16x16x32_bf16 v[98:101], v[152:155], v[196:199], v[98:101]
	v_mfma_f32_16x16x32_bf16 v[90:93], v[178:181], v[196:199], v[90:93]
	v_mfma_f32_16x16x32_bf16 v[82:85], v[152:155], v[204:207], v[82:85]
	v_mfma_f32_16x16x32_bf16 v[74:77], v[178:181], v[204:207], v[74:77]
	v_mfma_f32_16x16x32_bf16 v[70:73], v[152:155], v[222:225], v[70:73]
	v_mfma_f32_16x16x32_bf16 v[66:69], v[178:181], v[222:225], v[66:69]
	s_setprio 0
	s_barrier
; #define PG8_STAGE(bufoff, gbase, voff) do { _Pragma("unroll") for (int _i = 0; _i < 2; ++_i) \
;         __builtin_amdgcn_global_load_lds((const unsigned*)((const char*)(gbase) + (voff)[_i]), (PG8_LAS unsigned*)(lds + (bufoff) + ldsw + _i * 8192), 16, 0, 0); } while (0)
; #define PG8_LDA(dst, b, h) do { _Pragma("unroll") for (int m = 0; m < 4; ++m) _Pragma("unroll") for (int k = 0; k < 2; ++k) dst[m][k] = *(const PG8_LAS bf16x8*)(lds + PG8_SA(b, h) + aoff + m * 2048 + k * 1024); } while (0)
; #define PG8_MMA(ai, bj, At, Bt) do { __builtin_amdgcn_s_setprio(1); _Pragma("unroll") for (int m = 0; m < 4; ++m) _Pragma("unroll") for (int n = 0; n < 2; ++n) _Pragma("unroll") for (int k = 0; k < 2; ++k) \
;         acc[ai][bj][m][n] = __builtin_amdgcn_mfma_f32_16x16x32_bf16(Bt[n][k], At[m][k], acc[ai][bj][m][n], 0, 0, 0); __builtin_amdgcn_s_setprio(0); } while (0)
; #define PG8_WAIT_V(n) asm volatile("s_waitcnt vmcnt(" #n ")" ::: "memory")
; #define PG8_WAIT_L(n) asm volatile("s_waitcnt lgkmcnt(" #n ")" ::: "memory")
; #define PG8_BAR __builtin_amdgcn_s_barrier()
; #define PG8_SCHED __builtin_amdgcn_sched_barrier(0)
; #define PG8_STAGE(bufoff, gbase, voff) do { _Pragma("unroll") for (int _i = 0; _i < 2; ++_i) \
;         __builtin_amdgcn_global_load_lds((const unsigned*)((const char*)(gbase) + (voff)[_i]), (PG8_LAS unsigned*)(lds + (bufoff) + ldsw + _i * 8192), 16, 0, 0); } while (0)
; #define PG8_LDA(dst, b, h) do { _Pragma("unroll") for (int m = 0; m < 4; ++m) _Pragma("unroll") for (int k = 0; k < 2; ++k) dst[m][k] = *(const PG8_LAS bf16x8*)(lds + PG8_SA(b, h) + aoff + m * 2048 + k * 1024); } while (0)
; #define PG8_WAIT_V(n) asm volatile("s_waitcnt vmcnt(" #n ")" ::: "memory")
; template <class Epi, class Sched, bool ALIGN_EPI = false, bool SP2 = false>
; __device__ __forceinline__ void gemm_phase(PG8_LAS unsigned char* lds, const Gemm g, const Sched& S, const Epi& E) {
;     ...
;             PG8_LDA(At, 1, 1); PG8_STAGE(PG8_SB(1, 0), b3, voffB); PG8_STAGE(PG8_SB(1, 1), b3 + hstep, voffB); PG8_STAGE(PG8_SA(1, 0), a3, voffA);
;             PG8_WAIT_V(8); PG8_WAIT_L(0); PG8_BAR; PG8_MMA(1, 0, At, B0); PG8_MMA(1, 1, At, B1); PG8_BAR; PG8_SCHED;
;     ...
;         if constexpr (Sched::DYNAMIC) { static_assert(!Sched::DYNAMIC || ALIGN_EPI, "dynamic orders publish in front of the ALIGN_EPI barrier"); S.claim_publish(ui + 2, pend, wid, lane); }
	s_add_i32 s4, s96, s66
	v_lshl_add_u64 v[160:161], v[160:161], 0, s[40:41]
	s_mov_b32 m0, s4
	ds_read_b128 v[182:185], v215 offset:49152
	ds_read_b128 v[188:191], v215 offset:50176
	ds_read_b128 v[192:195], v215 offset:51200
	ds_read_b128 v[196:199], v215 offset:52224
	ds_read_b128 v[200:203], v215 offset:53248
	ds_read_b128 v[204:207], v215 offset:54272
	ds_read_b128 v[218:221], v215 offset:55296
	ds_read_b128 v[222:225], v215 offset:56320
	global_load_lds_dwordx4 v[160:161], off
	s_add_i32 m0, s4, 0x2000
	s_add_u32 s2, s2, 0x80080
	v_lshl_add_u64 v[160:161], v[208:209], 0, s[40:41]
	s_addc_u32 s3, s3, 0
	s_add_i32 s4, s97, s66
	global_load_lds_dwordx4 v[160:161], off
	v_lshl_add_u64 v[160:161], s[2:3], 0, v[164:165]
	s_mov_b32 m0, s4
	s_nop 0
	global_load_lds_dwordx4 v[160:161], off
	v_lshl_add_u64 v[160:161], s[2:3], 0, v[168:169]
	s_add_i32 m0, s4, 0x2000
	s_nop 0
	global_load_lds_dwordx4 v[160:161], off
	v_lshl_add_u64 v[160:161], v[226:227], 0, s[40:41]
	s_mov_b32 m0, s74
	s_nop 0
	global_load_lds_dwordx4 v[160:161], off
	v_lshl_add_u64 v[160:161], v[228:229], 0, s[40:41]
	s_mov_b32 m0, s75
	s_nop 0
	global_load_lds_dwordx4 v[160:161], off
	s_waitcnt vmcnt(8)
	s_waitcnt lgkmcnt(0)
	s_barrier
	s_setprio 1
	s_waitcnt lgkmcnt(0)
	v_mfma_f32_16x16x32_bf16 v[62:65], v[132:135], v[182:185], v[62:65]
	v_mfma_f32_16x16x32_bf16 v[58:61], v[140:143], v[182:185], v[58:61]
	v_mfma_f32_16x16x32_bf16 v[54:57], v[132:135], v[192:195], v[54:57]
	v_mfma_f32_16x16x32_bf16 v[46:49], v[140:143], v[192:195], v[46:49]
	v_mfma_f32_16x16x32_bf16 v[38:41], v[132:135], v[200:203], v[38:41]
	v_mfma_f32_16x16x32_bf16 v[30:33], v[140:143], v[200:203], v[30:33]
	v_mfma_f32_16x16x32_bf16 v[22:25], v[132:135], v[218:221], v[22:25]
	v_mfma_f32_16x16x32_bf16 v[14:17], v[140:143], v[218:221], v[14:17]
	v_mfma_f32_16x16x32_bf16 v[62:65], v[136:139], v[188:191], v[62:65]
	v_mfma_f32_16x16x32_bf16 v[58:61], v[144:147], v[188:191], v[58:61]
	v_mfma_f32_16x16x32_bf16 v[54:57], v[136:139], v[196:199], v[54:57]
	v_mfma_f32_16x16x32_bf16 v[46:49], v[144:147], v[196:199], v[46:49]
	v_mfma_f32_16x16x32_bf16 v[38:41], v[136:139], v[204:207], v[38:41]
	v_mfma_f32_16x16x32_bf16 v[30:33], v[144:147], v[204:207], v[30:33]
	v_mfma_f32_16x16x32_bf16 v[22:25], v[136:139], v[222:225], v[22:25]
	v_mfma_f32_16x16x32_bf16 v[14:17], v[144:147], v[222:225], v[14:17]
	s_setprio 0
	s_setprio 1
	v_mfma_f32_16x16x32_bf16 v[50:53], v[148:151], v[182:185], v[50:53]
	v_mfma_f32_16x16x32_bf16 v[42:45], v[156:159], v[182:185], v[42:45]
	v_mfma_f32_16x16x32_bf16 v[34:37], v[148:151], v[192:195], v[34:37]
	v_mfma_f32_16x16x32_bf16 v[26:29], v[156:159], v[192:195], v[26:29]
	v_mfma_f32_16x16x32_bf16 v[18:21], v[148:151], v[200:203], v[18:21]
	v_mfma_f32_16x16x32_bf16 v[10:13], v[156:159], v[200:203], v[10:13]
	v_mfma_f32_16x16x32_bf16 v[6:9], v[148:151], v[218:221], v[6:9]
	v_mfma_f32_16x16x32_bf16 v[2:5], v[156:159], v[218:221], v[2:5]
	v_mfma_f32_16x16x32_bf16 v[50:53], v[152:155], v[188:191], v[50:53]
	v_mfma_f32_16x16x32_bf16 v[42:45], v[178:181], v[188:191], v[42:45]
	v_mfma_f32_16x16x32_bf16 v[34:37], v[152:155], v[196:199], v[34:37]
	v_mfma_f32_16x16x32_bf16 v[26:29], v[178:181], v[196:199], v[26:29]
	v_mfma_f32_16x16x32_bf16 v[18:21], v[152:155], v[204:207], v[18:21]
	v_mfma_f32_16x16x32_bf16 v[10:13], v[178:181], v[204:207], v[10:13]
	v_mfma_f32_16x16x32_bf16 v[6:9], v[152:155], v[222:225], v[6:9]
	v_mfma_f32_16x16x32_bf16 v[2:5], v[178:181], v[222:225], v[2:5]
	s_setprio 0
	s_barrier
	s_add_i32 s95, s95, 2
	s_add_u32 s0, s0, 0x100
	s_addc_u32 s1, s1, 0
	s_add_u32 s84, s84, 0x100
	s_addc_u32 s85, s85, 0
	s_cmp_gt_u32 s95, 29
	s_cbranch_scc0 .LBB0_332
	s_waitcnt vmcnt(8)
	v_readfirstlane_b32 s2, v130
	s_and_saveexec_b64 s[0:1], s[10:11]
	s_cbranch_execz .LBB0_335
	s_and_b32 s3, s6, 3
	s_xor_b32 s3, s3, 2
	s_and_b64 s[4:5], s[42:43], exec
	s_cselect_b32 s3, s3, s76
	s_lshl_b32 s3, s3, 2
	s_add_i32 s3, s3, 0
	s_add_i32 s3, s3, 0x27da0
	v_mov_b32_e32 v130, s3
	v_mov_b32_e32 v131, s2
	ds_write_b32 v130, v131

; __device__ __forceinline__ float softplusf(float x) { return x > 20.f ? x : log1pf(expf(x)); }
;     __device__ __forceinline__ void operator()(const f32x4 (&acc)[2][2][4][2], const pg8::Unit& u, int wr, int wc, int fr, int fq_in) const {
;         int fq = fq_in; asm volatile("" : "+v"(fq));
;         const int row0 = u.pm * 256 + wr * 64 + fr; const int pn = u.pn;
;         if (pn < 12) {
;     ...
;         } else {
;             if (wc < 2) {
;                 const int col0 = wc * 32 + 8 * fq; const f32x4 b0 = *(const f32x4*)(dtb + col0), b1 = *(const f32x4*)(dtb + col0 + 4);
; #pragma unroll
;                 for (int ai = 0; ai < 2; ++ai)
; #pragma unroll
;                     for (int m = 0; m < 4; ++m) { float* rowp = DTS + (size_t)(row0 + ai * 128 + m * 16) * 64 + col0; f32x4 o0, o1;
; #pragma unroll
;                         for (int q = 0; q < 4; ++q) { o0[q] = softplusf(acc[ai][0][m][0][q] + b0[q]); o1[q] = softplusf(acc[ai][0][m][1][q] + b1[q]); }
.LBB0_337:
	s_mov_b32 s98, 0
	v_mov_b32_e32 v148, v1
	v_lshl_add_u32 v178, s62, 8, v210
	s_cmp_gt_i32 s64, 11
	s_mov_b64 s[0:1], -1
	s_cbranch_scc0 .LBB0_477
	s_cmp_gt_u32 s64, 43
	s_cbranch_scc0 .LBB0_474
	s_cmp_gt_u32 s64, 59
	s_cbranch_scc0 .LBB0_471
	s_andn2_b64 vcc, exec, s[46:47]
	s_cbranch_vccnz .LBB0_470
	v_lshl_add_u32 v146, v148, 3, s73
	v_ashrrev_i32_e32 v147, 31, v146
	v_lshl_add_u64 v[130:131], v[146:147], 2, s[22:23]
	global_load_dwordx4 v[134:137], v[130:131], off
	s_nop 0
	global_load_dwordx4 v[130:133], v[130:131], off offset:16
	s_waitcnt vmcnt(1)
	v_add_f32_e32 v138, v126, v134
	v_cmp_nlt_f32_e32 vcc, s83, v138
	s_and_saveexec_b64 s[0:1], vcc
	s_cbranch_execz .LBB0_343
	v_mul_f32_e32 v139, 0x3fb8aa3b, v138
	v_rndne_f32_e32 v140, v139
	v_sub_f32_e32 v141, v139, v140
	v_fma_f32 v139, v138, s86, -v139
	v_fmac_f32_e32 v139, 0x32a5705f, v138
	v_add_f32_e32 v139, v141, v139
	v_cvt_i32_f32_e32 v140, v140
	v_exp_f32_e32 v139, v139
	v_cmp_ngt_f32_e32 vcc, s87, v138
	v_ldexp_f32 v139, v139, v140
	s_nop 0
	v_cndmask_b32_e32 v139, 0, v139, vcc
	v_cmp_nlt_f32_e32 vcc, s88, v138
	s_nop 1
	v_cndmask_b32_e32 v149, v217, v139, vcc
	v_add_f32_e32 v140, 1.0, v149
	v_add_f32_e32 v138, -1.0, v140
	v_sub_f32_e32 v139, v138, v140
	v_add_f32_e32 v139, 1.0, v139
	v_sub_f32_e32 v138, v149, v138
	v_add_f32_e32 v141, v138, v139
	v_frexp_mant_f32_e32 v142, v140
	v_cvt_f64_f32_e32 v[138:139], v140
	v_frexp_exp_i32_f64_e32 v138, v[138:139]
	v_cmp_gt_f32_e32 vcc, s90, v142
	s_nop 1
	v_subbrev_co_u32_e32 v150, vcc, 0, v138, vcc
	v_sub_u32_e32 v138, 0, v150
	v_ldexp_f32 v139, v140, v138
	v_add_f32_e32 v140, -1.0, v139
	v_add_f32_e32 v142, 1.0, v139
	v_ldexp_f32 v138, v141, v138
	v_add_f32_e32 v141, 1.0, v140
	v_add_f32_e32 v143, -1.0, v142
	v_sub_f32_e32 v141, v139, v141
	v_sub_f32_e32 v139, v139, v143
	v_add_f32_e32 v141, v138, v141
	v_add_f32_e32 v138, v138, v139
	v_add_f32_e32 v151, v142, v138
	v_rcp_f32_e32 v153, v151
	v_sub_f32_e32 v139, v142, v151
	v_add_f32_e32 v152, v138, v139
	v_add_f32_e32 v139, v140, v141
	v_mul_f32_e32 v155, v139, v153
	v_sub_f32_e32 v138, v140, v139
	v_mul_f32_e32 v140, v151, v155
	v_fma_f32 v142, v155, v151, -v140
	v_fmac_f32_e32 v142, v155, v152
	v_add_f32_e32 v154, v141, v138
	v_add_f32_e32 v138, v140, v142
	v_sub_f32_e32 v141, v139, v138
	v_pk_add_f32 v[144:145], v[138:139], v[140:141] neg_lo:[0,1] neg_hi:[0,1]
	v_mov_b32_e32 v143, v138
	v_pk_add_f32 v[138:139], v[144:145], v[142:143] neg_lo:[0,1] neg_hi:[0,1]
	v_cmp_neq_f32_e32 vcc, s89, v149
	v_add_f32_e32 v139, v154, v139
	v_add_f32_e32 v138, v138, v139
	v_add_f32_e32 v139, v141, v138
	v_mul_f32_e32 v154, v153, v139
	v_mul_f32_e32 v140, v151, v154
	v_fma_f32 v142, v154, v151, -v140
	v_fmac_f32_e32 v142, v154, v152
	v_sub_f32_e32 v141, v141, v139
	v_add_f32_e32 v151, v138, v141
	v_add_f32_e32 v138, v140, v142
	v_sub_f32_e32 v141, v139, v138
	v_pk_add_f32 v[144:145], v[138:139], v[140:141] neg_lo:[0,1] neg_hi:[0,1]
	v_mov_b32_e32 v143, v138
	v_pk_add_f32 v[138:139], v[144:145], v[142:143] neg_lo:[0,1] neg_hi:[0,1]
	s_nop 0
	v_add_f32_e32 v139, v151, v139
	v_add_f32_e32 v138, v138, v139
	v_add_f32_e32 v139, v155, v154
	v_add_f32_e32 v138, v141, v138
	v_sub_f32_e32 v140, v139, v155
	v_mul_f32_e32 v138, v153, v138
	v_sub_f32_e32 v140, v154, v140
	v_add_f32_e32 v140, v140, v138
	v_add_f32_e32 v142, v139, v140
	v_mul_f32_e32 v143, v142, v142
	v_fmamk_f32 v138, v143, 0x3e9b6dac, v216
	v_fmaak_f32 v177, v143, v138, 0x3f2aaada
	v_cvt_f32_i32_e32 v138, v150
	v_sub_f32_e32 v139, v142, v139
	v_sub_f32_e32 v139, v140, v139
	v_ldexp_f32 v144, v139, 1
	v_mul_f32_e32 v139, v142, v143
	v_ldexp_f32 v141, v142, 1
	v_pk_mul_f32 v[142:143], v[138:139], v[176:177]
	s_nop 0
	v_fma_f32 v140, v138, s91, -v142
	v_fmac_f32_e32 v140, 0xb102e308, v138
	v_pk_add_f32 v[138:139], v[142:143], v[140:141]
	s_nop 0
	v_sub_f32_e32 v141, v139, v141
	v_sub_f32_e32 v141, v143, v141
	v_add_f32_e32 v145, v144, v141
	v_mov_b32_e32 v144, v142
	v_pk_add_f32 v[142:143], v[138:139], v[142:143] neg_lo:[0,1] neg_hi:[0,1]
	v_pk_add_f32 v[150:151], v[138:139], v[144:145]
	v_mov_b32_e32 v141, v138
	v_mov_b32_e32 v143, v151
	v_pk_add_f32 v[152:153], v[140:141], v[142:143] neg_lo:[0,1] neg_hi:[0,1]
	v_pk_add_f32 v[140:141], v[140:141], v[142:143]
	v_mov_b32_e32 v144, v145
	v_pk_add_f32 v[142:143], v[140:141], v[138:139] op_sel:[1,0] op_sel_hi:[0,1] neg_lo:[0,1] neg_hi:[0,1]
	v_pk_add_f32 v[154:155], v[150:151], v[142:143] op_sel_hi:[1,0] neg_lo:[0,1] neg_hi:[0,1]
	v_mov_b32_e32 v150, v151
	v_mov_b32_e32 v151, v141
	v_pk_mov_b32 v[142:143], v[138:139], v[142:143] op_sel:[1,0]
	v_mov_b32_e32 v145, v138
	v_pk_add_f32 v[142:143], v[150:151], v[142:143] neg_lo:[0,1] neg_hi:[0,1]
	v_mov_b32_e32 v154, v152
	v_pk_add_f32 v[138:139], v[144:145], v[142:143] neg_lo:[0,1] neg_hi:[0,1]
	v_mov_b32_e32 v153, v141
	v_pk_add_f32 v[142:143], v[154:155], v[138:139]
	s_nop 0
	v_pk_add_f32 v[144:145], v[142:143], v[142:143] op_sel:[0,1] op_sel_hi:[1,0]
	s_nop 0
	v_pk_add_f32 v[140:141], v[140:141], v[144:145] op_sel:[1,0] op_sel_hi:[0,1]
	v_mov_b32_e32 v143, v140
	v_pk_add_f32 v[150:151], v[142:143], v[152:153] neg_lo:[0,1] neg_hi:[0,1]
	v_mov_b32_e32 v139, v144
	v_sub_f32_e32 v141, v142, v150
	v_pk_add_f32 v[138:139], v[138:139], v[150:151] neg_lo:[0,1] neg_hi:[0,1]
	v_sub_f32_e32 v141, v152, v141
	v_add_f32_e32 v138, v138, v141
	v_add_f32_e32 v138, v138, v139
	v_add_f32_e32 v138, v140, v138
	v_cndmask_b32_e32 v138, v217, v138, vcc
	v_cmp_lt_f32_e64 vcc, |v149|, s92
	s_nop 1
	v_cndmask_b32_e32 v138, v138, v149, vcc

; __device__ __forceinline__ unsigned cvt_pk_bf16(float lo, float hi) { unsigned r; asm volatile("v_cvt_pk_bf16_f32 %0, %1, %2" : "=v"(r) : "v"(lo), "v"(hi)); return r; }
;     __device__ __forceinline__ void operator()(const f32x4 (&acc)[2][2][4][2], const pg8::Unit& u, int wr, int wc, int fr, int fq_in) const {
;     ...
;         } else if (pn < 60) {
;             const int col0 = (pn - 44) * 256 + wc * 32 + 8 * fq;
; #pragma unroll
;             for (int ai = 0; ai < 2; ++ai)
; #pragma unroll
;                 for (int m = 0; m < 4; ++m) { bf16* rowp = Gt + (size_t)(row0 + ai * 128 + m * 16) * (2 * D) + col0;
; #pragma unroll
;                     for (int bj = 0; bj < 2; ++bj) { const f32x4 v0 = acc[ai][bj][m][0], v1 = acc[ai][bj][m][1];
;                         u32x4 w; w.x = pg8::cvt_pk_bf16(v0[0], v0[1]); w.y = pg8::cvt_pk_bf16(v0[2], v0[3]); w.z = pg8::cvt_pk_bf16(v1[0], v1[1]); w.w = pg8::cvt_pk_bf16(v1[2], v1[3]);
;                         *(u32x4*)(rowp + bj * 128) = w; } }
.LBB0_471:
	s_andn2_b64 vcc, exec, s[0:1]
	s_cbranch_vccnz .LBB0_473
	s_lshl_b32 s0, s64, 8
	s_add_i32 s0, s77, s0
	v_lshl_add_u32 v130, v148, 3, s0
	v_ashrrev_i32_e32 v179, 31, v178
	v_ashrrev_i32_e32 v131, 31, v130
	v_lshlrev_b64 v[132:133], 13, v[178:179]
	v_lshl_add_u64 v[132:133], s[36:37], 0, v[132:133]
	v_lshlrev_b64 v[136:137], 1, v[130:131]
	v_lshl_add_u64 v[130:131], v[132:133], 0, v[136:137]
	v_cvt_pk_bf16_f32 v132, v126, v127
	v_cvt_pk_bf16_f32 v133, v128, v129
	v_cvt_pk_bf16_f32 v134, v122, v123
	v_cvt_pk_bf16_f32 v135, v124, v125
	global_store_dwordx4 v[130:131], v[132:135], off
	s_mov_b64 s[0:1], 0x100000
	s_nop 0
	v_cvt_pk_bf16_f32 v132, v114, v115
	v_cvt_pk_bf16_f32 v133, v116, v117
	v_cvt_pk_bf16_f32 v134, v106, v107
	v_cvt_pk_bf16_f32 v135, v108, v109
	global_store_dwordx4 v[130:131], v[132:135], off offset:256
	s_nop 1
	v_or_b32_e32 v132, 16, v178
	v_ashrrev_i32_e32 v133, 31, v132
	v_lshlrev_b64 v[132:133], 13, v[132:133]
	v_lshl_add_u64 v[132:133], s[36:37], 0, v[132:133]
	v_lshl_add_u64 v[138:139], v[132:133], 0, v[136:137]
	v_cvt_pk_bf16_f32 v132, v118, v119
	v_cvt_pk_bf16_f32 v133, v120, v121
	v_cvt_pk_bf16_f32 v134, v110, v111
	v_cvt_pk_bf16_f32 v135, v112, v113
	global_store_dwordx4 v[138:139], v[132:135], off
	s_nop 1
	v_cvt_pk_bf16_f32 v132, v98, v99
	v_cvt_pk_bf16_f32 v133, v100, v101
	v_cvt_pk_bf16_f32 v134, v90, v91
	v_cvt_pk_bf16_f32 v135, v92, v93
	global_store_dwordx4 v[138:139], v[132:135], off offset:256
	s_nop 1
	v_or_b32_e32 v132, 32, v178
	v_ashrrev_i32_e32 v133, 31, v132
	v_lshlrev_b64 v[132:133], 13, v[132:133]
	v_lshl_add_u64 v[132:133], s[36:37], 0, v[132:133]
	v_lshl_add_u64 v[138:139], v[132:133], 0, v[136:137]
	v_cvt_pk_bf16_f32 v132, v102, v103
	v_cvt_pk_bf16_f32 v133, v104, v105
	v_cvt_pk_bf16_f32 v134, v94, v95
	v_cvt_pk_bf16_f32 v135, v96, v97
	global_store_dwordx4 v[138:139], v[132:135], off
	s_nop 1
	v_cvt_pk_bf16_f32 v132, v82, v83
	v_cvt_pk_bf16_f32 v133, v84, v85
	v_cvt_pk_bf16_f32 v134, v74, v75
	v_cvt_pk_bf16_f32 v135, v76, v77
	global_store_dwordx4 v[138:139], v[132:135], off offset:256
	s_nop 1
	v_or_b32_e32 v132, 48, v178
	v_ashrrev_i32_e32 v133, 31, v132
	v_lshlrev_b64 v[132:133], 13, v[132:133]
	v_lshl_add_u64 v[132:133], s[36:37], 0, v[132:133]
	v_lshl_add_u64 v[136:137], v[132:133], 0, v[136:137]
	v_cvt_pk_bf16_f32 v132, v86, v87
	v_cvt_pk_bf16_f32 v133, v88, v89
	v_cvt_pk_bf16_f32 v134, v78, v79
	v_cvt_pk_bf16_f32 v135, v80, v81
	global_store_dwordx4 v[136:137], v[132:135], off
	s_nop 1
	v_cvt_pk_bf16_f32 v132, v70, v71
	v_cvt_pk_bf16_f32 v133, v72, v73
	v_cvt_pk_bf16_f32 v134, v66, v67
	v_cvt_pk_bf16_f32 v135, v68, v69
	global_store_dwordx4 v[136:137], v[132:135], off offset:256
	v_lshl_add_u64 v[136:137], v[130:131], 0, s[0:1]
	s_mov_b32 s0, 0x100000
	v_add_co_u32_e32 v138, vcc, s0, v130
	v_cvt_pk_bf16_f32 v132, v62, v63
	v_cvt_pk_bf16_f32 v133, v64, v65
	v_cvt_pk_bf16_f32 v134, v58, v59
	v_cvt_pk_bf16_f32 v135, v60, v61
	s_nop 1
	v_addc_co_u32_e32 v139, vcc, 0, v131, vcc
	s_mov_b64 s[0:1], 0x120000
	global_store_dwordx4 v[138:139], v[132:135], off
	s_nop 1
	v_cvt_pk_bf16_f32 v132, v50, v51
	v_cvt_pk_bf16_f32 v133, v52, v53
	v_cvt_pk_bf16_f32 v134, v42, v43
	v_cvt_pk_bf16_f32 v135, v44, v45
	global_store_dwordx4 v[136:137], v[132:135], off offset:256
	v_lshl_add_u64 v[136:137], v[130:131], 0, s[0:1]
	s_mov_b32 s0, 0x120000
	v_add_co_u32_e32 v138, vcc, s0, v130
	v_cvt_pk_bf16_f32 v132, v54, v55
	v_cvt_pk_bf16_f32 v133, v56, v57
	v_cvt_pk_bf16_f32 v134, v46, v47
	v_cvt_pk_bf16_f32 v135, v48, v49
	s_nop 1
	v_addc_co_u32_e32 v139, vcc, 0, v131, vcc
	s_mov_b64 s[0:1], 0x140000
	global_store_dwordx4 v[138:139], v[132:135], off
	s_nop 1
	v_cvt_pk_bf16_f32 v132, v34, v35
	v_cvt_pk_bf16_f32 v133, v36, v37
	v_cvt_pk_bf16_f32 v134, v26, v27
	v_cvt_pk_bf16_f32 v135, v28, v29
	global_store_dwordx4 v[136:137], v[132:135], off offset:256
	v_lshl_add_u64 v[136:137], v[130:131], 0, s[0:1]
	s_mov_b32 s0, 0x140000
	v_add_co_u32_e32 v138, vcc, s0, v130
	v_cvt_pk_bf16_f32 v132, v38, v39
	v_cvt_pk_bf16_f32 v133, v40, v41
	v_cvt_pk_bf16_f32 v134, v30, v31
	v_cvt_pk_bf16_f32 v135, v32, v33
	s_nop 1
	v_addc_co_u32_e32 v139, vcc, 0, v131, vcc
	s_mov_b64 s[0:1], 0x160000
	global_store_dwordx4 v[138:139], v[132:135], off
	s_nop 1
	v_cvt_pk_bf16_f32 v132, v18, v19
	v_cvt_pk_bf16_f32 v133, v20, v21
	v_cvt_pk_bf16_f32 v134, v10, v11
	v_cvt_pk_bf16_f32 v135, v12, v13
	global_store_dwordx4 v[136:137], v[132:135], off offset:256
	v_lshl_add_u64 v[136:137], v[130:131], 0, s[0:1]
	s_mov_b32 s0, 0x160000
	v_add_co_u32_e32 v130, vcc, s0, v130
	v_cvt_pk_bf16_f32 v132, v22, v23
	v_cvt_pk_bf16_f32 v133, v24, v25
	v_cvt_pk_bf16_f32 v134, v14, v15
	v_cvt_pk_bf16_f32 v135, v16, v17
	s_nop 1
	v_addc_co_u32_e32 v131, vcc, 0, v131, vcc
	global_store_dwordx4 v[130:131], v[132:135], off
	v_cvt_pk_bf16_f32 v130, v6, v7
	v_cvt_pk_bf16_f32 v131, v8, v9
	s_nop 1
	v_cvt_pk_bf16_f32 v132, v2, v3
	v_cvt_pk_bf16_f32 v133, v4, v5
	s_mov_b32 s98, 1
	global_store_dwordx4 v[136:137], v[130:133], off offset:256

; #define LAS __attribute__((address_space(3)))
; __device__ __forceinline__ float dpp_ror1(float v) { return __builtin_bit_cast(float, __builtin_amdgcn_update_dpp(0, __builtin_bit_cast(int, v), 0x121, 0xf, 0xf, false)); }
; __device__ __forceinline__ float dpp_ror15(float v) { return __builtin_bit_cast(float, __builtin_amdgcn_update_dpp(0, __builtin_bit_cast(int, v), 0x12F, 0xf, 0xf, false)); }
;     __device__ __forceinline__ void operator()(const f32x4 (&acc)[2][2][4][2], const pg8::Unit& u, int wr, int wc, int fr, int fq_in) const {
;     ...
;         } else if (pn < 44) {
;             const int ch = (pn - 12) * 64 + wc * 16 + 4 * fq;
;             const f32x4 w0 = *(const LAS f32x4*)(scw_lds + ch), w1 = *(const LAS f32x4*)(scw_lds + D + ch), w2 = *(const LAS f32x4*)(scw_lds + 2 * D + ch);
; #pragma unroll
;             for (int ai = 0; ai < 2; ++ai) {
;                 f32x4 cv[4];
; #pragma unroll
;                 for (int m = 0; m < 4; ++m) cv[m] = acc[ai][0][m][1] * acc[ai][1][m][0];
;                 f32x4 o[4];
; #pragma unroll
;                 for (int q = 0; q < 4; ++q) { float A[4], B[4];
; #pragma unroll
;                     for (int m = 0; m < 4; ++m) { A[m] = dpp_ror1(cv[m][q]); B[m] = dpp_ror15(cv[m][q]); }
; #pragma unroll
;                     for (int m = 0; m < 4; ++m) { const float pv = fr > 0 ? A[m] : (m > 0 ? A[m > 0 ? m - 1 : 0] : 0.f), nv = fr < 15 ? B[m] : (m < 3 ? B[m < 3 ? m + 1 : 3] : 0.f);
;                         o[m][q] = acc[ai][0][m][0][q] * (w0[q] * pv + w1[q] * cv[m][q] + w2[q] * nv); } }
.LBB0_474:
	s_andn2_b64 vcc, exec, s[0:1]
	s_cbranch_vccnz .LBB0_476
	s_lshl_b32 s0, s64, 6
	s_add_i32 s0, s78, s0
	v_lshl_add_u32 v146, v148, 2, s0
	v_lshl_add_u32 v134, v146, 2, 0
	v_add_u32_e32 v130, 0x20000, v134
	v_add_u32_e32 v131, 0x22000, v134
	v_add_u32_e32 v134, 0x24000, v134
	ds_read_b128 v[138:141], v130
	ds_read_b128 v[130:133], v131
	ds_read_b128 v[134:137], v134
	v_pk_mul_f32 v[144:145], v[122:123], v[114:115]
	v_pk_mul_f32 v[154:155], v[110:111], v[98:99]
	v_mov_b32_e32 v149, v171
	v_mov_b32_e32 v170, v171
	v_mov_b32_e32 v179, v171
	v_mov_b32_dpp v149, v144 row_ror:1 row_mask:0xf bank_mask:0xf
	v_mov_b32_dpp v170, v144 row_ror:15 row_mask:0xf bank_mask:0xf
	v_mov_b32_dpp v179, v154 row_ror:15 row_mask:0xf bank_mask:0xf
	s_waitcnt lgkmcnt(2)
	v_mov_b32_e32 v142, v138
	s_waitcnt lgkmcnt(0)
	v_mov_b32_e32 v143, v134
	v_cndmask_b32_e64 v183, v170, v179, s[12:13]
	v_cndmask_b32_e64 v182, v149, 0, s[14:15]
	v_pk_mul_f32 v[158:159], v[94:95], v[82:83]
	v_mov_b32_e32 v177, v171
	v_mov_b32_e32 v185, v171
	v_pk_mul_f32 v[182:183], v[142:143], v[182:183]
	v_mov_b32_dpp v177, v154 row_ror:1 row_mask:0xf bank_mask:0xf
	v_mov_b32_dpp v185, v158 row_ror:15 row_mask:0xf bank_mask:0xf
	v_fma_f32 v134, v144, v130, v182
	v_add_f32_e32 v134, v134, v183
	v_cndmask_b32_e64 v183, v179, v185, s[12:13]
	v_cndmask_b32_e64 v182, v177, v149, s[14:15]
	v_pk_mul_f32 v[180:181], v[78:79], v[70:71]
	v_mov_b32_e32 v184, v171
	v_mov_b32_e32 v189, v171
	v_pk_mul_f32 v[182:183], v[142:143], v[182:183]
	v_mov_b32_dpp v184, v158 row_ror:1 row_mask:0xf bank_mask:0xf
	v_mov_b32_dpp v189, v180 row_ror:15 row_mask:0xf bank_mask:0xf
	v_mul_f32_e32 v170, v126, v134
	v_fma_f32 v134, v154, v130, v182
	v_add_f32_e32 v134, v134, v183
	v_cndmask_b32_e64 v183, v185, v189, s[12:13]
	v_cndmask_b32_e64 v182, v184, v177, s[14:15]
	v_mov_b32_e32 v188, v171
	v_pk_mul_f32 v[182:183], v[142:143], v[182:183]
	v_mul_f32_e32 v149, v118, v134
	v_mov_b32_dpp v188, v180 row_ror:1 row_mask:0xf bank_mask:0xf
	v_fma_f32 v134, v158, v130, v182
	v_add_f32_e32 v134, v134, v183
	v_cndmask_b32_e64 v182, v188, v184, s[14:15]
	v_cndmask_b32_e64 v183, v189, 0, s[12:13]
	v_pk_mul_f32 v[182:183], v[142:143], v[182:183]
	v_mul_f32_e32 v154, v102, v134
	v_fma_f32 v134, v180, v130, v182
	v_mov_b32_e32 v144, v171
	v_mov_b32_e32 v138, v171
	v_mov_b32_e32 v179, v171
	v_add_f32_e32 v134, v183, v134
	v_mov_b32_dpp v144, v145 row_ror:1 row_mask:0xf bank_mask:0xf
	v_mov_b32_dpp v138, v145 row_ror:15 row_mask:0xf bank_mask:0xf
	v_mov_b32_dpp v179, v155 row_ror:15 row_mask:0xf bank_mask:0xf
	v_mul_f32_e32 v158, v86, v134
	v_mov_b32_e32 v134, v139
	v_cndmask_b32_e64 v139, v138, v179, s[12:13]
	v_cndmask_b32_e64 v138, v144, 0, s[14:15]
	v_pk_mul_f32 v[138:139], v[134:135], v[138:139]
	v_mov_b32_e32 v177, v171
	v_mov_b32_e32 v182, v171
	v_fma_f32 v138, v145, v131, v138
	v_mov_b32_dpp v177, v155 row_ror:1 row_mask:0xf bank_mask:0xf
	v_mov_b32_dpp v182, v159 row_ror:15 row_mask:0xf bank_mask:0xf
	v_add_f32_e32 v138, v138, v139
	v_mul_f32_e32 v185, v127, v138
	v_cndmask_b32_e64 v139, v179, v182, s[12:13]
	v_cndmask_b32_e64 v138, v177, v144, s[14:15]
	v_pk_mul_f32 v[138:139], v[134:135], v[138:139]
	v_mov_b32_e32 v180, v171
	v_mov_b32_e32 v184, v171
	v_fma_f32 v138, v155, v131, v138
	v_mov_b32_dpp v180, v159 row_ror:1 row_mask:0xf bank_mask:0xf
	v_mov_b32_dpp v184, v181 row_ror:15 row_mask:0xf bank_mask:0xf
	v_add_f32_e32 v138, v138, v139
	v_mul_f32_e32 v155, v119, v138
	v_cndmask_b32_e64 v139, v182, v184, s[12:13]
	v_cndmask_b32_e64 v138, v180, v177, s[14:15]
	v_pk_mul_f32 v[138:139], v[134:135], v[138:139]
	v_mov_b32_e32 v183, v171
	v_fma_f32 v138, v159, v131, v138
	v_add_f32_e32 v138, v138, v139
	v_mov_b32_dpp v183, v181 row_ror:1 row_mask:0xf bank_mask:0xf
	v_mul_f32_e32 v159, v103, v138
	v_cndmask_b32_e64 v138, v183, v180, s[14:15]
	v_cndmask_b32_e64 v139, v184, 0, s[12:13]
	v_pk_mul_f32 v[138:139], v[134:135], v[138:139]
	v_pk_mul_f32 v[150:151], v[124:125], v[116:117]
	v_fma_f32 v138, v181, v131, v138
	v_add_f32_e32 v138, v139, v138
	v_pk_mul_f32 v[152:153], v[112:113], v[100:101]
	v_mul_f32_e32 v177, v87, v138
	v_mov_b32_e32 v179, v171
	v_mov_b32_e32 v138, v171
	v_mov_b32_e32 v181, v171
	v_mov_b32_dpp v179, v150 row_ror:1 row_mask:0xf bank_mask:0xf
	v_mov_b32_dpp v138, v150 row_ror:15 row_mask:0xf bank_mask:0xf
	v_mov_b32_dpp v181, v152 row_ror:15 row_mask:0xf bank_mask:0xf
	v_mov_b32_e32 v144, v140
	v_mov_b32_e32 v145, v136
	v_cndmask_b32_e64 v139, v138, v181, s[12:13]
	v_cndmask_b32_e64 v138, v179, 0, s[14:15]
	v_pk_mul_f32 v[156:157], v[96:97], v[84:85]
	v_mov_b32_e32 v180, v171
	v_mov_b32_e32 v183, v171
	v_pk_mul_f32 v[138:139], v[144:145], v[138:139]
	v_mov_b32_dpp v180, v152 row_ror:1 row_mask:0xf bank_mask:0xf
	v_mov_b32_dpp v183, v156 row_ror:15 row_mask:0xf bank_mask:0xf
	v_fma_f32 v136, v150, v132, v138
	v_add_f32_e32 v136, v136, v139
	v_cndmask_b32_e64 v139, v181, v183, s[12:13]
	v_cndmask_b32_e64 v138, v180, v179, s[14:15]
	v_pk_mul_f32 v[160:161], v[80:81], v[72:73]
	v_mov_b32_e32 v182, v171
	v_mov_b32_e32 v188, v171
	v_pk_mul_f32 v[138:139], v[144:145], v[138:139]
	v_mov_b32_dpp v182, v156 row_ror:1 row_mask:0xf bank_mask:0xf
	v_mov_b32_dpp v188, v160 row_ror:15 row_mask:0xf bank_mask:0xf
	v_mul_f32_e32 v140, v128, v136
	v_fma_f32 v136, v152, v132, v138
	v_add_f32_e32 v136, v136, v139
	v_cndmask_b32_e64 v139, v183, v188, s[12:13]
	v_cndmask_b32_e64 v138, v182, v180, s[14:15]
	v_mov_b32_e32 v184, v171
	v_pk_mul_f32 v[138:139], v[144:145], v[138:139]
	v_mul_f32_e32 v181, v120, v136
	v_mov_b32_dpp v184, v160 row_ror:1 row_mask:0xf bank_mask:0xf
	v_fma_f32 v136, v156, v132, v138
; __device__ __forceinline__ unsigned cvt_pk_bf16(float lo, float hi) { unsigned r; asm volatile("v_cvt_pk_bf16_f32 %0, %1, %2" : "=v"(r) : "v"(lo), "v"(hi)); return r; }
; #define LAS __attribute__((address_space(3)))
; __device__ __forceinline__ float dpp_ror1(float v) { return __builtin_bit_cast(float, __builtin_amdgcn_update_dpp(0, __builtin_bit_cast(int, v), 0x121, 0xf, 0xf, false)); }
; __device__ __forceinline__ float dpp_ror15(float v) { return __builtin_bit_cast(float, __builtin_amdgcn_update_dpp(0, __builtin_bit_cast(int, v), 0x12F, 0xf, 0xf, false)); }
;     __device__ __forceinline__ void operator()(const f32x4 (&acc)[2][2][4][2], const pg8::Unit& u, int wr, int wc, int fr, int fq_in) const {
;     ...
;             const int ch = (pn - 12) * 64 + wc * 16 + 4 * fq;
;             const f32x4 w0 = *(const LAS f32x4*)(scw_lds + ch), w1 = *(const LAS f32x4*)(scw_lds + D + ch), w2 = *(const LAS f32x4*)(scw_lds + 2 * D + ch);
; #pragma unroll
;             for (int ai = 0; ai < 2; ++ai) {
;                 f32x4 cv[4];
; #pragma unroll
;                 for (int m = 0; m < 4; ++m) cv[m] = acc[ai][0][m][1] * acc[ai][1][m][0];
;                 f32x4 o[4];
; #pragma unroll
;                 for (int q = 0; q < 4; ++q) { float A[4], B[4];
; #pragma unroll
;                     for (int m = 0; m < 4; ++m) { A[m] = dpp_ror1(cv[m][q]); B[m] = dpp_ror15(cv[m][q]); }
; #pragma unroll
;                     for (int m = 0; m < 4; ++m) { const float pv = fr > 0 ? A[m] : (m > 0 ? A[m > 0 ? m - 1 : 0] : 0.f), nv = fr < 15 ? B[m] : (m < 3 ? B[m < 3 ? m + 1 : 3] : 0.f);
;                         o[m][q] = acc[ai][0][m][0][q] * (w0[q] * pv + w1[q] * cv[m][q] + w2[q] * nv); } }
; #pragma unroll
;                 for (int m = 0; m < 4; ++m) { const size_t row = (size_t)(row0 + ai * 128 + m * 16); const f32x4 zz = acc[ai][1][m][1];
;                     v2u ws_; ws_.x = pg8::cvt_pk_bf16(o[m][0], o[m][1]); ws_.y = pg8::cvt_pk_bf16(o[m][2], o[m][3]); *(v2u*)(SCY + row * D + ch) = ws_;
;                     v2u wz; wz.x = pg8::cvt_pk_bf16(zz[0], zz[1]); wz.y = pg8::cvt_pk_bf16(zz[2], zz[3]); *(v2u*)(Z + row * D + ch) = wz; }
	v_add_f32_e32 v136, v136, v139
	v_cndmask_b32_e64 v138, v184, v182, s[14:15]
	v_cndmask_b32_e64 v139, v188, 0, s[12:13]
	v_pk_mul_f32 v[138:139], v[144:145], v[138:139]
	v_mul_f32_e32 v156, v104, v136
	v_fma_f32 v136, v160, v132, v138
	v_mov_b32_e32 v150, v171
	v_mov_b32_e32 v138, v171
	v_mov_b32_e32 v179, v171
	v_add_f32_e32 v136, v139, v136
	v_mov_b32_dpp v150, v151 row_ror:1 row_mask:0xf bank_mask:0xf
	v_mov_b32_dpp v138, v151 row_ror:15 row_mask:0xf bank_mask:0xf
	v_mov_b32_dpp v179, v153 row_ror:15 row_mask:0xf bank_mask:0xf
	v_mul_f32_e32 v160, v88, v136
	v_mov_b32_e32 v136, v141
	v_cndmask_b32_e64 v139, v138, v179, s[12:13]
	v_cndmask_b32_e64 v138, v150, 0, s[14:15]
	v_pk_mul_f32 v[138:139], v[136:137], v[138:139]
	v_mov_b32_e32 v152, v171
	v_mov_b32_e32 v182, v171
	v_fma_f32 v138, v151, v133, v138
	v_mov_b32_dpp v152, v153 row_ror:1 row_mask:0xf bank_mask:0xf
	v_mov_b32_dpp v182, v157 row_ror:15 row_mask:0xf bank_mask:0xf
	v_add_f32_e32 v138, v138, v139
	v_mul_f32_e32 v141, v129, v138
	v_cndmask_b32_e64 v139, v179, v182, s[12:13]
	v_cndmask_b32_e64 v138, v152, v150, s[14:15]
	v_pk_mul_f32 v[138:139], v[136:137], v[138:139]
	v_mov_b32_e32 v180, v171
	v_mov_b32_e32 v184, v171
	v_fma_f32 v138, v153, v133, v138
	v_mov_b32_dpp v180, v157 row_ror:1 row_mask:0xf bank_mask:0xf
	v_mov_b32_dpp v184, v161 row_ror:15 row_mask:0xf bank_mask:0xf
	v_add_f32_e32 v138, v138, v139
	v_mul_f32_e32 v188, v121, v138
	v_cndmask_b32_e64 v139, v182, v184, s[12:13]
	v_cndmask_b32_e64 v138, v180, v152, s[14:15]
	v_pk_mul_f32 v[138:139], v[136:137], v[138:139]
	v_mov_b32_e32 v183, v171
	v_fma_f32 v138, v157, v133, v138
	v_add_f32_e32 v138, v138, v139
	v_mov_b32_dpp v183, v161 row_ror:1 row_mask:0xf bank_mask:0xf
	v_mul_f32_e32 v157, v105, v138
	v_cndmask_b32_e64 v138, v183, v180, s[14:15]
	v_cndmask_b32_e64 v139, v184, 0, s[12:13]
	v_pk_mul_f32 v[138:139], v[136:137], v[138:139]
	v_ashrrev_i32_e32 v179, 31, v178
	v_fma_f32 v138, v161, v133, v138
	v_ashrrev_i32_e32 v147, 31, v146
	v_add_f32_e32 v138, v139, v138
	v_cvt_pk_bf16_f32 v150, v170, v185
	v_cvt_pk_bf16_f32 v151, v140, v141
	v_lshlrev_b64 v[140:141], 12, v[178:179]
	v_mul_f32_e32 v161, v89, v138
	v_lshl_add_u64 v[152:153], s[34:35], 0, v[140:141]
	v_lshlrev_b64 v[138:139], 1, v[146:147]
	v_lshl_add_u64 v[146:147], v[152:153], 0, v[138:139]
	global_store_dwordx2 v[146:147], v[150:151], off
	v_lshl_add_u64 v[150:151], s[26:27], 0, v[140:141]
	v_cvt_pk_bf16_f32 v146, v106, v107
	v_lshl_add_u64 v[150:151], v[150:151], 0, v[138:139]
	v_cvt_pk_bf16_f32 v147, v108, v109
	global_store_dwordx2 v[150:151], v[146:147], off
	v_or_b32_e32 v146, 16, v178
	v_ashrrev_i32_e32 v147, 31, v146
	v_lshlrev_b64 v[146:147], 12, v[146:147]
	v_lshl_add_u64 v[152:153], s[34:35], 0, v[146:147]
	v_lshl_add_u64 v[146:147], s[26:27], 0, v[146:147]
	v_cvt_pk_bf16_f32 v150, v149, v155
	v_cvt_pk_bf16_f32 v151, v181, v188
	v_lshl_add_u64 v[152:153], v[152:153], 0, v[138:139]
	v_lshl_add_u64 v[146:147], v[146:147], 0, v[138:139]
	global_store_dwordx2 v[152:153], v[150:151], off
	v_cvt_pk_bf16_f32 v150, v90, v91
	v_cvt_pk_bf16_f32 v151, v92, v93
	global_store_dwordx2 v[146:147], v[150:151], off
	v_or_b32_e32 v146, 32, v178
	v_ashrrev_i32_e32 v147, 31, v146
	v_lshlrev_b64 v[146:147], 12, v[146:147]
	v_lshl_add_u64 v[152:153], s[34:35], 0, v[146:147]
	v_lshl_add_u64 v[146:147], s[26:27], 0, v[146:147]
	v_cvt_pk_bf16_f32 v150, v154, v159
	v_cvt_pk_bf16_f32 v151, v156, v157
	v_lshl_add_u64 v[152:153], v[152:153], 0, v[138:139]
	v_lshl_add_u64 v[146:147], v[146:147], 0, v[138:139]
	global_store_dwordx2 v[152:153], v[150:151], off
	v_cvt_pk_bf16_f32 v150, v74, v75
	v_cvt_pk_bf16_f32 v151, v76, v77
	global_store_dwordx2 v[146:147], v[150:151], off
	v_or_b32_e32 v146, 48, v178
	v_ashrrev_i32_e32 v147, 31, v146
	v_lshlrev_b64 v[146:147], 12, v[146:147]
	v_lshl_add_u64 v[152:153], s[34:35], 0, v[146:147]
	v_cvt_pk_bf16_f32 v150, v158, v177
	v_cvt_pk_bf16_f32 v151, v160, v161
	v_lshl_add_u64 v[152:153], v[152:153], 0, v[138:139]
	v_lshl_add_u64 v[146:147], s[26:27], 0, v[146:147]
	global_store_dwordx2 v[152:153], v[150:151], off
	v_cvt_pk_bf16_f32 v150, v66, v67
	v_cvt_pk_bf16_f32 v151, v68, v69
	v_lshl_add_u64 v[146:147], v[146:147], 0, v[138:139]
	global_store_dwordx2 v[146:147], v[150:151], off
	v_pk_mul_f32 v[150:151], v[58:59], v[50:51]
	v_pk_mul_f32 v[154:155], v[46:47], v[34:35]
	v_mov_b32_e32 v149, v171
	v_mov_b32_e32 v170, v171
	v_mov_b32_e32 v179, v171
	v_mov_b32_dpp v149, v150 row_ror:1 row_mask:0xf bank_mask:0xf
	v_mov_b32_dpp v170, v150 row_ror:15 row_mask:0xf bank_mask:0xf
	v_mov_b32_dpp v179, v154 row_ror:15 row_mask:0xf bank_mask:0xf
	v_cndmask_b32_e64 v183, v170, v179, s[12:13]
	v_cndmask_b32_e64 v182, v149, 0, s[14:15]
	v_pk_mul_f32 v[158:159], v[30:31], v[18:19]
	v_mov_b32_e32 v177, v171
	v_mov_b32_e32 v185, v171
	v_pk_mul_f32 v[182:183], v[142:143], v[182:183]
	v_mov_b32_dpp v177, v154 row_ror:1 row_mask:0xf bank_mask:0xf
	v_mov_b32_dpp v185, v158 row_ror:15 row_mask:0xf bank_mask:0xf
	v_fma_f32 v150, v150, v130, v182
	v_add_f32_e32 v150, v150, v183
	v_cndmask_b32_e64 v183, v179, v185, s[12:13]
	v_cndmask_b32_e64 v182, v177, v149, s[14:15]
	v_pk_mul_f32 v[180:181], v[14:15], v[6:7]
	v_mov_b32_e32 v184, v171
	v_mov_b32_e32 v189, v171
	v_pk_mul_f32 v[182:183], v[142:143], v[182:183]
	v_mov_b32_dpp v184, v158 row_ror:1 row_mask:0xf bank_mask:0xf
	v_mov_b32_dpp v189, v180 row_ror:15 row_mask:0xf bank_mask:0xf
	v_fma_f32 v149, v154, v130, v182
	v_add_f32_e32 v149, v149, v183
	v_cndmask_b32_e64 v183, v185, v189, s[12:13]
	v_cndmask_b32_e64 v182, v184, v177, s[14:15]
	v_mov_b32_e32 v188, v171
	v_pk_mul_f32 v[182:183], v[142:143], v[182:183]
; __device__ __forceinline__ float dpp_ror1(float v) { return __builtin_bit_cast(float, __builtin_amdgcn_update_dpp(0, __builtin_bit_cast(int, v), 0x121, 0xf, 0xf, false)); }
; __device__ __forceinline__ float dpp_ror15(float v) { return __builtin_bit_cast(float, __builtin_amdgcn_update_dpp(0, __builtin_bit_cast(int, v), 0x12F, 0xf, 0xf, false)); }
;     __device__ __forceinline__ void operator()(const f32x4 (&acc)[2][2][4][2], const pg8::Unit& u, int wr, int wc, int fr, int fq_in) const {
;     ...
;                 for (int m = 0; m < 4; ++m) cv[m] = acc[ai][0][m][1] * acc[ai][1][m][0];
;                 f32x4 o[4];
; #pragma unroll
;                 for (int q = 0; q < 4; ++q) { float A[4], B[4];
; #pragma unroll
;                     for (int m = 0; m < 4; ++m) { A[m] = dpp_ror1(cv[m][q]); B[m] = dpp_ror15(cv[m][q]); }
; #pragma unroll
;                     for (int m = 0; m < 4; ++m) { const float pv = fr > 0 ? A[m] : (m > 0 ? A[m > 0 ? m - 1 : 0] : 0.f), nv = fr < 15 ? B[m] : (m < 3 ? B[m < 3 ? m + 1 : 3] : 0.f);
;                         o[m][q] = acc[ai][0][m][0][q] * (w0[q] * pv + w1[q] * cv[m][q] + w2[q] * nv); } }
	v_mov_b32_e32 v177, v171
	v_mov_b32_dpp v188, v180 row_ror:1 row_mask:0xf bank_mask:0xf
	v_fma_f32 v154, v158, v130, v182
	v_add_f32_e32 v154, v154, v183
	v_cndmask_b32_e64 v182, v188, v184, s[14:15]
	v_cndmask_b32_e64 v183, v189, 0, s[12:13]
	v_pk_mul_f32 v[142:143], v[142:143], v[182:183]
	v_mov_b32_dpp v177, v155 row_ror:15 row_mask:0xf bank_mask:0xf
	v_fma_f32 v130, v180, v130, v142
	v_add_f32_e32 v130, v143, v130
	v_mul_f32_e32 v158, v22, v130
	v_mov_b32_e32 v130, v171
	v_mov_b32_e32 v142, v171
	v_mov_b32_e32 v170, v171
	v_mov_b32_dpp v130, v151 row_ror:1 row_mask:0xf bank_mask:0xf
	v_mov_b32_dpp v142, v151 row_ror:15 row_mask:0xf bank_mask:0xf
	v_cndmask_b32_e64 v143, v142, v177, s[12:13]
	v_cndmask_b32_e64 v142, v130, 0, s[14:15]
	v_pk_mul_f32 v[142:143], v[134:135], v[142:143]
	v_mov_b32_e32 v180, v171
	v_fma_f32 v142, v151, v131, v142
	v_mov_b32_dpp v170, v155 row_ror:1 row_mask:0xf bank_mask:0xf
	v_mov_b32_dpp v180, v159 row_ror:15 row_mask:0xf bank_mask:0xf
	v_add_f32_e32 v142, v142, v143
	v_mul_f32_e32 v151, v63, v142
	v_cndmask_b32_e64 v143, v177, v180, s[12:13]
	v_cndmask_b32_e64 v142, v170, v130, s[14:15]
	v_mov_b32_e32 v179, v171
	v_mov_b32_e32 v183, v171
	v_pk_mul_f32 v[142:143], v[134:135], v[142:143]
	v_mov_b32_dpp v179, v159 row_ror:1 row_mask:0xf bank_mask:0xf
	v_mov_b32_dpp v183, v181 row_ror:15 row_mask:0xf bank_mask:0xf
	v_fma_f32 v130, v155, v131, v142
	v_add_f32_e32 v130, v130, v143
	v_cndmask_b32_e64 v143, v180, v183, s[12:13]
	v_cndmask_b32_e64 v142, v179, v170, s[14:15]
	v_mov_b32_e32 v182, v171
	v_pk_mul_f32 v[142:143], v[134:135], v[142:143]
	v_mul_f32_e32 v155, v55, v130
	v_mov_b32_dpp v182, v181 row_ror:1 row_mask:0xf bank_mask:0xf
	v_fma_f32 v130, v159, v131, v142
	v_add_f32_e32 v130, v130, v143
	v_cndmask_b32_e64 v142, v182, v179, s[14:15]
	v_cndmask_b32_e64 v143, v183, 0, s[12:13]
	v_pk_mul_f32 v[134:135], v[134:135], v[142:143]
	v_mul_f32_e32 v159, v39, v130
	v_fma_f32 v130, v181, v131, v134
	v_add_f32_e32 v130, v135, v130
	v_pk_mul_f32 v[146:147], v[60:61], v[52:53]
	v_pk_mul_f32 v[152:153], v[48:49], v[36:37]
	v_mul_f32_e32 v142, v23, v130
	v_mov_b32_e32 v134, v171
	v_mov_b32_e32 v130, v171
	v_mov_b32_e32 v143, v171
	v_mov_b32_dpp v134, v146 row_ror:1 row_mask:0xf bank_mask:0xf
	v_mov_b32_dpp v130, v146 row_ror:15 row_mask:0xf bank_mask:0xf
	v_mov_b32_dpp v143, v152 row_ror:15 row_mask:0xf bank_mask:0xf
	v_cndmask_b32_e64 v131, v130, v143, s[12:13]
	v_cndmask_b32_e64 v130, v134, 0, s[14:15]
	v_pk_mul_f32 v[130:131], v[144:145], v[130:131]
	v_pk_mul_f32 v[156:157], v[32:33], v[20:21]
	v_mov_b32_e32 v135, v171
	v_mov_b32_e32 v177, v171
	v_fma_f32 v130, v146, v132, v130
	v_mov_b32_dpp v135, v152 row_ror:1 row_mask:0xf bank_mask:0xf
	v_mov_b32_dpp v177, v156 row_ror:15 row_mask:0xf bank_mask:0xf
	v_add_f32_e32 v130, v130, v131
	v_mul_f32_e32 v146, v64, v130
	v_cndmask_b32_e64 v131, v143, v177, s[12:13]
	v_cndmask_b32_e64 v130, v135, v134, s[14:15]
	v_pk_mul_f32 v[130:131], v[144:145], v[130:131]
	v_pk_mul_f32 v[160:161], v[16:17], v[8:9]
	v_mov_b32_e32 v170, v171
	v_mov_b32_e32 v180, v171
	v_fma_f32 v130, v152, v132, v130
	v_mov_b32_dpp v170, v156 row_ror:1 row_mask:0xf bank_mask:0xf
	v_mov_b32_dpp v180, v160 row_ror:15 row_mask:0xf bank_mask:0xf
	v_add_f32_e32 v130, v130, v131
	v_mul_f32_e32 v143, v56, v130
	v_cndmask_b32_e64 v131, v177, v180, s[12:13]
	v_cndmask_b32_e64 v130, v170, v135, s[14:15]
	v_pk_mul_f32 v[130:131], v[144:145], v[130:131]
	v_mov_b32_e32 v179, v171
	v_fma_f32 v130, v156, v132, v130
	v_add_f32_e32 v130, v130, v131
	v_mov_b32_dpp v179, v160 row_ror:1 row_mask:0xf bank_mask:0xf
	v_mul_f32_e32 v152, v40, v130
	v_cndmask_b32_e64 v130, v179, v170, s[14:15]
	v_cndmask_b32_e64 v131, v180, 0, s[12:13]
	v_pk_mul_f32 v[130:131], v[144:145], v[130:131]
	v_mov_b32_e32 v135, v171
	v_fma_f32 v130, v160, v132, v130
	v_add_f32_e32 v130, v131, v130
; __device__ __forceinline__ unsigned cvt_pk_bf16(float lo, float hi) { unsigned r; asm volatile("v_cvt_pk_bf16_f32 %0, %1, %2" : "=v"(r) : "v"(lo), "v"(hi)); return r; }
; __device__ __forceinline__ float dpp_ror1(float v) { return __builtin_bit_cast(float, __builtin_amdgcn_update_dpp(0, __builtin_bit_cast(int, v), 0x121, 0xf, 0xf, false)); }
; __device__ __forceinline__ float dpp_ror15(float v) { return __builtin_bit_cast(float, __builtin_amdgcn_update_dpp(0, __builtin_bit_cast(int, v), 0x12F, 0xf, 0xf, false)); }
;     __device__ __forceinline__ void operator()(const f32x4 (&acc)[2][2][4][2], const pg8::Unit& u, int wr, int wc, int fr, int fq_in) const {
;     ...
;                 for (int q = 0; q < 4; ++q) { float A[4], B[4];
; #pragma unroll
;                     for (int m = 0; m < 4; ++m) { A[m] = dpp_ror1(cv[m][q]); B[m] = dpp_ror15(cv[m][q]); }
; #pragma unroll
;                     for (int m = 0; m < 4; ++m) { const float pv = fr > 0 ? A[m] : (m > 0 ? A[m > 0 ? m - 1 : 0] : 0.f), nv = fr < 15 ? B[m] : (m < 3 ? B[m < 3 ? m + 1 : 3] : 0.f);
;                         o[m][q] = acc[ai][0][m][0][q] * (w0[q] * pv + w1[q] * cv[m][q] + w2[q] * nv); } }
; #pragma unroll
;                 for (int m = 0; m < 4; ++m) { const size_t row = (size_t)(row0 + ai * 128 + m * 16); const f32x4 zz = acc[ai][1][m][1];
;                     v2u ws_; ws_.x = pg8::cvt_pk_bf16(o[m][0], o[m][1]); ws_.y = pg8::cvt_pk_bf16(o[m][2], o[m][3]); *(v2u*)(SCY + row * D + ch) = ws_;
;                     v2u wz; wz.x = pg8::cvt_pk_bf16(zz[0], zz[1]); wz.y = pg8::cvt_pk_bf16(zz[2], zz[3]); *(v2u*)(Z + row * D + ch) = wz; }
	v_mul_f32_e32 v144, v24, v130
	v_mov_b32_e32 v132, v171
	v_mov_b32_e32 v130, v171
	v_mov_b32_dpp v135, v153 row_ror:15 row_mask:0xf bank_mask:0xf
	v_mov_b32_dpp v132, v147 row_ror:1 row_mask:0xf bank_mask:0xf
	v_mov_b32_dpp v130, v147 row_ror:15 row_mask:0xf bank_mask:0xf
	v_cndmask_b32_e64 v131, v130, v135, s[12:13]
	v_cndmask_b32_e64 v130, v132, 0, s[14:15]
	v_pk_mul_f32 v[130:131], v[136:137], v[130:131]
	v_mov_b32_e32 v134, v171
	v_mov_b32_e32 v156, v171
	v_fma_f32 v130, v147, v133, v130
	v_mov_b32_dpp v134, v153 row_ror:1 row_mask:0xf bank_mask:0xf
	v_mov_b32_dpp v156, v157 row_ror:15 row_mask:0xf bank_mask:0xf
	v_add_f32_e32 v130, v130, v131
	v_mul_f32_e32 v147, v65, v130
	v_cndmask_b32_e64 v131, v135, v156, s[12:13]
	v_cndmask_b32_e64 v130, v134, v132, s[14:15]
	v_pk_mul_f32 v[130:131], v[136:137], v[130:131]
	v_mov_b32_e32 v145, v171
	v_mov_b32_e32 v170, v171
	v_fma_f32 v130, v153, v133, v130
	v_mov_b32_dpp v145, v157 row_ror:1 row_mask:0xf bank_mask:0xf
	v_mov_b32_dpp v170, v161 row_ror:15 row_mask:0xf bank_mask:0xf
	v_add_f32_e32 v130, v130, v131
	v_mul_f32_e32 v153, v57, v130
	v_cndmask_b32_e64 v131, v156, v170, s[12:13]
	v_cndmask_b32_e64 v130, v145, v134, s[14:15]
	v_pk_mul_f32 v[130:131], v[136:137], v[130:131]
	v_mov_b32_e32 v160, v171
	v_fma_f32 v130, v157, v133, v130
	v_add_f32_e32 v130, v130, v131
	v_mov_b32_dpp v160, v161 row_ror:1 row_mask:0xf bank_mask:0xf
	v_mul_f32_e32 v156, v41, v130
	v_cndmask_b32_e64 v130, v160, v145, s[14:15]
	v_cndmask_b32_e64 v131, v170, 0, s[12:13]
	v_pk_mul_f32 v[130:131], v[136:137], v[130:131]
	s_mov_b64 s[0:1], 0x80000
	v_fma_f32 v130, v161, v133, v130
	v_add_f32_e32 v130, v131, v130
	v_mul_f32_e32 v136, v25, v130
	v_lshl_add_u64 v[130:131], v[140:141], 0, s[0:1]
	v_lshl_add_u64 v[134:135], s[34:35], 0, v[130:131]
	v_lshl_add_u64 v[130:131], s[26:27], 0, v[130:131]
	v_mul_f32_e32 v150, v62, v150
	v_cvt_pk_bf16_f32 v132, v150, v151
	v_cvt_pk_bf16_f32 v133, v146, v147
	v_lshl_add_u64 v[134:135], v[134:135], 0, v[138:139]
	v_lshl_add_u64 v[130:131], v[130:131], 0, v[138:139]
	s_mov_b64 s[0:1], 0x90000
	global_store_dwordx2 v[134:135], v[132:133], off
	v_cvt_pk_bf16_f32 v132, v42, v43
	v_cvt_pk_bf16_f32 v133, v44, v45
	global_store_dwordx2 v[130:131], v[132:133], off
	v_lshl_add_u64 v[130:131], v[140:141], 0, s[0:1]
	v_lshl_add_u64 v[134:135], s[34:35], 0, v[130:131]
	v_lshl_add_u64 v[130:131], s[26:27], 0, v[130:131]
	v_mul_f32_e32 v149, v54, v149
	v_cvt_pk_bf16_f32 v132, v149, v155
	v_cvt_pk_bf16_f32 v133, v143, v153
	v_lshl_add_u64 v[134:135], v[134:135], 0, v[138:139]
	v_lshl_add_u64 v[130:131], v[130:131], 0, v[138:139]
	s_mov_b64 s[0:1], 0xa0000
	global_store_dwordx2 v[134:135], v[132:133], off
	v_cvt_pk_bf16_f32 v132, v26, v27
	v_cvt_pk_bf16_f32 v133, v28, v29
	global_store_dwordx2 v[130:131], v[132:133], off
	v_lshl_add_u64 v[130:131], v[140:141], 0, s[0:1]
	v_lshl_add_u64 v[134:135], s[34:35], 0, v[130:131]
	v_lshl_add_u64 v[130:131], s[26:27], 0, v[130:131]
	v_mul_f32_e32 v154, v38, v154
	v_cvt_pk_bf16_f32 v132, v154, v159
	v_cvt_pk_bf16_f32 v133, v152, v156
	v_lshl_add_u64 v[134:135], v[134:135], 0, v[138:139]
	v_lshl_add_u64 v[130:131], v[130:131], 0, v[138:139]
	s_mov_b64 s[0:1], 0xb0000
	global_store_dwordx2 v[134:135], v[132:133], off
	v_cvt_pk_bf16_f32 v132, v10, v11
	v_cvt_pk_bf16_f32 v133, v12, v13
	global_store_dwordx2 v[130:131], v[132:133], off
	v_lshl_add_u64 v[130:131], v[140:141], 0, s[0:1]
	v_lshl_add_u64 v[134:135], s[34:35], 0, v[130:131]
	v_lshl_add_u64 v[130:131], s[26:27], 0, v[130:131]
	v_cvt_pk_bf16_f32 v132, v158, v142
	v_cvt_pk_bf16_f32 v133, v144, v136
	v_lshl_add_u64 v[134:135], v[134:135], 0, v[138:139]
	v_lshl_add_u64 v[130:131], v[130:131], 0, v[138:139]
	global_store_dwordx2 v[134:135], v[132:133], off
	v_cvt_pk_bf16_f32 v132, v2, v3
	v_cvt_pk_bf16_f32 v133, v4, v5
	s_mov_b32 s98, 1
	global_store_dwordx2 v[130:131], v[132:133], off

; __device__ __forceinline__ unsigned cvt_pk_bf16(float lo, float hi) { unsigned r; asm volatile("v_cvt_pk_bf16_f32 %0, %1, %2" : "=v"(r) : "v"(lo), "v"(hi)); return r; }
; __device__ __forceinline__ float siluf(float x) { return x * __builtin_amdgcn_rcpf(1.f + __expf(-x)); }
;     __device__ __forceinline__ void operator()(const f32x4 (&acc)[2][2][4][2], const pg8::Unit& u, int wr, int wc, int fr, int fq_in) const {
;     ...
;         if (pn < 12) {
;             const int col0 = pn * 256 + wc * 32 + 8 * fq;
;             if (u.pm >= 64) {
; #pragma unroll
;                 for (int ai = 0; ai < 2; ++ai)
; #pragma unroll
;                     for (int m = 0; m < 4; ++m) { bf16* rowp = XBCR + (size_t)(row0 - M + ai * 128 + m * 16) * XBCW + col0;
; #pragma unroll
;                         for (int bj = 0; bj < 2; ++bj) { const f32x4 v0 = acc[ai][bj][m][0], v1 = acc[ai][bj][m][1];
;                             u32x4 w; w.x = pg8::cvt_pk_bf16(v0[0], v0[1]); w.y = pg8::cvt_pk_bf16(v0[2], v0[3]); w.z = pg8::cvt_pk_bf16(v1[0], v1[1]); w.w = pg8::cvt_pk_bf16(v1[2], v1[3]);
;                             *(u32x4*)(rowp + bj * 128) = w; } }
;             } else {
; #pragma unroll
;                 for (int bj = 0; bj < 2; ++bj) {
;                     const int col = col0 + bj * 128;
;                     f32x4 w0[2], w1[2], w2[2], bb[2];
; #pragma unroll
;                     for (int n = 0; n < 2; ++n) { w0[n] = *(const f32x4*)(cw + col + 4 * n); w1[n] = *(const f32x4*)(cw + XBCW + col + 4 * n); w2[n] = *(const f32x4*)(cw + 2 * XBCW + col + 4 * n); bb[n] = *(const f32x4*)(cb + col + 4 * n); }
; #pragma unroll
;                     for (int ai = 0; ai < 2; ++ai) {
;                         f32x4 o[4][2];
; #pragma unroll
;                         for (int n = 0; n < 2; ++n)
; #pragma unroll
;                             for (int q = 0; q < 4; ++q) { float A[4], B[4];
; #pragma unroll
;                                 for (int m = 0; m < 4; ++m) { A[m] = dpp_ror1(acc[ai][bj][m][n][q]); B[m] = dpp_ror15(acc[ai][bj][m][n][q]); }
; #pragma unroll
;                                 for (int m = 0; m < 4; ++m) { const float pv = fr > 0 ? A[m] : (m > 0 ? A[m > 0 ? m - 1 : 0] : 0.f), nv = fr < 15 ? B[m] : (m < 3 ? B[m < 3 ? m + 1 : 3] : 0.f);
;                                     o[m][n][q] = siluf(bb[n][q] + w0[n][q] * pv + w1[n][q] * acc[ai][bj][m][n][q] + w2[n][q] * nv); } }
.LBB0_477:
	s_andn2_b64 vcc, exec, s[0:1]
	s_cbranch_vccnz .LBB0_482
	s_lshl_b32 s0, s64, 8
	s_or_b32 s0, s0, s73
	v_lshl_add_u32 v180, v148, 3, s0
	s_cmp_gt_i32 s62, 63
	v_ashrrev_i32_e32 v181, 31, v180
	s_mov_b64 s[0:1], -1
	s_cbranch_scc1 .LBB0_480
	v_lshlrev_b64 v[130:131], 2, v[180:181]
	v_lshl_add_u64 v[182:183], s[16:17], 0, v[130:131]
	v_lshl_add_u64 v[184:185], s[48:49], 0, v[130:131]
	v_lshl_add_u64 v[188:189], s[50:51], 0, v[130:131]
	v_lshl_add_u64 v[190:191], s[18:19], 0, v[130:131]
	global_load_dwordx4 v[146:149], v[182:183], off
	global_load_dwordx4 v[150:153], v[190:191], off
	global_load_dwordx4 v[158:161], v[188:189], off
	global_load_dwordx4 v[154:157], v[184:185], off
	v_mov_b32_e32 v170, v171
	v_mov_b32_e32 v177, v171
	v_mov_b32_e32 v179, v171
	v_mov_b32_e32 v193, v171
	v_mov_b32_e32 v195, v171
	v_mov_b32_e32 v197, v171
	v_mov_b32_e32 v198, v171
	v_mov_b32_e32 v200, v171
	v_mov_b32_dpp v170, v126 row_ror:1 row_mask:0xf bank_mask:0xf
	v_mov_b32_dpp v177, v126 row_ror:15 row_mask:0xf bank_mask:0xf
	v_mov_b32_dpp v179, v118 row_ror:1 row_mask:0xf bank_mask:0xf
	v_mov_b32_dpp v193, v118 row_ror:15 row_mask:0xf bank_mask:0xf
	v_mov_b32_dpp v195, v102 row_ror:1 row_mask:0xf bank_mask:0xf
	v_mov_b32_dpp v197, v102 row_ror:15 row_mask:0xf bank_mask:0xf
	v_mov_b32_dpp v198, v86 row_ror:1 row_mask:0xf bank_mask:0xf
	v_mov_b32_dpp v200, v86 row_ror:15 row_mask:0xf bank_mask:0xf
	v_cndmask_b32_e64 v202, v170, 0, s[14:15]
	v_mov_b32_e32 v192, v126
	v_mov_b32_e32 v194, v118
	v_cndmask_b32_e64 v201, v177, v193, s[12:13]
	v_cndmask_b32_e64 v170, v179, v170, s[14:15]
	v_cndmask_b32_e64 v203, v193, v197, s[12:13]
	v_cndmask_b32_e64 v177, v195, v179, s[14:15]
	v_cndmask_b32_e64 v205, v197, v200, s[12:13]
	v_cndmask_b32_e64 v179, v198, v195, s[14:15]
	v_cndmask_b32_e64 v206, v200, 0, s[12:13]
	v_mov_b32_e32 v196, v102
	v_mov_b32_e32 v199, v86
	v_mov_b32_e32 v208, v171
	v_mov_b32_e32 v209, v171
	v_mov_b32_e32 v219, v171
	v_mov_b32_dpp v208, v127 row_ror:1 row_mask:0xf bank_mask:0xf
	v_mov_b32_dpp v209, v127 row_ror:15 row_mask:0xf bank_mask:0xf
	v_mov_b32_dpp v219, v119 row_ror:15 row_mask:0xf bank_mask:0xf
	v_mov_b32_e32 v218, v171
	v_mov_b32_e32 v221, v171
	v_mov_b32_e32 v220, v171
	v_mov_b32_dpp v218, v119 row_ror:1 row_mask:0xf bank_mask:0xf
	v_mov_b32_dpp v221, v103 row_ror:15 row_mask:0xf bank_mask:0xf
	v_mov_b32_dpp v220, v103 row_ror:1 row_mask:0xf bank_mask:0xf
	global_load_dwordx4 v[138:141], v[182:183], off offset:16
	global_load_dwordx4 v[130:133], v[184:185], off offset:16
	global_load_dwordx4 v[142:145], v[188:189], off offset:16
	global_load_dwordx4 v[134:137], v[190:191], off offset:16
	v_mov_b32_e32 v223, v171
	v_mov_b32_e32 v227, v171
	v_mov_b32_e32 v226, v171
	v_mov_b32_dpp v223, v78 row_ror:15 row_mask:0xf bank_mask:0xf
	v_mov_b32_dpp v227, v79 row_ror:15 row_mask:0xf bank_mask:0xf
	v_mov_b32_dpp v226, v79 row_ror:1 row_mask:0xf bank_mask:0xf
	v_mov_b32_e32 v231, v171
	v_mov_b32_e32 v230, v171
	v_mov_b32_e32 v235, v171
	v_mov_b32_dpp v231, v80 row_ror:15 row_mask:0xf bank_mask:0xf
	v_mov_b32_dpp v230, v80 row_ror:1 row_mask:0xf bank_mask:0xf
	v_mov_b32_dpp v235, v81 row_ror:15 row_mask:0xf bank_mask:0xf
	v_mov_b32_e32 v234, v171
	v_mov_b32_e32 v239, v171
	v_mov_b32_e32 v238, v171
	v_mov_b32_dpp v234, v81 row_ror:1 row_mask:0xf bank_mask:0xf
	v_mov_b32_dpp v239, v68 row_ror:15 row_mask:0xf bank_mask:0xf
	v_mov_b32_dpp v238, v68 row_ror:1 row_mask:0xf bank_mask:0xf
	v_mov_b32_e32 v243, v171
	v_mov_b32_e32 v242, v171
	s_waitcnt vmcnt(6)
	v_fma_f32 v222, v146, v202, v150
	s_waitcnt vmcnt(5)
	v_mov_b32_e32 v193, v158
	s_waitcnt vmcnt(4)
	v_mov_b32_e32 v200, v154
	v_mov_b32_e32 v195, v158
	v_mov_b32_e32 v202, v154
	v_fma_f32 v170, v146, v170, v150
	v_mov_b32_e32 v197, v158
	v_mov_b32_e32 v204, v154
	v_mov_b32_e32 v198, v158
	v_mov_b32_e32 v207, v154
	v_pk_mul_f32 v[192:193], v[192:193], v[200:201]
	v_pk_mul_f32 v[194:195], v[194:195], v[202:203]
	v_fma_f32 v177, v146, v177, v150
	v_fma_f32 v179, v146, v179, v150
	v_pk_mul_f32 v[196:197], v[196:197], v[204:205]
	v_pk_mul_f32 v[198:199], v[198:199], v[206:207]
	v_add_f32_e32 v192, v192, v222
	v_add_f32_e32 v170, v194, v170
	v_add_f32_e32 v177, v196, v177
	v_add_f32_e32 v179, v199, v179
	v_add_f32_e32 v192, v192, v193
	v_add_f32_e32 v170, v170, v195
	v_add_f32_e32 v177, v177, v197
	v_add_f32_e32 v193, v198, v179
	v_mul_f32_e32 v179, 0xbfb8aa3b, v192
	v_mul_f32_e32 v194, 0xbfb8aa3b, v170
	v_mul_f32_e32 v195, 0xbfb8aa3b, v177
	v_mul_f32_e32 v196, 0xbfb8aa3b, v193
	v_exp_f32_e32 v179, v179
	v_exp_f32_e32 v194, v194
	v_exp_f32_e32 v195, v195
	v_exp_f32_e32 v196, v196
	v_add_f32_e32 v179, 1.0, v179
	v_add_f32_e32 v194, 1.0, v194
	v_add_f32_e32 v195, 1.0, v195
	v_add_f32_e32 v196, 1.0, v196
	v_rcp_f32_e32 v179, v179
	v_rcp_f32_e32 v194, v194
	v_rcp_f32_e32 v195, v195
	v_rcp_f32_e32 v196, v196
	v_mul_f32_e32 v192, v192, v179
	v_mul_f32_e32 v179, v170, v194
	v_cndmask_b32_e64 v194, v208, 0, s[14:15]
	v_mul_f32_e32 v177, v177, v195
	v_mul_f32_e32 v170, v193, v196
	v_cndmask_b32_e64 v195, v209, v219, s[12:13]
	v_fma_f32 v199, v147, v194, v151
	v_mov_b32_e32 v196, v127
	v_mov_b32_e32 v197, v159
	v_mov_b32_e32 v194, v155
	v_pk_mul_f32 v[194:195], v[196:197], v[194:195]
	v_mov_b32_e32 v196, v119
	v_add_f32_e32 v194, v194, v199
	v_add_f32_e32 v199, v194, v195
	v_mul_f32_e32 v194, 0xbfb8aa3b, v199
	v_exp_f32_e32 v200, v194
	v_cndmask_b32_e64 v194, v218, v208, s[14:15]
	v_cndmask_b32_e64 v195, v219, v221, s[12:13]
	v_fma_f32 v201, v147, v194, v151
	v_mov_b32_e32 v194, v155
	v_pk_mul_f32 v[194:195], v[196:197], v[194:195]
	v_mov_b32_e32 v198, v171
	v_add_f32_e32 v194, v194, v201
; __device__ __forceinline__ float siluf(float x) { return x * __builtin_amdgcn_rcpf(1.f + __expf(-x)); }
; __device__ __forceinline__ float dpp_ror1(float v) { return __builtin_bit_cast(float, __builtin_amdgcn_update_dpp(0, __builtin_bit_cast(int, v), 0x121, 0xf, 0xf, false)); }
; __device__ __forceinline__ float dpp_ror15(float v) { return __builtin_bit_cast(float, __builtin_amdgcn_update_dpp(0, __builtin_bit_cast(int, v), 0x12F, 0xf, 0xf, false)); }
;     __device__ __forceinline__ void operator()(const f32x4 (&acc)[2][2][4][2], const pg8::Unit& u, int wr, int wc, int fr, int fq_in) const {
;     ...
;                     for (int ai = 0; ai < 2; ++ai) {
;                         f32x4 o[4][2];
; #pragma unroll
;                         for (int n = 0; n < 2; ++n)
; #pragma unroll
;                             for (int q = 0; q < 4; ++q) { float A[4], B[4];
; #pragma unroll
;                                 for (int m = 0; m < 4; ++m) { A[m] = dpp_ror1(acc[ai][bj][m][n][q]); B[m] = dpp_ror15(acc[ai][bj][m][n][q]); }
; #pragma unroll
;                                 for (int m = 0; m < 4; ++m) { const float pv = fr > 0 ? A[m] : (m > 0 ? A[m > 0 ? m - 1 : 0] : 0.f), nv = fr < 15 ? B[m] : (m < 3 ? B[m < 3 ? m + 1 : 3] : 0.f);
;                                     o[m][n][q] = siluf(bb[n][q] + w0[n][q] * pv + w1[n][q] * acc[ai][bj][m][n][q] + w2[n][q] * nv); } }
	v_add_f32_e32 v201, v194, v195
	v_mul_f32_e32 v194, 0xbfb8aa3b, v201
	v_exp_f32_e32 v194, v194
	v_mov_b32_dpp v198, v87 row_ror:15 row_mask:0xf bank_mask:0xf
	v_add_f32_e32 v195, 1.0, v200
	v_rcp_f32_e32 v200, v195
	v_add_f32_e32 v202, 1.0, v194
	v_cndmask_b32_e64 v194, v220, v218, s[14:15]
	v_cndmask_b32_e64 v195, v221, v198, s[12:13]
	v_fma_f32 v203, v147, v194, v151
	v_mov_b32_e32 v196, v103
	v_mov_b32_e32 v194, v155
	v_pk_mul_f32 v[194:195], v[196:197], v[194:195]
	v_mov_b32_e32 v193, v171
	v_add_f32_e32 v194, v194, v203
	v_add_f32_e32 v203, v194, v195
	v_mov_b32_dpp v193, v87 row_ror:1 row_mask:0xf bank_mask:0xf
	v_mul_f32_e32 v194, 0xbfb8aa3b, v203
	v_exp_f32_e32 v204, v194
	v_cndmask_b32_e64 v193, v193, v220, s[14:15]
	v_cndmask_b32_e64 v194, v198, 0, s[12:13]
	v_mov_b32_e32 v196, v159
	v_mov_b32_e32 v197, v87
	v_mov_b32_e32 v195, v155
	v_fma_f32 v193, v147, v193, v151
	v_pk_mul_f32 v[194:195], v[196:197], v[194:195]
	v_add_f32_e32 v196, 1.0, v204
	v_add_f32_e32 v193, v195, v193
	v_add_f32_e32 v195, v194, v193
	v_mul_f32_e32 v193, 0xbfb8aa3b, v195
	v_exp_f32_e32 v193, v193
	v_rcp_f32_e32 v194, v202
	v_rcp_f32_e32 v196, v196
	v_mov_b32_e32 v204, v171
	v_add_f32_e32 v193, 1.0, v193
	v_rcp_f32_e32 v197, v193
	v_mul_f32_e32 v193, v199, v200
	v_mov_b32_dpp v204, v120 row_ror:15 row_mask:0xf bank_mask:0xf
	v_mul_f32_e32 v194, v201, v194
	v_mul_f32_e32 v198, v195, v197
	v_mov_b32_e32 v195, v171
	v_mov_b32_e32 v197, v171
	v_mul_f32_e32 v196, v203, v196
	v_mov_b32_dpp v195, v128 row_ror:1 row_mask:0xf bank_mask:0xf
	v_mov_b32_dpp v197, v128 row_ror:15 row_mask:0xf bank_mask:0xf
	v_cndmask_b32_e64 v200, v195, 0, s[14:15]
	v_cndmask_b32_e64 v201, v197, v204, s[12:13]
	v_fma_f32 v197, v148, v200, v152
	v_mov_b32_e32 v202, v128
	v_mov_b32_e32 v203, v160
	v_mov_b32_e32 v200, v156
	v_pk_mul_f32 v[200:201], v[202:203], v[200:201]
	v_mov_b32_e32 v199, v171
	v_add_f32_e32 v197, v200, v197
	v_mov_b32_e32 v206, v171
	v_add_f32_e32 v197, v197, v201
	v_mov_b32_dpp v199, v120 row_ror:1 row_mask:0xf bank_mask:0xf
	v_mov_b32_dpp v206, v104 row_ror:15 row_mask:0xf bank_mask:0xf
	v_mul_f32_e32 v200, 0xbfb8aa3b, v197
	v_exp_f32_e32 v209, v200
	v_cndmask_b32_e64 v195, v199, v195, s[14:15]
	v_cndmask_b32_e64 v201, v204, v206, s[12:13]
	v_mov_b32_e32 v202, v120
	v_mov_b32_e32 v200, v156
	v_fma_f32 v195, v148, v195, v152
	v_pk_mul_f32 v[200:201], v[202:203], v[200:201]
	v_mov_b32_e32 v205, v171
	v_add_f32_e32 v195, v200, v195
	v_add_f32_e32 v195, v195, v201
	v_mul_f32_e32 v200, 0xbfb8aa3b, v195
	v_exp_f32_e32 v200, v200
	v_mov_b32_e32 v208, v171
	v_mov_b32_dpp v205, v104 row_ror:1 row_mask:0xf bank_mask:0xf
	v_add_f32_e32 v201, 1.0, v209
	v_mov_b32_dpp v208, v88 row_ror:15 row_mask:0xf bank_mask:0xf
	v_rcp_f32_e32 v204, v201
	v_add_f32_e32 v209, 1.0, v200
	v_cndmask_b32_e64 v199, v205, v199, s[14:15]
	v_cndmask_b32_e64 v201, v206, v208, s[12:13]
	v_mov_b32_e32 v202, v104
	v_mov_b32_e32 v200, v156
	v_fma_f32 v199, v148, v199, v152
	v_pk_mul_f32 v[200:201], v[202:203], v[200:201]
	v_mov_b32_e32 v207, v171
	v_add_f32_e32 v199, v200, v199
	v_add_f32_e32 v199, v199, v201
	v_mov_b32_dpp v207, v88 row_ror:1 row_mask:0xf bank_mask:0xf
	v_mul_f32_e32 v200, 0xbfb8aa3b, v199
	v_cndmask_b32_e64 v201, v207, v205, s[14:15]
	v_exp_f32_e32 v206, v200
	v_cndmask_b32_e64 v200, v208, 0, s[12:13]
	v_fma_f32 v205, v148, v201, v152
	v_mov_b32_e32 v202, v160
	v_mov_b32_e32 v203, v88
	v_mov_b32_e32 v201, v156
	v_pk_mul_f32 v[200:201], v[202:203], v[200:201]
	v_rcp_f32_e32 v202, v209
	v_add_f32_e32 v201, v201, v205
	v_add_f32_e32 v200, v200, v201
	v_mul_f32_e32 v201, 0xbfb8aa3b, v200
	v_exp_f32_e32 v201, v201
	v_add_f32_e32 v203, 1.0, v206
	v_rcp_f32_e32 v203, v203
	v_mov_b32_e32 v205, v171
	v_add_f32_e32 v201, 1.0, v201
	v_rcp_f32_e32 v201, v201
	v_mul_f32_e32 v197, v197, v204
	v_mov_b32_dpp v205, v129 row_ror:1 row_mask:0xf bank_mask:0xf
	v_mov_b32_e32 v207, v171
	v_mul_f32_e32 v204, v200, v201
	v_mov_b32_e32 v200, v171
	v_mul_f32_e32 v195, v195, v202
	v_mov_b32_dpp v207, v121 row_ror:15 row_mask:0xf bank_mask:0xf
	v_mov_b32_dpp v200, v129 row_ror:15 row_mask:0xf bank_mask:0xf
	v_cndmask_b32_e64 v202, v205, 0, s[14:15]
	v_mul_f32_e32 v199, v199, v203
	v_cndmask_b32_e64 v201, v200, v207, s[12:13]
	v_fma_f32 v220, v149, v202, v153
	v_mov_b32_e32 v202, v129
	v_mov_b32_e32 v203, v161
	v_mov_b32_e32 v200, v157
	v_pk_mul_f32 v[200:201], v[202:203], v[200:201]
	v_mov_b32_e32 v206, v171
	v_add_f32_e32 v200, v200, v220
	v_add_f32_e32 v220, v200, v201
	v_mov_b32_dpp v206, v121 row_ror:1 row_mask:0xf bank_mask:0xf
	v_mov_b32_e32 v209, v171
	v_mul_f32_e32 v200, 0xbfb8aa3b, v220
	v_exp_f32_e32 v221, v200
	v_mov_b32_dpp v209, v105 row_ror:15 row_mask:0xf bank_mask:0xf
	v_cndmask_b32_e64 v200, v206, v205, s[14:15]
	v_cndmask_b32_e64 v201, v207, v209, s[12:13]
	v_fma_f32 v205, v149, v200, v153
	v_mov_b32_e32 v202, v121
	v_mov_b32_e32 v200, v157
	v_pk_mul_f32 v[200:201], v[202:203], v[200:201]
	v_mov_b32_e32 v208, v171
	v_add_f32_e32 v200, v200, v205
	v_add_f32_e32 v205, v200, v201
	v_mul_f32_e32 v200, 0xbfb8aa3b, v205
	v_exp_f32_e32 v200, v200
	v_mov_b32_dpp v208, v105 row_ror:1 row_mask:0xf bank_mask:0xf
	v_mov_b32_e32 v219, v171
	v_add_f32_e32 v201, 1.0, v221
	v_add_f32_e32 v221, 1.0, v200
	v_mov_b32_dpp v219, v89 row_ror:15 row_mask:0xf bank_mask:0xf
	v_cndmask_b32_e64 v200, v208, v206, s[14:15]
	v_rcp_f32_e32 v207, v201
	v_cndmask_b32_e64 v201, v209, v219, s[12:13]
	v_fma_f32 v206, v149, v200, v153
	v_mov_b32_e32 v202, v105
	v_mov_b32_e32 v200, v157
	v_pk_mul_f32 v[200:201], v[202:203], v[200:201]
	v_mov_b32_e32 v218, v171
	v_add_f32_e32 v200, v200, v206
	v_add_f32_e32 v206, v200, v201
	v_mov_b32_dpp v218, v89 row_ror:1 row_mask:0xf bank_mask:0xf
	v_mul_f32_e32 v200, 0xbfb8aa3b, v206
	v_cndmask_b32_e64 v201, v218, v208, s[14:15]
	v_exp_f32_e32 v209, v200
	v_cndmask_b32_e64 v200, v219, 0, s[12:13]
	v_fma_f32 v208, v149, v201, v153
	v_mov_b32_e32 v202, v161
	v_mov_b32_e32 v203, v89
	v_mov_b32_e32 v201, v157
	v_pk_mul_f32 v[200:201], v[202:203], v[200:201]
	v_add_f32_e32 v203, 1.0, v209
	v_add_f32_e32 v201, v201, v208
	v_add_f32_e32 v200, v200, v201
	v_mul_f32_e32 v201, 0xbfb8aa3b, v200
	v_exp_f32_e32 v201, v201
	v_rcp_f32_e32 v203, v203
	v_rcp_f32_e32 v202, v221
	v_mov_b32_e32 v209, v171
	v_add_f32_e32 v201, 1.0, v201
	v_rcp_f32_e32 v201, v201
	v_mul_f32_e32 v218, v206, v203
	v_mov_b32_e32 v206, v171
	v_mul_f32_e32 v205, v205, v202
	v_mul_f32_e32 v219, v200, v201
	v_mov_b32_dpp v206, v122 row_ror:1 row_mask:0xf bank_mask:0xf
	v_mov_b32_e32 v200, v171
	v_mov_b32_dpp v209, v110 row_ror:15 row_mask:0xf bank_mask:0xf
	v_cndmask_b32_e64 v202, v206, 0, s[14:15]
	v_mov_b32_dpp v200, v122 row_ror:15 row_mask:0xf bank_mask:0xf
	v_cndmask_b32_e64 v201, v200, v209, s[12:13]
	s_waitcnt vmcnt(0)
; __device__ __forceinline__ float siluf(float x) { return x * __builtin_amdgcn_rcpf(1.f + __expf(-x)); }
; __device__ __forceinline__ float dpp_ror1(float v) { return __builtin_bit_cast(float, __builtin_amdgcn_update_dpp(0, __builtin_bit_cast(int, v), 0x121, 0xf, 0xf, false)); }
; __device__ __forceinline__ float dpp_ror15(float v) { return __builtin_bit_cast(float, __builtin_amdgcn_update_dpp(0, __builtin_bit_cast(int, v), 0x12F, 0xf, 0xf, false)); }
;     __device__ __forceinline__ void operator()(const f32x4 (&acc)[2][2][4][2], const pg8::Unit& u, int wr, int wc, int fr, int fq_in) const {
;     ...
;                     for (int ai = 0; ai < 2; ++ai) {
;                         f32x4 o[4][2];
; #pragma unroll
;                         for (int n = 0; n < 2; ++n)
; #pragma unroll
;                             for (int q = 0; q < 4; ++q) { float A[4], B[4];
; #pragma unroll
;                                 for (int m = 0; m < 4; ++m) { A[m] = dpp_ror1(acc[ai][bj][m][n][q]); B[m] = dpp_ror15(acc[ai][bj][m][n][q]); }
; #pragma unroll
;                                 for (int m = 0; m < 4; ++m) { const float pv = fr > 0 ? A[m] : (m > 0 ? A[m > 0 ? m - 1 : 0] : 0.f), nv = fr < 15 ? B[m] : (m < 3 ? B[m < 3 ? m + 1 : 3] : 0.f);
;                                     o[m][n][q] = siluf(bb[n][q] + w0[n][q] * pv + w1[n][q] * acc[ai][bj][m][n][q] + w2[n][q] * nv); } }
	v_fma_f32 v224, v138, v202, v134
	v_mov_b32_e32 v202, v122
	v_mov_b32_e32 v203, v142
	v_mov_b32_e32 v200, v130
	v_pk_mul_f32 v[200:201], v[202:203], v[200:201]
	v_mov_b32_e32 v208, v171
	v_add_f32_e32 v200, v200, v224
	v_add_f32_e32 v224, v200, v201
	v_mov_b32_dpp v208, v110 row_ror:1 row_mask:0xf bank_mask:0xf
	v_mov_b32_e32 v221, v171
	v_mul_f32_e32 v200, 0xbfb8aa3b, v224
	v_exp_f32_e32 v225, v200
	v_mov_b32_dpp v221, v94 row_ror:15 row_mask:0xf bank_mask:0xf
	v_cndmask_b32_e64 v200, v208, v206, s[14:15]
	v_cndmask_b32_e64 v201, v209, v221, s[12:13]
	v_fma_f32 v206, v138, v200, v134
	v_mov_b32_e32 v202, v110
	v_mov_b32_e32 v200, v130
	v_pk_mul_f32 v[200:201], v[202:203], v[200:201]
	v_mul_f32_e32 v207, v220, v207
	v_add_f32_e32 v200, v200, v206
	v_add_f32_e32 v206, v200, v201
	v_mul_f32_e32 v200, 0xbfb8aa3b, v206
	v_exp_f32_e32 v200, v200
	v_mov_b32_e32 v220, v171
	v_add_f32_e32 v201, 1.0, v225
	v_rcp_f32_e32 v209, v201
	v_mov_b32_dpp v220, v94 row_ror:1 row_mask:0xf bank_mask:0xf
	v_add_f32_e32 v225, 1.0, v200
	v_cndmask_b32_e64 v200, v220, v208, s[14:15]
	v_cndmask_b32_e64 v201, v221, v223, s[12:13]
	v_fma_f32 v208, v138, v200, v134
	v_mov_b32_e32 v202, v94
	v_mov_b32_e32 v200, v130
	v_pk_mul_f32 v[200:201], v[202:203], v[200:201]
	v_mov_b32_e32 v222, v171
	v_add_f32_e32 v200, v200, v208
	v_add_f32_e32 v208, v200, v201
	v_mov_b32_dpp v222, v78 row_ror:1 row_mask:0xf bank_mask:0xf
	v_mul_f32_e32 v200, 0xbfb8aa3b, v208
	v_cndmask_b32_e64 v201, v222, v220, s[14:15]
	v_exp_f32_e32 v221, v200
	v_cndmask_b32_e64 v200, v223, 0, s[12:13]
	v_fma_f32 v220, v138, v201, v134
	v_mov_b32_e32 v202, v142
	v_mov_b32_e32 v203, v78
	v_mov_b32_e32 v201, v130
	v_pk_mul_f32 v[200:201], v[202:203], v[200:201]
	v_rcp_f32_e32 v202, v225
	v_add_f32_e32 v201, v201, v220
	v_add_f32_e32 v200, v200, v201
	v_mul_f32_e32 v201, 0xbfb8aa3b, v200
	v_exp_f32_e32 v201, v201
	v_add_f32_e32 v203, 1.0, v221
	v_rcp_f32_e32 v203, v203
	v_mul_f32_e32 v220, v206, v202
	v_add_f32_e32 v201, 1.0, v201
	v_rcp_f32_e32 v201, v201
	v_mov_b32_e32 v206, v171
	v_mov_b32_e32 v223, v171
	v_mul_f32_e32 v221, v208, v203
	v_mul_f32_e32 v222, v200, v201
	v_mov_b32_dpp v206, v123 row_ror:1 row_mask:0xf bank_mask:0xf
	v_mov_b32_e32 v200, v171
	v_mov_b32_dpp v223, v111 row_ror:15 row_mask:0xf bank_mask:0xf
	v_cndmask_b32_e64 v202, v206, 0, s[14:15]
	v_mov_b32_dpp v200, v123 row_ror:15 row_mask:0xf bank_mask:0xf
	v_cndmask_b32_e64 v201, v200, v223, s[12:13]
	v_fma_f32 v228, v139, v202, v135
	v_mov_b32_e32 v202, v123
	v_mov_b32_e32 v203, v143
	v_mov_b32_e32 v200, v131
	v_pk_mul_f32 v[200:201], v[202:203], v[200:201]
	v_mov_b32_e32 v208, v171
	v_add_f32_e32 v200, v200, v228
	v_add_f32_e32 v228, v200, v201
	v_mov_b32_dpp v208, v111 row_ror:1 row_mask:0xf bank_mask:0xf
	v_mov_b32_e32 v225, v171
	v_mul_f32_e32 v200, 0xbfb8aa3b, v228
	v_exp_f32_e32 v229, v200
	v_mov_b32_dpp v225, v95 row_ror:15 row_mask:0xf bank_mask:0xf
	v_cndmask_b32_e64 v200, v208, v206, s[14:15]
	v_cndmask_b32_e64 v201, v223, v225, s[12:13]
	v_fma_f32 v206, v139, v200, v135
	v_mov_b32_e32 v202, v111
	v_mov_b32_e32 v200, v131
	v_pk_mul_f32 v[200:201], v[202:203], v[200:201]
	v_mul_f32_e32 v209, v224, v209
	v_add_f32_e32 v200, v200, v206
	v_add_f32_e32 v206, v200, v201
	v_mul_f32_e32 v200, 0xbfb8aa3b, v206
	v_exp_f32_e32 v200, v200
	v_mov_b32_e32 v224, v171
	v_add_f32_e32 v201, 1.0, v229
	v_rcp_f32_e32 v223, v201
	v_mov_b32_dpp v224, v95 row_ror:1 row_mask:0xf bank_mask:0xf
	v_add_f32_e32 v229, 1.0, v200
	v_cndmask_b32_e64 v200, v224, v208, s[14:15]
	v_cndmask_b32_e64 v201, v225, v227, s[12:13]
	v_fma_f32 v208, v139, v200, v135
	v_mov_b32_e32 v202, v95
	v_mov_b32_e32 v200, v131
	v_pk_mul_f32 v[200:201], v[202:203], v[200:201]
	v_mov_b32_e32 v202, v143
	v_add_f32_e32 v200, v200, v208
	v_add_f32_e32 v208, v200, v201
	v_mul_f32_e32 v200, 0xbfb8aa3b, v208
	v_cndmask_b32_e64 v201, v226, v224, s[14:15]
	v_exp_f32_e32 v225, v200
	v_cndmask_b32_e64 v200, v227, 0, s[12:13]
	v_fma_f32 v224, v139, v201, v135
	v_mov_b32_e32 v203, v79
	v_mov_b32_e32 v201, v131
	v_pk_mul_f32 v[200:201], v[202:203], v[200:201]
	v_rcp_f32_e32 v202, v229
	v_add_f32_e32 v201, v201, v224
	v_add_f32_e32 v200, v200, v201
	v_mul_f32_e32 v201, 0xbfb8aa3b, v200
	v_exp_f32_e32 v201, v201
	v_add_f32_e32 v203, 1.0, v225
	v_rcp_f32_e32 v203, v203
	v_mul_f32_e32 v224, v206, v202
	v_add_f32_e32 v201, 1.0, v201
	v_rcp_f32_e32 v201, v201
	v_mov_b32_e32 v206, v171
	v_mov_b32_e32 v227, v171
	v_mul_f32_e32 v225, v208, v203
	v_mul_f32_e32 v226, v200, v201
	v_mov_b32_dpp v206, v124 row_ror:1 row_mask:0xf bank_mask:0xf
	v_mov_b32_e32 v200, v171
	v_mov_b32_dpp v227, v112 row_ror:15 row_mask:0xf bank_mask:0xf
	v_cndmask_b32_e64 v202, v206, 0, s[14:15]
	v_mov_b32_dpp v200, v124 row_ror:15 row_mask:0xf bank_mask:0xf
	v_cndmask_b32_e64 v201, v200, v227, s[12:13]
	v_fma_f32 v232, v140, v202, v136
	v_mov_b32_e32 v202, v124
	v_mov_b32_e32 v203, v144
	v_mov_b32_e32 v200, v132
	v_pk_mul_f32 v[200:201], v[202:203], v[200:201]
	v_mov_b32_e32 v208, v171
	v_add_f32_e32 v200, v200, v232
	v_add_f32_e32 v232, v200, v201
	v_mov_b32_dpp v208, v112 row_ror:1 row_mask:0xf bank_mask:0xf
	v_mov_b32_e32 v229, v171
	v_mul_f32_e32 v200, 0xbfb8aa3b, v232
	v_exp_f32_e32 v233, v200
	v_mov_b32_dpp v229, v96 row_ror:15 row_mask:0xf bank_mask:0xf
	v_cndmask_b32_e64 v200, v208, v206, s[14:15]
	v_cndmask_b32_e64 v201, v227, v229, s[12:13]
	v_fma_f32 v206, v140, v200, v136
	v_mov_b32_e32 v202, v112
	v_mov_b32_e32 v200, v132
	v_pk_mul_f32 v[200:201], v[202:203], v[200:201]
	v_mul_f32_e32 v223, v228, v223
	v_add_f32_e32 v200, v200, v206
	v_add_f32_e32 v206, v200, v201
	v_mul_f32_e32 v200, 0xbfb8aa3b, v206
	v_exp_f32_e32 v200, v200
; __device__ __forceinline__ unsigned cvt_pk_bf16(float lo, float hi) { unsigned r; asm volatile("v_cvt_pk_bf16_f32 %0, %1, %2" : "=v"(r) : "v"(lo), "v"(hi)); return r; }
; __device__ __forceinline__ float siluf(float x) { return x * __builtin_amdgcn_rcpf(1.f + __expf(-x)); }
; __device__ __forceinline__ float dpp_ror1(float v) { return __builtin_bit_cast(float, __builtin_amdgcn_update_dpp(0, __builtin_bit_cast(int, v), 0x121, 0xf, 0xf, false)); }
; __device__ __forceinline__ float dpp_ror15(float v) { return __builtin_bit_cast(float, __builtin_amdgcn_update_dpp(0, __builtin_bit_cast(int, v), 0x12F, 0xf, 0xf, false)); }
;     __device__ __forceinline__ void operator()(const f32x4 (&acc)[2][2][4][2], const pg8::Unit& u, int wr, int wc, int fr, int fq_in) const {
;     ...
;                     for (int ai = 0; ai < 2; ++ai) {
;                         f32x4 o[4][2];
; #pragma unroll
;                         for (int n = 0; n < 2; ++n)
; #pragma unroll
;                             for (int q = 0; q < 4; ++q) { float A[4], B[4];
; #pragma unroll
;                                 for (int m = 0; m < 4; ++m) { A[m] = dpp_ror1(acc[ai][bj][m][n][q]); B[m] = dpp_ror15(acc[ai][bj][m][n][q]); }
; #pragma unroll
;                                 for (int m = 0; m < 4; ++m) { const float pv = fr > 0 ? A[m] : (m > 0 ? A[m > 0 ? m - 1 : 0] : 0.f), nv = fr < 15 ? B[m] : (m < 3 ? B[m < 3 ? m + 1 : 3] : 0.f);
;                                     o[m][n][q] = siluf(bb[n][q] + w0[n][q] * pv + w1[n][q] * acc[ai][bj][m][n][q] + w2[n][q] * nv); } }
; #pragma unroll
;                         for (int m = 0; m < 4; ++m) { u32x4 w; w.x = pg8::cvt_pk_bf16(o[m][0][0], o[m][0][1]); w.y = pg8::cvt_pk_bf16(o[m][0][2], o[m][0][3]); w.z = pg8::cvt_pk_bf16(o[m][1][0], o[m][1][1]); w.w = pg8::cvt_pk_bf16(o[m][1][2], o[m][1][3]);
;                             *(u32x4*)(XBC + (size_t)(row0 + ai * 128 + m * 16) * XBCW + col) = w; }
	v_mov_b32_e32 v228, v171
	v_add_f32_e32 v201, 1.0, v233
	v_rcp_f32_e32 v227, v201
	v_mov_b32_dpp v228, v96 row_ror:1 row_mask:0xf bank_mask:0xf
	v_add_f32_e32 v233, 1.0, v200
	v_cndmask_b32_e64 v200, v228, v208, s[14:15]
	v_cndmask_b32_e64 v201, v229, v231, s[12:13]
	v_fma_f32 v208, v140, v200, v136
	v_mov_b32_e32 v202, v96
	v_mov_b32_e32 v200, v132
	v_pk_mul_f32 v[200:201], v[202:203], v[200:201]
	v_mov_b32_e32 v202, v144
	v_add_f32_e32 v200, v200, v208
	v_add_f32_e32 v208, v200, v201
	v_mul_f32_e32 v200, 0xbfb8aa3b, v208
	v_cndmask_b32_e64 v201, v230, v228, s[14:15]
	v_exp_f32_e32 v229, v200
	v_cndmask_b32_e64 v200, v231, 0, s[12:13]
	v_fma_f32 v228, v140, v201, v136
	v_mov_b32_e32 v203, v80
	v_mov_b32_e32 v201, v132
	v_pk_mul_f32 v[200:201], v[202:203], v[200:201]
	v_rcp_f32_e32 v202, v233
	v_add_f32_e32 v201, v201, v228
	v_add_f32_e32 v200, v200, v201
	v_mul_f32_e32 v201, 0xbfb8aa3b, v200
	v_exp_f32_e32 v201, v201
	v_add_f32_e32 v203, 1.0, v229
	v_rcp_f32_e32 v203, v203
	v_mul_f32_e32 v228, v206, v202
	v_add_f32_e32 v201, 1.0, v201
	v_rcp_f32_e32 v201, v201
	v_mov_b32_e32 v206, v171
	v_mov_b32_e32 v231, v171
	v_mul_f32_e32 v229, v208, v203
	v_mul_f32_e32 v230, v200, v201
	v_mov_b32_dpp v206, v125 row_ror:1 row_mask:0xf bank_mask:0xf
	v_mov_b32_e32 v200, v171
	v_mov_b32_dpp v231, v113 row_ror:15 row_mask:0xf bank_mask:0xf
	v_cndmask_b32_e64 v202, v206, 0, s[14:15]
	v_mov_b32_dpp v200, v125 row_ror:15 row_mask:0xf bank_mask:0xf
	v_cndmask_b32_e64 v201, v200, v231, s[12:13]
	v_fma_f32 v236, v141, v202, v137
	v_mov_b32_e32 v202, v125
	v_mov_b32_e32 v203, v145
	v_mov_b32_e32 v200, v133
	v_pk_mul_f32 v[200:201], v[202:203], v[200:201]
	v_mov_b32_e32 v208, v171
	v_add_f32_e32 v200, v200, v236
	v_add_f32_e32 v236, v200, v201
	v_mov_b32_dpp v208, v113 row_ror:1 row_mask:0xf bank_mask:0xf
	v_mov_b32_e32 v233, v171
	v_mul_f32_e32 v200, 0xbfb8aa3b, v236
	v_exp_f32_e32 v237, v200
	v_mov_b32_dpp v233, v97 row_ror:15 row_mask:0xf bank_mask:0xf
	v_cndmask_b32_e64 v200, v208, v206, s[14:15]
	v_cndmask_b32_e64 v201, v231, v233, s[12:13]
	v_fma_f32 v206, v141, v200, v137
	v_mov_b32_e32 v202, v113
	v_mov_b32_e32 v200, v133
	v_pk_mul_f32 v[200:201], v[202:203], v[200:201]
	v_mul_f32_e32 v227, v232, v227
	v_add_f32_e32 v200, v200, v206
	v_add_f32_e32 v206, v200, v201
	v_mul_f32_e32 v200, 0xbfb8aa3b, v206
	v_exp_f32_e32 v200, v200
	v_mov_b32_e32 v232, v171
	v_add_f32_e32 v201, 1.0, v237
	v_rcp_f32_e32 v231, v201
	v_mov_b32_dpp v232, v97 row_ror:1 row_mask:0xf bank_mask:0xf
	v_add_f32_e32 v237, 1.0, v200
	v_cndmask_b32_e64 v200, v232, v208, s[14:15]
	v_cndmask_b32_e64 v201, v233, v235, s[12:13]
	v_fma_f32 v208, v141, v200, v137
	v_mov_b32_e32 v202, v97
	v_mov_b32_e32 v200, v133
	v_pk_mul_f32 v[200:201], v[202:203], v[200:201]
	v_mov_b32_e32 v202, v145
	v_add_f32_e32 v200, v200, v208
	v_add_f32_e32 v208, v200, v201
	v_mul_f32_e32 v200, 0xbfb8aa3b, v208
	v_cndmask_b32_e64 v201, v234, v232, s[14:15]
	v_exp_f32_e32 v233, v200
	v_cndmask_b32_e64 v200, v235, 0, s[12:13]
	v_fma_f32 v232, v141, v201, v137
	v_mov_b32_e32 v203, v81
	v_mov_b32_e32 v201, v133
	v_pk_mul_f32 v[200:201], v[202:203], v[200:201]
	v_rcp_f32_e32 v202, v237
	v_add_f32_e32 v201, v201, v232
	v_add_f32_e32 v200, v200, v201
	v_mul_f32_e32 v201, 0xbfb8aa3b, v200
	v_exp_f32_e32 v201, v201
	v_add_f32_e32 v203, 1.0, v233
	v_rcp_f32_e32 v203, v203
	v_mul_f32_e32 v232, v206, v202
	v_add_f32_e32 v201, 1.0, v201
	v_rcp_f32_e32 v201, v201
	v_mul_f32_e32 v233, v208, v203
	v_mul_f32_e32 v231, v236, v231
	v_mov_b32_e32 v235, v171
	v_mul_f32_e32 v234, v200, v201
	v_cvt_pk_bf16_f32 v200, v192, v193
	v_cvt_pk_bf16_f32 v201, v197, v207
	v_mov_b64_e32 v[206:207], s[28:29]
	v_cvt_pk_bf16_f32 v202, v209, v223
	v_mad_i64_i32 v[192:193], s[0:1], v178, s93, v[206:207]
	v_lshlrev_b64 v[208:209], 1, v[180:181]
	v_lshl_add_u64 v[192:193], v[192:193], 0, v[208:209]
	v_cvt_pk_bf16_f32 v203, v227, v231
	global_store_dwordx4 v[192:193], v[200:203], off
	v_mov_b32_e32 v223, v171
	v_mov_b32_e32 v227, v171
	v_cvt_pk_bf16_f32 v200, v179, v194
	v_or_b32_e32 v179, 16, v178
	v_cvt_pk_bf16_f32 v201, v195, v205
	v_mad_i64_i32 v[194:195], s[0:1], v179, s93, v[206:207]
	v_lshl_add_u64 v[194:195], v[194:195], 0, v[208:209]
	v_cvt_pk_bf16_f32 v202, v220, v224
	v_cvt_pk_bf16_f32 v203, v228, v232
	global_store_dwordx4 v[194:195], v[200:203], off
	v_mov_b32_e32 v179, v171
	v_mov_b32_e32 v205, v171
	v_cvt_pk_bf16_f32 v200, v177, v196
	v_or_b32_e32 v177, 32, v178
	v_mad_i64_i32 v[196:197], s[0:1], v177, s93, v[206:207]
	v_lshl_add_u64 v[196:197], v[196:197], 0, v[208:209]
	v_cvt_pk_bf16_f32 v201, v199, v218
	v_cvt_pk_bf16_f32 v202, v221, v225
	v_cvt_pk_bf16_f32 v203, v229, v233
	global_store_dwordx4 v[196:197], v[200:203], off
	v_mov_b32_e32 v177, v171
	v_mov_b32_e32 v218, v171
	v_cvt_pk_bf16_f32 v200, v170, v198
	v_or_b32_e32 v170, 48, v178
	v_mad_i64_i32 v[198:199], s[0:1], v170, s93, v[206:207]
	v_mov_b32_e32 v170, v171
	v_cvt_pk_bf16_f32 v201, v204, v219
	v_lshl_add_u64 v[198:199], v[198:199], 0, v[208:209]
	v_mov_b32_e32 v204, v171
	v_mov_b32_dpp v170, v62 row_ror:1 row_mask:0xf bank_mask:0xf
	v_cvt_pk_bf16_f32 v202, v222, v226
	v_cvt_pk_bf16_f32 v203, v230, v234
	global_store_dwordx4 v[198:199], v[200:203], off
	v_mov_b32_dpp v177, v62 row_ror:15 row_mask:0xf bank_mask:0xf
	v_mov_b32_dpp v204, v54 row_ror:15 row_mask:0xf bank_mask:0xf
	v_cndmask_b32_e64 v200, v170, 0, s[14:15]
	v_cndmask_b32_e64 v201, v177, v204, s[12:13]
	v_fma_f32 v177, v146, v200, v150
	v_mov_b32_e32 v202, v62
	v_mov_b32_e32 v203, v158
	v_mov_b32_e32 v200, v154
	v_pk_mul_f32 v[200:201], v[202:203], v[200:201]
	v_mov_b32_dpp v179, v54 row_ror:1 row_mask:0xf bank_mask:0xf
; __device__ __forceinline__ float siluf(float x) { return x * __builtin_amdgcn_rcpf(1.f + __expf(-x)); }
; __device__ __forceinline__ float dpp_ror1(float v) { return __builtin_bit_cast(float, __builtin_amdgcn_update_dpp(0, __builtin_bit_cast(int, v), 0x121, 0xf, 0xf, false)); }
; __device__ __forceinline__ float dpp_ror15(float v) { return __builtin_bit_cast(float, __builtin_amdgcn_update_dpp(0, __builtin_bit_cast(int, v), 0x12F, 0xf, 0xf, false)); }
;     __device__ __forceinline__ void operator()(const f32x4 (&acc)[2][2][4][2], const pg8::Unit& u, int wr, int wc, int fr, int fq_in) const {
;     ...
;                     for (int ai = 0; ai < 2; ++ai) {
;                         f32x4 o[4][2];
; #pragma unroll
;                         for (int n = 0; n < 2; ++n)
; #pragma unroll
;                             for (int q = 0; q < 4; ++q) { float A[4], B[4];
; #pragma unroll
;                                 for (int m = 0; m < 4; ++m) { A[m] = dpp_ror1(acc[ai][bj][m][n][q]); B[m] = dpp_ror15(acc[ai][bj][m][n][q]); }
; #pragma unroll
;                                 for (int m = 0; m < 4; ++m) { const float pv = fr > 0 ? A[m] : (m > 0 ? A[m > 0 ? m - 1 : 0] : 0.f), nv = fr < 15 ? B[m] : (m < 3 ? B[m < 3 ? m + 1 : 3] : 0.f);
;                                     o[m][n][q] = siluf(bb[n][q] + w0[n][q] * pv + w1[n][q] * acc[ai][bj][m][n][q] + w2[n][q] * nv); } }
	v_add_f32_e32 v177, v200, v177
	v_add_f32_e32 v177, v177, v201
	v_mov_b32_dpp v218, v38 row_ror:15 row_mask:0xf bank_mask:0xf
	v_mul_f32_e32 v200, 0xbfb8aa3b, v177
	v_exp_f32_e32 v221, v200
	v_cndmask_b32_e64 v170, v179, v170, s[14:15]
	v_cndmask_b32_e64 v201, v204, v218, s[12:13]
	v_mov_b32_e32 v202, v54
	v_mov_b32_e32 v200, v154
	v_fma_f32 v170, v146, v170, v150
	v_pk_mul_f32 v[200:201], v[202:203], v[200:201]
	v_mov_b32_e32 v220, v171
	v_add_f32_e32 v170, v200, v170
	v_add_f32_e32 v170, v170, v201
	v_mul_f32_e32 v200, 0xbfb8aa3b, v170
	v_exp_f32_e32 v200, v200
	v_mov_b32_dpp v205, v38 row_ror:1 row_mask:0xf bank_mask:0xf
	v_mov_b32_dpp v220, v22 row_ror:15 row_mask:0xf bank_mask:0xf
	v_add_f32_e32 v201, 1.0, v221
	v_rcp_f32_e32 v204, v201
	v_add_f32_e32 v221, 1.0, v200
	v_cndmask_b32_e64 v179, v205, v179, s[14:15]
	v_cndmask_b32_e64 v201, v218, v220, s[12:13]
	v_mov_b32_e32 v202, v38
	v_mov_b32_e32 v200, v154
	v_fma_f32 v179, v146, v179, v150
	v_pk_mul_f32 v[200:201], v[202:203], v[200:201]
	v_mov_b32_e32 v219, v171
	v_add_f32_e32 v179, v200, v179
	v_add_f32_e32 v179, v179, v201
	v_mov_b32_dpp v219, v22 row_ror:1 row_mask:0xf bank_mask:0xf
	v_mul_f32_e32 v200, 0xbfb8aa3b, v179
	v_cndmask_b32_e64 v201, v219, v205, s[14:15]
	v_exp_f32_e32 v218, v200
	v_cndmask_b32_e64 v200, v220, 0, s[12:13]
	v_fma_f32 v146, v146, v201, v150
	v_mov_b32_e32 v202, v158
	v_mov_b32_e32 v203, v22
	v_mov_b32_e32 v201, v154
	v_pk_mul_f32 v[200:201], v[202:203], v[200:201]
	v_rcp_f32_e32 v154, v221
	v_add_f32_e32 v146, v201, v146
	v_add_f32_e32 v146, v200, v146
	v_mul_f32_e32 v150, 0xbfb8aa3b, v146
	v_exp_f32_e32 v150, v150
	v_add_f32_e32 v158, 1.0, v218
	v_rcp_f32_e32 v158, v158
	v_mul_f32_e32 v170, v170, v154
	v_add_f32_e32 v150, 1.0, v150
	v_rcp_f32_e32 v200, v150
	v_mov_b32_e32 v154, v171
	v_mul_f32_e32 v150, v179, v158
	v_mov_b32_e32 v158, v171
	v_mov_b32_dpp v154, v63 row_ror:1 row_mask:0xf bank_mask:0xf
	v_mov_b32_e32 v202, v171
	v_mul_f32_e32 v146, v146, v200
	v_mov_b32_dpp v158, v63 row_ror:15 row_mask:0xf bank_mask:0xf
	v_mov_b32_dpp v202, v55 row_ror:15 row_mask:0xf bank_mask:0xf
	v_cndmask_b32_e64 v200, v154, 0, s[14:15]
	v_cndmask_b32_e64 v201, v158, v202, s[12:13]
	v_fma_f32 v219, v147, v200, v151
	v_mov_b32_e32 v158, v63
	v_mov_b32_e32 v200, v155
	v_pk_mul_f32 v[200:201], v[158:159], v[200:201]
	v_mul_f32_e32 v177, v177, v204
	v_add_f32_e32 v158, v200, v219
	v_mov_b32_e32 v179, v171
	v_mov_b32_e32 v204, v171
	v_add_f32_e32 v219, v158, v201
	v_mov_b32_dpp v179, v55 row_ror:1 row_mask:0xf bank_mask:0xf
	v_mov_b32_dpp v204, v39 row_ror:15 row_mask:0xf bank_mask:0xf
	v_mul_f32_e32 v158, 0xbfb8aa3b, v219
	v_exp_f32_e32 v220, v158
	v_cndmask_b32_e64 v154, v179, v154, s[14:15]
	v_cndmask_b32_e64 v201, v202, v204, s[12:13]
	v_mov_b32_e32 v158, v55
	v_mov_b32_e32 v200, v155
	v_fma_f32 v154, v147, v154, v151
	v_pk_mul_f32 v[200:201], v[158:159], v[200:201]
	v_mov_b32_e32 v203, v171
	v_add_f32_e32 v154, v200, v154
	v_add_f32_e32 v202, v154, v201
	v_mul_f32_e32 v154, 0xbfb8aa3b, v202
	v_exp_f32_e32 v154, v154
	v_mov_b32_e32 v218, v171
	v_mov_b32_dpp v203, v39 row_ror:1 row_mask:0xf bank_mask:0xf
	v_add_f32_e32 v158, 1.0, v220
	v_mov_b32_dpp v218, v23 row_ror:15 row_mask:0xf bank_mask:0xf
	v_rcp_f32_e32 v220, v158
	v_add_f32_e32 v221, 1.0, v154
	v_cndmask_b32_e64 v154, v203, v179, s[14:15]
	v_cndmask_b32_e64 v201, v204, v218, s[12:13]
	v_mov_b32_e32 v158, v39
	v_mov_b32_e32 v200, v155
	v_fma_f32 v154, v147, v154, v151
	v_pk_mul_f32 v[200:201], v[158:159], v[200:201]
	v_mov_b32_e32 v205, v171
	v_add_f32_e32 v154, v200, v154
	v_add_f32_e32 v179, v154, v201
	v_mov_b32_dpp v205, v23 row_ror:1 row_mask:0xf bank_mask:0xf
	v_mul_f32_e32 v154, 0xbfb8aa3b, v179
	v_cndmask_b32_e64 v158, v205, v203, s[14:15]
	v_exp_f32_e32 v200, v154
	v_cndmask_b32_e64 v154, v218, 0, s[12:13]
	v_fma_f32 v147, v147, v158, v151
	v_mov_b32_e32 v158, v159
	v_mov_b32_e32 v159, v23
	v_pk_mul_f32 v[154:155], v[158:159], v[154:155]
	v_mov_b32_e32 v203, v171
	v_add_f32_e32 v147, v155, v147
	v_add_f32_e32 v147, v154, v147
	v_mul_f32_e32 v151, 0xbfb8aa3b, v147
	v_exp_f32_e32 v151, v151
	v_add_f32_e32 v155, 1.0, v200
	v_rcp_f32_e32 v158, v155
	v_rcp_f32_e32 v154, v221
	v_add_f32_e32 v151, 1.0, v151
	v_rcp_f32_e32 v159, v151
	v_mul_f32_e32 v151, v179, v158
	v_mov_b32_e32 v179, v171
	v_mov_b32_e32 v158, v171
	v_mov_b32_dpp v203, v56 row_ror:15 row_mask:0xf bank_mask:0xf
	v_mov_b32_dpp v179, v64 row_ror:1 row_mask:0xf bank_mask:0xf
	v_mov_b32_dpp v158, v64 row_ror:15 row_mask:0xf bank_mask:0xf
	v_cndmask_b32_e64 v200, v179, 0, s[14:15]
	v_mul_f32_e32 v155, v219, v220
	v_mul_f32_e32 v147, v147, v159
	v_cndmask_b32_e64 v159, v158, v203, s[12:13]
	v_fma_f32 v220, v148, v200, v152
	v_mov_b32_e32 v200, v64
	v_mov_b32_e32 v201, v160
	v_mov_b32_e32 v158, v156
	v_pk_mul_f32 v[158:159], v[200:201], v[158:159]
	v_mul_f32_e32 v154, v202, v154
	v_add_f32_e32 v158, v158, v220
	v_mov_b32_e32 v202, v171
	v_add_f32_e32 v220, v158, v159
	v_mov_b32_e32 v205, v171
	v_mov_b32_dpp v202, v56 row_ror:1 row_mask:0xf bank_mask:0xf
	v_mul_f32_e32 v158, 0xbfb8aa3b, v220
	v_mov_b32_dpp v205, v40 row_ror:15 row_mask:0xf bank_mask:0xf
	v_exp_f32_e32 v221, v158
	v_cndmask_b32_e64 v158, v202, v179, s[14:15]
	v_cndmask_b32_e64 v159, v203, v205, s[12:13]
	v_fma_f32 v179, v148, v158, v152
	v_mov_b32_e32 v200, v56
	v_mov_b32_e32 v158, v156
	v_pk_mul_f32 v[158:159], v[200:201], v[158:159]
	v_mov_b32_e32 v204, v171
	v_add_f32_e32 v158, v158, v179
	v_add_f32_e32 v179, v158, v159
	v_mul_f32_e32 v158, 0xbfb8aa3b, v179
	v_exp_f32_e32 v158, v158
	v_mov_b32_dpp v204, v40 row_ror:1 row_mask:0xf bank_mask:0xf
	v_mov_b32_e32 v219, v171
; __device__ __forceinline__ float siluf(float x) { return x * __builtin_amdgcn_rcpf(1.f + __expf(-x)); }
; __device__ __forceinline__ float dpp_ror1(float v) { return __builtin_bit_cast(float, __builtin_amdgcn_update_dpp(0, __builtin_bit_cast(int, v), 0x121, 0xf, 0xf, false)); }
; __device__ __forceinline__ float dpp_ror15(float v) { return __builtin_bit_cast(float, __builtin_amdgcn_update_dpp(0, __builtin_bit_cast(int, v), 0x12F, 0xf, 0xf, false)); }
;     __device__ __forceinline__ void operator()(const f32x4 (&acc)[2][2][4][2], const pg8::Unit& u, int wr, int wc, int fr, int fq_in) const {
;     ...
;                     for (int ai = 0; ai < 2; ++ai) {
;                         f32x4 o[4][2];
; #pragma unroll
;                         for (int n = 0; n < 2; ++n)
; #pragma unroll
;                             for (int q = 0; q < 4; ++q) { float A[4], B[4];
; #pragma unroll
;                                 for (int m = 0; m < 4; ++m) { A[m] = dpp_ror1(acc[ai][bj][m][n][q]); B[m] = dpp_ror15(acc[ai][bj][m][n][q]); }
; #pragma unroll
;                                 for (int m = 0; m < 4; ++m) { const float pv = fr > 0 ? A[m] : (m > 0 ? A[m > 0 ? m - 1 : 0] : 0.f), nv = fr < 15 ? B[m] : (m < 3 ? B[m < 3 ? m + 1 : 3] : 0.f);
;                                     o[m][n][q] = siluf(bb[n][q] + w0[n][q] * pv + w1[n][q] * acc[ai][bj][m][n][q] + w2[n][q] * nv); } }
	v_add_f32_e32 v159, 1.0, v221
	v_add_f32_e32 v221, 1.0, v158
	v_mov_b32_dpp v219, v24 row_ror:15 row_mask:0xf bank_mask:0xf
	v_cndmask_b32_e64 v158, v204, v202, s[14:15]
	v_rcp_f32_e32 v203, v159
	v_cndmask_b32_e64 v159, v205, v219, s[12:13]
	v_fma_f32 v202, v148, v158, v152
	v_mov_b32_e32 v200, v40
	v_mov_b32_e32 v158, v156
	v_pk_mul_f32 v[158:159], v[200:201], v[158:159]
	v_mov_b32_e32 v218, v171
	v_add_f32_e32 v158, v158, v202
	v_add_f32_e32 v202, v158, v159
	v_mov_b32_dpp v218, v24 row_ror:1 row_mask:0xf bank_mask:0xf
	v_mul_f32_e32 v158, 0xbfb8aa3b, v202
	v_cndmask_b32_e64 v159, v218, v204, s[14:15]
	v_exp_f32_e32 v205, v158
	v_cndmask_b32_e64 v158, v219, 0, s[12:13]
	v_fma_f32 v148, v148, v159, v152
	v_mov_b32_e32 v200, v160
	v_mov_b32_e32 v201, v24
	v_mov_b32_e32 v159, v156
	v_pk_mul_f32 v[158:159], v[200:201], v[158:159]
	v_mov_b32_e32 v201, v171
	v_add_f32_e32 v148, v159, v148
	v_add_f32_e32 v148, v158, v148
	v_mul_f32_e32 v152, 0xbfb8aa3b, v148
	v_exp_f32_e32 v152, v152
	v_add_f32_e32 v158, 1.0, v205
	v_rcp_f32_e32 v158, v158
	v_rcp_f32_e32 v156, v221
	v_add_f32_e32 v152, 1.0, v152
	v_rcp_f32_e32 v152, v152
	v_mul_f32_e32 v204, v202, v158
	v_mov_b32_dpp v201, v57 row_ror:15 row_mask:0xf bank_mask:0xf
	v_mov_b32_e32 v160, v65
	v_mul_f32_e32 v218, v148, v152
	v_mov_b32_e32 v148, v171
	v_mov_b32_e32 v152, v171
	v_mul_f32_e32 v200, v220, v203
	v_mov_b32_dpp v148, v65 row_ror:1 row_mask:0xf bank_mask:0xf
	v_mov_b32_dpp v152, v65 row_ror:15 row_mask:0xf bank_mask:0xf
	v_cndmask_b32_e64 v158, v148, 0, s[14:15]
	v_cndmask_b32_e64 v159, v152, v201, s[12:13]
	v_fma_f32 v152, v149, v158, v153
	v_mov_b32_e32 v158, v157
	v_pk_mul_f32 v[158:159], v[160:161], v[158:159]
	v_mul_f32_e32 v179, v179, v156
	v_add_f32_e32 v152, v158, v152
	v_mov_b32_e32 v156, v171
	v_mov_b32_e32 v203, v171
	v_add_f32_e32 v152, v152, v159
	v_mov_b32_dpp v156, v57 row_ror:1 row_mask:0xf bank_mask:0xf
	v_mov_b32_dpp v203, v41 row_ror:15 row_mask:0xf bank_mask:0xf
	v_mul_f32_e32 v158, 0xbfb8aa3b, v152
	v_exp_f32_e32 v220, v158
	v_cndmask_b32_e64 v148, v156, v148, s[14:15]
	v_cndmask_b32_e64 v159, v201, v203, s[12:13]
	v_mov_b32_e32 v160, v57
	v_mov_b32_e32 v158, v157
	v_fma_f32 v148, v149, v148, v153
	v_pk_mul_f32 v[158:159], v[160:161], v[158:159]
	v_mov_b32_e32 v202, v171
	v_add_f32_e32 v148, v158, v148
	v_add_f32_e32 v201, v148, v159
	v_mul_f32_e32 v148, 0xbfb8aa3b, v201
	v_exp_f32_e32 v148, v148
	v_mov_b32_e32 v219, v171
	v_mov_b32_dpp v202, v41 row_ror:1 row_mask:0xf bank_mask:0xf
	v_add_f32_e32 v158, 1.0, v220
	v_mov_b32_dpp v219, v25 row_ror:15 row_mask:0xf bank_mask:0xf
	v_rcp_f32_e32 v220, v158
	v_add_f32_e32 v221, 1.0, v148
	v_cndmask_b32_e64 v148, v202, v156, s[14:15]
	v_cndmask_b32_e64 v159, v203, v219, s[12:13]
	v_mov_b32_e32 v160, v41
	v_mov_b32_e32 v158, v157
	v_fma_f32 v148, v149, v148, v153
	v_pk_mul_f32 v[158:159], v[160:161], v[158:159]
	v_mov_b32_e32 v205, v171
	v_add_f32_e32 v148, v158, v148
	v_add_f32_e32 v158, v148, v159
	v_mov_b32_dpp v205, v25 row_ror:1 row_mask:0xf bank_mask:0xf
	v_mul_f32_e32 v148, 0xbfb8aa3b, v158
	v_exp_f32_e32 v159, v148
	v_cndmask_b32_e64 v148, v205, v202, s[14:15]
	v_cndmask_b32_e64 v156, v219, 0, s[12:13]
	v_fmac_f32_e32 v153, v149, v148
	v_mov_b32_e32 v148, v161
	v_mov_b32_e32 v149, v25
	v_pk_mul_f32 v[148:149], v[148:149], v[156:157]
	v_add_f32_e32 v156, 1.0, v159
	v_add_f32_e32 v149, v149, v153
	v_add_f32_e32 v148, v148, v149
	v_mul_f32_e32 v149, 0xbfb8aa3b, v148
	v_exp_f32_e32 v149, v149
	v_rcp_f32_e32 v153, v221
	v_rcp_f32_e32 v156, v156
	v_mov_b32_e32 v160, v171
	v_add_f32_e32 v149, 1.0, v149
	v_rcp_f32_e32 v149, v149
	v_mul_f32_e32 v159, v201, v153
	v_mul_f32_e32 v156, v158, v156
	v_mov_b32_dpp v160, v58 row_ror:1 row_mask:0xf bank_mask:0xf
	v_mul_f32_e32 v158, v148, v149
	v_mov_b32_e32 v148, v171
	v_mov_b32_e32 v201, v171
	v_mul_f32_e32 v157, v152, v220
	v_mov_b32_dpp v148, v58 row_ror:15 row_mask:0xf bank_mask:0xf
	v_mov_b32_dpp v201, v46 row_ror:15 row_mask:0xf bank_mask:0xf
	v_cndmask_b32_e64 v152, v160, 0, s[14:15]
	v_cndmask_b32_e64 v149, v148, v201, s[12:13]
	v_fma_f32 v220, v138, v152, v134
	v_mov_b32_e32 v152, v58
	v_mov_b32_e32 v153, v142
	v_mov_b32_e32 v148, v130
	v_pk_mul_f32 v[148:149], v[152:153], v[148:149]
	v_mov_b32_e32 v161, v171
	v_add_f32_e32 v148, v148, v220
	v_add_f32_e32 v220, v148, v149
	v_mov_b32_dpp v161, v46 row_ror:1 row_mask:0xf bank_mask:0xf
	v_mov_b32_e32 v203, v171
	v_mul_f32_e32 v148, 0xbfb8aa3b, v220
	v_exp_f32_e32 v221, v148
	v_mov_b32_dpp v203, v30 row_ror:15 row_mask:0xf bank_mask:0xf
	v_cndmask_b32_e64 v148, v161, v160, s[14:15]
	v_cndmask_b32_e64 v149, v201, v203, s[12:13]
	v_fma_f32 v160, v138, v148, v134
	v_mov_b32_e32 v152, v46
	v_mov_b32_e32 v148, v130
	v_pk_mul_f32 v[148:149], v[152:153], v[148:149]
	v_mov_b32_e32 v202, v171
	v_add_f32_e32 v148, v148, v160
	v_add_f32_e32 v160, v148, v149
	v_mul_f32_e32 v148, 0xbfb8aa3b, v160
	v_exp_f32_e32 v148, v148
	v_mov_b32_dpp v202, v30 row_ror:1 row_mask:0xf bank_mask:0xf
	v_mov_b32_e32 v219, v171
	v_add_f32_e32 v149, 1.0, v221
	v_add_f32_e32 v221, 1.0, v148
	v_mov_b32_dpp v219, v14 row_ror:15 row_mask:0xf bank_mask:0xf
	v_cndmask_b32_e64 v148, v202, v161, s[14:15]
	v_rcp_f32_e32 v201, v149
	v_cndmask_b32_e64 v149, v203, v219, s[12:13]
	v_fma_f32 v161, v138, v148, v134
	v_mov_b32_e32 v152, v30
	v_mov_b32_e32 v148, v130
	v_pk_mul_f32 v[148:149], v[152:153], v[148:149]
	v_mov_b32_e32 v205, v171
	v_add_f32_e32 v148, v148, v161
	v_add_f32_e32 v161, v148, v149
	v_mov_b32_dpp v205, v14 row_ror:1 row_mask:0xf bank_mask:0xf
	v_mul_f32_e32 v148, 0xbfb8aa3b, v161
	v_cndmask_b32_e64 v149, v205, v202, s[14:15]
	v_exp_f32_e32 v203, v148
; __device__ __forceinline__ float siluf(float x) { return x * __builtin_amdgcn_rcpf(1.f + __expf(-x)); }
; __device__ __forceinline__ float dpp_ror1(float v) { return __builtin_bit_cast(float, __builtin_amdgcn_update_dpp(0, __builtin_bit_cast(int, v), 0x121, 0xf, 0xf, false)); }
; __device__ __forceinline__ float dpp_ror15(float v) { return __builtin_bit_cast(float, __builtin_amdgcn_update_dpp(0, __builtin_bit_cast(int, v), 0x12F, 0xf, 0xf, false)); }
;     __device__ __forceinline__ void operator()(const f32x4 (&acc)[2][2][4][2], const pg8::Unit& u, int wr, int wc, int fr, int fq_in) const {
;     ...
;                     for (int ai = 0; ai < 2; ++ai) {
;                         f32x4 o[4][2];
; #pragma unroll
;                         for (int n = 0; n < 2; ++n)
; #pragma unroll
;                             for (int q = 0; q < 4; ++q) { float A[4], B[4];
; #pragma unroll
;                                 for (int m = 0; m < 4; ++m) { A[m] = dpp_ror1(acc[ai][bj][m][n][q]); B[m] = dpp_ror15(acc[ai][bj][m][n][q]); }
; #pragma unroll
;                                 for (int m = 0; m < 4; ++m) { const float pv = fr > 0 ? A[m] : (m > 0 ? A[m > 0 ? m - 1 : 0] : 0.f), nv = fr < 15 ? B[m] : (m < 3 ? B[m < 3 ? m + 1 : 3] : 0.f);
;                                     o[m][n][q] = siluf(bb[n][q] + w0[n][q] * pv + w1[n][q] * acc[ai][bj][m][n][q] + w2[n][q] * nv); } }
	v_cndmask_b32_e64 v148, v219, 0, s[12:13]
	v_fma_f32 v134, v138, v149, v134
	v_mov_b32_e32 v152, v142
	v_mov_b32_e32 v153, v14
	v_mov_b32_e32 v149, v130
	v_pk_mul_f32 v[148:149], v[152:153], v[148:149]
	v_rcp_f32_e32 v138, v221
	v_add_f32_e32 v130, v149, v134
	v_add_f32_e32 v130, v148, v130
	v_mul_f32_e32 v134, 0xbfb8aa3b, v130
	v_exp_f32_e32 v134, v134
	v_add_f32_e32 v142, 1.0, v203
	v_rcp_f32_e32 v142, v142
	v_mul_f32_e32 v138, v160, v138
	v_add_f32_e32 v134, 1.0, v134
	v_rcp_f32_e32 v134, v134
	v_mul_f32_e32 v152, v220, v201
	v_mov_b32_e32 v201, v171
	v_mul_f32_e32 v153, v161, v142
	v_mul_f32_e32 v160, v130, v134
	v_mov_b32_e32 v130, v171
	v_mov_b32_e32 v134, v171
	v_mov_b32_dpp v201, v47 row_ror:15 row_mask:0xf bank_mask:0xf
	v_mov_b32_dpp v130, v59 row_ror:1 row_mask:0xf bank_mask:0xf
	v_mov_b32_dpp v134, v59 row_ror:15 row_mask:0xf bank_mask:0xf
	v_cndmask_b32_e64 v142, v130, 0, s[14:15]
	v_cndmask_b32_e64 v149, v134, v201, s[12:13]
	v_fma_f32 v134, v139, v142, v135
	v_mov_b32_e32 v142, v59
	v_mov_b32_e32 v148, v131
	v_mov_b32_e32 v161, v171
	v_mov_b32_e32 v203, v171
	v_pk_mul_f32 v[148:149], v[142:143], v[148:149]
	v_mov_b32_dpp v161, v47 row_ror:1 row_mask:0xf bank_mask:0xf
	v_mov_b32_dpp v203, v31 row_ror:15 row_mask:0xf bank_mask:0xf
	v_add_f32_e32 v134, v148, v134
	v_add_f32_e32 v220, v134, v149
	v_cndmask_b32_e64 v130, v161, v130, s[14:15]
	v_cndmask_b32_e64 v149, v201, v203, s[12:13]
	v_mov_b32_e32 v142, v47
	v_mov_b32_e32 v148, v131
	v_fma_f32 v130, v139, v130, v135
	v_pk_mul_f32 v[148:149], v[142:143], v[148:149]
	v_mov_b32_e32 v202, v171
	v_add_f32_e32 v130, v148, v130
	v_add_f32_e32 v201, v130, v149
	v_mul_f32_e32 v130, 0xbfb8aa3b, v201
	v_exp_f32_e32 v130, v130
	v_mov_b32_e32 v219, v171
	v_mul_f32_e32 v134, 0xbfb8aa3b, v220
	v_mov_b32_dpp v202, v31 row_ror:1 row_mask:0xf bank_mask:0xf
	v_exp_f32_e32 v134, v134
	v_mov_b32_dpp v219, v15 row_ror:15 row_mask:0xf bank_mask:0xf
	v_add_f32_e32 v222, 1.0, v130
	v_cndmask_b32_e64 v130, v202, v161, s[14:15]
	v_cndmask_b32_e64 v149, v203, v219, s[12:13]
	v_mov_b32_e32 v142, v31
	v_mov_b32_e32 v148, v131
	v_fma_f32 v130, v139, v130, v135
	v_pk_mul_f32 v[148:149], v[142:143], v[148:149]
	v_mov_b32_e32 v205, v171
	v_add_f32_e32 v130, v148, v130
	v_add_f32_e32 v134, 1.0, v134
	v_mov_b32_dpp v205, v15 row_ror:1 row_mask:0xf bank_mask:0xf
	v_add_f32_e32 v142, v130, v149
	v_rcp_f32_e32 v221, v134
	v_mul_f32_e32 v130, 0xbfb8aa3b, v142
	v_cndmask_b32_e64 v134, v205, v202, s[14:15]
	v_exp_f32_e32 v148, v130
	v_cndmask_b32_e64 v130, v219, 0, s[12:13]
	v_fma_f32 v139, v139, v134, v135
	v_mov_b32_e32 v134, v143
	v_mov_b32_e32 v135, v15
	v_pk_mul_f32 v[130:131], v[134:135], v[130:131]
	v_rcp_f32_e32 v134, v222
	v_add_f32_e32 v131, v131, v139
	v_add_f32_e32 v130, v130, v131
	v_mul_f32_e32 v131, 0xbfb8aa3b, v130
	v_exp_f32_e32 v131, v131
	v_add_f32_e32 v135, 1.0, v148
	v_rcp_f32_e32 v135, v135
	v_mov_b32_e32 v149, v171
	v_add_f32_e32 v131, 1.0, v131
	v_rcp_f32_e32 v131, v131
	v_mul_f32_e32 v143, v201, v134
	v_mov_b32_dpp v149, v60 row_ror:1 row_mask:0xf bank_mask:0xf
	v_mov_b32_e32 v201, v171
	v_mul_f32_e32 v148, v130, v131
	v_mov_b32_e32 v130, v171
	v_mov_b32_dpp v201, v48 row_ror:15 row_mask:0xf bank_mask:0xf
	v_cndmask_b32_e64 v134, v149, 0, s[14:15]
	v_mov_b32_dpp v130, v60 row_ror:15 row_mask:0xf bank_mask:0xf
	v_mul_f32_e32 v139, v220, v221
	v_mul_f32_e32 v142, v142, v135
	v_cndmask_b32_e64 v131, v130, v201, s[12:13]
	v_fma_f32 v220, v140, v134, v136
	v_mov_b32_e32 v134, v60
	v_mov_b32_e32 v135, v144
	v_mov_b32_e32 v130, v132
	v_pk_mul_f32 v[130:131], v[134:135], v[130:131]
	v_mov_b32_e32 v161, v171
	v_add_f32_e32 v130, v130, v220
	v_add_f32_e32 v220, v130, v131
	v_mov_b32_dpp v161, v48 row_ror:1 row_mask:0xf bank_mask:0xf
	v_mov_b32_e32 v203, v171
	v_mul_f32_e32 v130, 0xbfb8aa3b, v220
	v_exp_f32_e32 v221, v130
	v_mov_b32_dpp v203, v32 row_ror:15 row_mask:0xf bank_mask:0xf
	v_cndmask_b32_e64 v130, v161, v149, s[14:15]
	v_cndmask_b32_e64 v131, v201, v203, s[12:13]
	v_fma_f32 v149, v140, v130, v136
	v_mov_b32_e32 v134, v48
	v_mov_b32_e32 v130, v132
	v_pk_mul_f32 v[130:131], v[134:135], v[130:131]
	v_mov_b32_e32 v202, v171
	v_add_f32_e32 v130, v130, v149
	v_add_f32_e32 v149, v130, v131
	v_mul_f32_e32 v130, 0xbfb8aa3b, v149
	v_exp_f32_e32 v130, v130
	v_mov_b32_dpp v202, v32 row_ror:1 row_mask:0xf bank_mask:0xf
	v_mov_b32_e32 v219, v171
	v_add_f32_e32 v131, 1.0, v221
	v_add_f32_e32 v221, 1.0, v130
	v_mov_b32_dpp v219, v16 row_ror:15 row_mask:0xf bank_mask:0xf
	v_cndmask_b32_e64 v130, v202, v161, s[14:15]
	v_rcp_f32_e32 v201, v131
	v_cndmask_b32_e64 v131, v203, v219, s[12:13]
	v_fma_f32 v161, v140, v130, v136
	v_mov_b32_e32 v134, v32
	v_mov_b32_e32 v130, v132
	v_pk_mul_f32 v[130:131], v[134:135], v[130:131]
	v_mov_b32_e32 v205, v171
	v_add_f32_e32 v130, v130, v161
	v_add_f32_e32 v161, v130, v131
	v_mov_b32_dpp v205, v16 row_ror:1 row_mask:0xf bank_mask:0xf
	v_mul_f32_e32 v130, 0xbfb8aa3b, v161
	v_cndmask_b32_e64 v131, v205, v202, s[14:15]
	v_exp_f32_e32 v203, v130
	v_cndmask_b32_e64 v130, v219, 0, s[12:13]
	v_fma_f32 v136, v140, v131, v136
	v_mov_b32_e32 v134, v144
	v_mov_b32_e32 v135, v16
	v_mov_b32_e32 v131, v132
	v_pk_mul_f32 v[130:131], v[134:135], v[130:131]
	v_rcp_f32_e32 v132, v221
	v_add_f32_e32 v131, v131, v136
	v_add_f32_e32 v130, v130, v131
	v_mul_f32_e32 v131, 0xbfb8aa3b, v130
	v_exp_f32_e32 v131, v131
	v_add_f32_e32 v134, 1.0, v203
	v_rcp_f32_e32 v134, v134
	v_mul_f32_e32 v136, v149, v132
	v_add_f32_e32 v131, 1.0, v131
	v_rcp_f32_e32 v131, v131
	v_mov_b32_e32 v132, v171
	v_mul_f32_e32 v140, v161, v134
	v_mov_b32_e32 v161, v171
	v_mul_f32_e32 v149, v130, v131
; __device__ __forceinline__ unsigned cvt_pk_bf16(float lo, float hi) { unsigned r; asm volatile("v_cvt_pk_bf16_f32 %0, %1, %2" : "=v"(r) : "v"(lo), "v"(hi)); return r; }
; __device__ __forceinline__ float siluf(float x) { return x * __builtin_amdgcn_rcpf(1.f + __expf(-x)); }
; __device__ __forceinline__ float dpp_ror1(float v) { return __builtin_bit_cast(float, __builtin_amdgcn_update_dpp(0, __builtin_bit_cast(int, v), 0x121, 0xf, 0xf, false)); }
; __device__ __forceinline__ float dpp_ror15(float v) { return __builtin_bit_cast(float, __builtin_amdgcn_update_dpp(0, __builtin_bit_cast(int, v), 0x12F, 0xf, 0xf, false)); }
;     __device__ __forceinline__ void operator()(const f32x4 (&acc)[2][2][4][2], const pg8::Unit& u, int wr, int wc, int fr, int fq_in) const {
;     ...
;                     for (int ai = 0; ai < 2; ++ai) {
;                         f32x4 o[4][2];
; #pragma unroll
;                         for (int n = 0; n < 2; ++n)
; #pragma unroll
;                             for (int q = 0; q < 4; ++q) { float A[4], B[4];
; #pragma unroll
;                                 for (int m = 0; m < 4; ++m) { A[m] = dpp_ror1(acc[ai][bj][m][n][q]); B[m] = dpp_ror15(acc[ai][bj][m][n][q]); }
; #pragma unroll
;                                 for (int m = 0; m < 4; ++m) { const float pv = fr > 0 ? A[m] : (m > 0 ? A[m > 0 ? m - 1 : 0] : 0.f), nv = fr < 15 ? B[m] : (m < 3 ? B[m < 3 ? m + 1 : 3] : 0.f);
;                                     o[m][n][q] = siluf(bb[n][q] + w0[n][q] * pv + w1[n][q] * acc[ai][bj][m][n][q] + w2[n][q] * nv); } }
; #pragma unroll
;                         for (int m = 0; m < 4; ++m) { u32x4 w; w.x = pg8::cvt_pk_bf16(o[m][0][0], o[m][0][1]); w.y = pg8::cvt_pk_bf16(o[m][0][2], o[m][0][3]); w.z = pg8::cvt_pk_bf16(o[m][1][0], o[m][1][1]); w.w = pg8::cvt_pk_bf16(o[m][1][2], o[m][1][3]);
;                             *(u32x4*)(XBC + (size_t)(row0 + ai * 128 + m * 16) * XBCW + col) = w; }
	v_mov_b32_dpp v132, v61 row_ror:1 row_mask:0xf bank_mask:0xf
	v_mov_b32_e32 v130, v171
	v_mov_b32_dpp v161, v49 row_ror:15 row_mask:0xf bank_mask:0xf
	v_cndmask_b32_e64 v144, v132, 0, s[14:15]
	v_mov_b32_dpp v130, v61 row_ror:15 row_mask:0xf bank_mask:0xf
	v_cndmask_b32_e64 v131, v130, v161, s[12:13]
	v_fma_f32 v219, v141, v144, v137
	v_mov_b32_e32 v144, v61
	v_mov_b32_e32 v130, v133
	v_pk_mul_f32 v[130:131], v[144:145], v[130:131]
	v_mov_b32_e32 v134, v171
	v_add_f32_e32 v130, v130, v219
	v_add_f32_e32 v219, v130, v131
	v_mov_b32_dpp v134, v49 row_ror:1 row_mask:0xf bank_mask:0xf
	v_mov_b32_e32 v202, v171
	v_mul_f32_e32 v130, 0xbfb8aa3b, v219
	v_mul_f32_e32 v135, v220, v201
	v_mov_b32_dpp v202, v33 row_ror:15 row_mask:0xf bank_mask:0xf
	v_exp_f32_e32 v220, v130
	v_cndmask_b32_e64 v130, v134, v132, s[14:15]
	v_cndmask_b32_e64 v131, v161, v202, s[12:13]
	v_fma_f32 v132, v141, v130, v137
	v_mov_b32_e32 v144, v49
	v_mov_b32_e32 v130, v133
	v_pk_mul_f32 v[130:131], v[144:145], v[130:131]
	v_mov_b32_e32 v201, v171
	v_add_f32_e32 v130, v130, v132
	v_add_f32_e32 v161, v130, v131
	v_mul_f32_e32 v130, 0xbfb8aa3b, v161
	v_exp_f32_e32 v130, v130
	v_mov_b32_dpp v201, v33 row_ror:1 row_mask:0xf bank_mask:0xf
	v_mov_b32_e32 v205, v171
	v_add_f32_e32 v131, 1.0, v220
	v_add_f32_e32 v221, 1.0, v130
	v_mov_b32_dpp v205, v17 row_ror:15 row_mask:0xf bank_mask:0xf
	v_cndmask_b32_e64 v130, v201, v134, s[14:15]
	v_rcp_f32_e32 v220, v131
	v_cndmask_b32_e64 v131, v202, v205, s[12:13]
	v_fma_f32 v132, v141, v130, v137
	v_mov_b32_e32 v144, v33
	v_mov_b32_e32 v130, v133
	v_pk_mul_f32 v[130:131], v[144:145], v[130:131]
	v_mov_b32_e32 v203, v171
	v_add_f32_e32 v130, v130, v132
	v_add_f32_e32 v134, v130, v131
	v_mov_b32_dpp v203, v17 row_ror:1 row_mask:0xf bank_mask:0xf
	v_mul_f32_e32 v130, 0xbfb8aa3b, v134
	v_exp_f32_e32 v144, v130
	v_cndmask_b32_e64 v130, v203, v201, s[14:15]
	v_cndmask_b32_e64 v132, v205, 0, s[12:13]
	v_fmac_f32_e32 v137, v141, v130
	v_mov_b32_e32 v130, v145
	v_mov_b32_e32 v131, v17
	v_pk_mul_f32 v[130:131], v[130:131], v[132:133]
	v_add_f32_e32 v133, 1.0, v144
	v_add_f32_e32 v131, v131, v137
	v_add_f32_e32 v130, v130, v131
	v_mul_f32_e32 v131, 0xbfb8aa3b, v130
	v_exp_f32_e32 v131, v131
	v_rcp_f32_e32 v133, v133
	v_rcp_f32_e32 v132, v221
	v_mul_f32_e32 v137, v219, v220
	v_add_f32_e32 v131, 1.0, v131
	v_rcp_f32_e32 v131, v131
	v_mul_f32_e32 v144, v134, v133
	v_add_u32_e32 v134, 0x80, v178
	v_mul_f32_e32 v141, v161, v132
	v_mul_f32_e32 v145, v130, v131
	v_cvt_pk_bf16_f32 v130, v177, v155
	v_cvt_pk_bf16_f32 v131, v200, v157
	v_cvt_pk_bf16_f32 v132, v152, v139
	v_cvt_pk_bf16_f32 v133, v135, v137
	v_mad_i64_i32 v[134:135], s[0:1], v134, s93, v[206:207]
	v_lshl_add_u64 v[200:201], v[134:135], 0, v[208:209]
	v_add_u32_e32 v134, 0x90, v178
	v_mad_i64_i32 v[134:135], s[0:1], v134, s93, v[206:207]
	v_lshl_add_u64 v[202:203], v[134:135], 0, v[208:209]
	v_add_u32_e32 v134, 0xa0, v178
	global_store_dwordx4 v[200:201], v[130:133], off
	v_mad_i64_i32 v[134:135], s[0:1], v134, s93, v[206:207]
	s_nop 0
	v_cvt_pk_bf16_f32 v130, v170, v154
	v_cvt_pk_bf16_f32 v131, v179, v159
	v_cvt_pk_bf16_f32 v132, v138, v143
	v_cvt_pk_bf16_f32 v133, v136, v141
	global_store_dwordx4 v[202:203], v[130:133], off
	v_mov_b32_e32 v170, v171
	v_mov_b32_e32 v177, v171
	v_cvt_pk_bf16_f32 v130, v150, v151
	v_cvt_pk_bf16_f32 v131, v204, v156
	v_lshl_add_u64 v[204:205], v[134:135], 0, v[208:209]
	v_add_u32_e32 v134, 0xb0, v178
	v_mad_i64_i32 v[134:135], s[0:1], v134, s93, v[206:207]
	v_cvt_pk_bf16_f32 v132, v153, v142
	v_cvt_pk_bf16_f32 v133, v140, v144
	v_lshl_add_u64 v[206:207], v[134:135], 0, v[208:209]
	global_store_dwordx4 v[204:205], v[130:133], off
	v_mov_b32_dpp v170, v114 row_ror:1 row_mask:0xf bank_mask:0xf
	v_mov_b32_dpp v177, v114 row_ror:15 row_mask:0xf bank_mask:0xf
	v_cvt_pk_bf16_f32 v130, v146, v147
	v_cvt_pk_bf16_f32 v131, v218, v158
	v_cvt_pk_bf16_f32 v132, v160, v148
	v_cvt_pk_bf16_f32 v133, v149, v145
	global_store_dwordx4 v[206:207], v[130:133], off
	global_load_dwordx4 v[146:149], v[182:183], off offset:512
	global_load_dwordx4 v[150:153], v[190:191], off offset:512
	global_load_dwordx4 v[158:161], v[188:189], off offset:512
	global_load_dwordx4 v[154:157], v[184:185], off offset:512
	global_load_dwordx4 v[138:141], v[182:183], off offset:528
	global_load_dwordx4 v[130:133], v[184:185], off offset:528
	global_load_dwordx4 v[142:145], v[188:189], off offset:528
	global_load_dwordx4 v[134:137], v[190:191], off offset:528
	v_mov_b32_e32 v188, v171
	v_cndmask_b32_e64 v182, v170, 0, s[14:15]
	v_mov_b32_e32 v184, v114
	v_mov_b32_dpp v188, v98 row_ror:15 row_mask:0xf bank_mask:0xf
	v_cndmask_b32_e64 v183, v177, v188, s[12:13]
	v_mov_b32_e32 v179, v171
	v_mov_b32_e32 v190, v171
	v_mov_b32_e32 v189, v171
	v_mov_b32_dpp v179, v98 row_ror:1 row_mask:0xf bank_mask:0xf
	v_mov_b32_dpp v190, v82 row_ror:15 row_mask:0xf bank_mask:0xf
	v_cndmask_b32_e64 v170, v179, v170, s[14:15]
	v_mov_b32_e32 v208, v171
	v_mov_b32_dpp v189, v82 row_ror:1 row_mask:0xf bank_mask:0xf
	v_cndmask_b32_e64 v179, v189, v179, s[14:15]
	v_mov_b32_dpp v208, v70 row_ror:15 row_mask:0xf bank_mask:0xf
	v_mov_b32_e32 v191, v171
	v_mov_b32_e32 v219, v171
	v_mov_b32_e32 v218, v171
	v_mov_b32_dpp v191, v70 row_ror:1 row_mask:0xf bank_mask:0xf
	v_mov_b32_dpp v219, v71 row_ror:15 row_mask:0xf bank_mask:0xf
	v_mov_b32_dpp v218, v71 row_ror:1 row_mask:0xf bank_mask:0xf
	v_mov_b32_dpp v223, v72 row_ror:15 row_mask:0xf bank_mask:0xf
	v_mov_b32_e32 v222, v171
	v_mov_b32_dpp v227, v73 row_ror:15 row_mask:0xf bank_mask:0xf
	v_mov_b32_e32 v226, v171
	v_mov_b32_dpp v222, v72 row_ror:1 row_mask:0xf bank_mask:0xf
	v_mov_b32_e32 v231, v171
	v_mov_b32_dpp v226, v73 row_ror:1 row_mask:0xf bank_mask:0xf
	v_mov_b32_e32 v230, v171
	v_mov_b32_dpp v231, v66 row_ror:15 row_mask:0xf bank_mask:0xf
	v_mov_b32_dpp v235, v67 row_ror:15 row_mask:0xf bank_mask:0xf
	v_mov_b32_dpp v230, v66 row_ror:1 row_mask:0xf bank_mask:0xf
	v_mov_b32_e32 v234, v171
	v_mov_b32_dpp v243, v69 row_ror:15 row_mask:0xf bank_mask:0xf
	v_mov_b32_dpp v242, v69 row_ror:1 row_mask:0xf bank_mask:0xf
	v_mov_b32_dpp v234, v67 row_ror:1 row_mask:0xf bank_mask:0xf
	s_mov_b64 s[0:1], 0
	s_waitcnt vmcnt(6)
; __device__ __forceinline__ float siluf(float x) { return x * __builtin_amdgcn_rcpf(1.f + __expf(-x)); }
; __device__ __forceinline__ float dpp_ror1(float v) { return __builtin_bit_cast(float, __builtin_amdgcn_update_dpp(0, __builtin_bit_cast(int, v), 0x121, 0xf, 0xf, false)); }
; __device__ __forceinline__ float dpp_ror15(float v) { return __builtin_bit_cast(float, __builtin_amdgcn_update_dpp(0, __builtin_bit_cast(int, v), 0x12F, 0xf, 0xf, false)); }
;     __device__ __forceinline__ void operator()(const f32x4 (&acc)[2][2][4][2], const pg8::Unit& u, int wr, int wc, int fr, int fq_in) const {
;     ...
;                     for (int ai = 0; ai < 2; ++ai) {
;                         f32x4 o[4][2];
; #pragma unroll
;                         for (int n = 0; n < 2; ++n)
; #pragma unroll
;                             for (int q = 0; q < 4; ++q) { float A[4], B[4];
; #pragma unroll
;                                 for (int m = 0; m < 4; ++m) { A[m] = dpp_ror1(acc[ai][bj][m][n][q]); B[m] = dpp_ror15(acc[ai][bj][m][n][q]); }
; #pragma unroll
;                                 for (int m = 0; m < 4; ++m) { const float pv = fr > 0 ? A[m] : (m > 0 ? A[m > 0 ? m - 1 : 0] : 0.f), nv = fr < 15 ? B[m] : (m < 3 ? B[m < 3 ? m + 1 : 3] : 0.f);
;                                     o[m][n][q] = siluf(bb[n][q] + w0[n][q] * pv + w1[n][q] * acc[ai][bj][m][n][q] + w2[n][q] * nv); } }
	v_fma_f32 v177, v146, v182, v150
	s_waitcnt vmcnt(5)
	v_mov_b32_e32 v185, v158
	s_waitcnt vmcnt(4)
	v_mov_b32_e32 v182, v154
	v_pk_mul_f32 v[182:183], v[184:185], v[182:183]
	v_mov_b32_e32 v184, v98
	v_add_f32_e32 v177, v182, v177
	v_add_f32_e32 v177, v177, v183
	v_mul_f32_e32 v182, 0xbfb8aa3b, v177
	v_exp_f32_e32 v209, v182
	v_cndmask_b32_e64 v183, v188, v190, s[12:13]
	v_mov_b32_e32 v182, v154
	v_fma_f32 v170, v146, v170, v150
	v_pk_mul_f32 v[182:183], v[184:185], v[182:183]
	v_mov_b32_e32 v184, v82
	v_add_f32_e32 v170, v182, v170
	v_add_f32_e32 v170, v170, v183
	v_mul_f32_e32 v182, 0xbfb8aa3b, v170
	v_exp_f32_e32 v182, v182
	v_add_f32_e32 v183, 1.0, v209
	v_rcp_f32_e32 v188, v183
	v_cndmask_b32_e64 v183, v190, v208, s[12:13]
	v_add_f32_e32 v209, 1.0, v182
	v_mov_b32_e32 v182, v154
	v_fma_f32 v179, v146, v179, v150
	v_pk_mul_f32 v[182:183], v[184:185], v[182:183]
	v_mov_b32_e32 v184, v158
	v_add_f32_e32 v179, v182, v179
	v_add_f32_e32 v190, v179, v183
	v_cndmask_b32_e64 v183, v191, v189, s[14:15]
	v_cndmask_b32_e64 v182, v208, 0, s[12:13]
	v_fma_f32 v189, v146, v183, v150
	v_mov_b32_e32 v185, v70
	v_mov_b32_e32 v183, v154
	v_pk_mul_f32 v[182:183], v[184:185], v[182:183]
	v_mul_f32_e32 v179, 0xbfb8aa3b, v190
	v_add_f32_e32 v183, v183, v189
	v_add_f32_e32 v183, v182, v183
	v_exp_f32_e32 v179, v179
	v_mul_f32_e32 v182, 0xbfb8aa3b, v183
	v_exp_f32_e32 v182, v182
	v_rcp_f32_e32 v184, v209
	v_add_f32_e32 v179, 1.0, v179
	v_rcp_f32_e32 v185, v179
	v_add_f32_e32 v179, 1.0, v182
	v_rcp_f32_e32 v189, v179
	v_mul_f32_e32 v179, v170, v184
	v_mov_b32_e32 v184, v171
	v_mov_b32_e32 v191, v171
	v_mul_f32_e32 v170, v183, v189
	v_mov_b32_e32 v183, v171
	v_mul_f32_e32 v182, v177, v188
	v_mov_b32_dpp v184, v115 row_ror:15 row_mask:0xf bank_mask:0xf
	v_mov_b32_dpp v183, v115 row_ror:1 row_mask:0xf bank_mask:0xf
	v_mov_b32_dpp v191, v99 row_ror:15 row_mask:0xf bank_mask:0xf
	v_cndmask_b32_e64 v188, v183, 0, s[14:15]
	v_mul_f32_e32 v177, v190, v185
	v_cndmask_b32_e64 v185, v184, v191, s[12:13]
	v_fma_f32 v220, v147, v188, v151
	v_mov_b32_e32 v188, v115
	v_mov_b32_e32 v189, v159
	v_mov_b32_e32 v184, v155
	v_pk_mul_f32 v[184:185], v[188:189], v[184:185]
	v_mov_b32_e32 v190, v171
	v_add_f32_e32 v184, v184, v220
	v_mov_b32_e32 v209, v171
	v_add_f32_e32 v220, v184, v185
	v_mov_b32_dpp v190, v99 row_ror:1 row_mask:0xf bank_mask:0xf
	v_mov_b32_dpp v209, v83 row_ror:15 row_mask:0xf bank_mask:0xf
	v_mul_f32_e32 v184, 0xbfb8aa3b, v220
	v_exp_f32_e32 v221, v184
	v_cndmask_b32_e64 v183, v190, v183, s[14:15]
	v_cndmask_b32_e64 v185, v191, v209, s[12:13]
	v_mov_b32_e32 v188, v99
	v_mov_b32_e32 v184, v155
	v_fma_f32 v183, v147, v183, v151
	v_pk_mul_f32 v[184:185], v[188:189], v[184:185]
	v_mov_b32_e32 v208, v171
	v_add_f32_e32 v183, v184, v183
	v_add_f32_e32 v183, v183, v185
	v_mul_f32_e32 v184, 0xbfb8aa3b, v183
	v_exp_f32_e32 v184, v184
	v_mov_b32_dpp v208, v83 row_ror:1 row_mask:0xf bank_mask:0xf
	v_add_f32_e32 v185, 1.0, v221
	v_rcp_f32_e32 v191, v185
	v_add_f32_e32 v221, 1.0, v184
	v_cndmask_b32_e64 v184, v208, v190, s[14:15]
	v_cndmask_b32_e64 v185, v209, v219, s[12:13]
	v_fma_f32 v190, v147, v184, v151
	v_mov_b32_e32 v188, v83
	v_mov_b32_e32 v184, v155
	v_pk_mul_f32 v[184:185], v[188:189], v[184:185]
	v_mov_b32_e32 v188, v159
	v_add_f32_e32 v184, v184, v190
	v_add_f32_e32 v190, v184, v185
	v_mul_f32_e32 v184, 0xbfb8aa3b, v190
	v_cndmask_b32_e64 v185, v218, v208, s[14:15]
	v_exp_f32_e32 v209, v184
	v_cndmask_b32_e64 v184, v219, 0, s[12:13]
	v_fma_f32 v208, v147, v185, v151
	v_mov_b32_e32 v189, v71
	v_mov_b32_e32 v185, v155
	v_pk_mul_f32 v[184:185], v[188:189], v[184:185]
	v_add_f32_e32 v188, 1.0, v209
	v_add_f32_e32 v185, v185, v208
	v_add_f32_e32 v189, v184, v185
	v_mul_f32_e32 v184, 0xbfb8aa3b, v189
	v_exp_f32_e32 v184, v184
	v_rcp_f32_e32 v185, v221
	v_rcp_f32_e32 v208, v188
	v_mov_b32_e32 v219, v171
	v_add_f32_e32 v184, 1.0, v184
	v_rcp_f32_e32 v209, v184
	v_mul_f32_e32 v185, v183, v185
	v_mul_f32_e32 v184, v190, v208
	v_mov_b32_e32 v190, v171
	v_mul_f32_e32 v183, v189, v209
	v_mov_b32_e32 v189, v171
	v_mov_b32_dpp v190, v116 row_ror:15 row_mask:0xf bank_mask:0xf
	v_mov_b32_dpp v219, v100 row_ror:15 row_mask:0xf bank_mask:0xf
	v_mov_b32_dpp v189, v116 row_ror:1 row_mask:0xf bank_mask:0xf
	v_cndmask_b32_e64 v208, v189, 0, s[14:15]
	v_mul_f32_e32 v188, v220, v191
	v_cndmask_b32_e64 v191, v190, v219, s[12:13]
	v_fma_f32 v224, v148, v208, v152
	v_mov_b32_e32 v208, v116
	v_mov_b32_e32 v209, v160
	v_mov_b32_e32 v190, v156
	v_pk_mul_f32 v[190:191], v[208:209], v[190:191]
	v_mov_b32_e32 v218, v171
	v_add_f32_e32 v190, v190, v224
	v_mov_b32_e32 v221, v171
	v_add_f32_e32 v224, v190, v191
	v_mov_b32_dpp v218, v100 row_ror:1 row_mask:0xf bank_mask:0xf
	v_mov_b32_dpp v221, v84 row_ror:15 row_mask:0xf bank_mask:0xf
	v_mul_f32_e32 v190, 0xbfb8aa3b, v224
	v_exp_f32_e32 v225, v190
	v_cndmask_b32_e64 v189, v218, v189, s[14:15]
	v_cndmask_b32_e64 v191, v219, v221, s[12:13]
	v_mov_b32_e32 v208, v100
	v_mov_b32_e32 v190, v156
	v_fma_f32 v189, v148, v189, v152
	v_pk_mul_f32 v[190:191], v[208:209], v[190:191]
	v_mov_b32_e32 v220, v171
	v_add_f32_e32 v189, v190, v189
	v_add_f32_e32 v189, v189, v191
	v_mul_f32_e32 v190, 0xbfb8aa3b, v189
	v_exp_f32_e32 v190, v190
	v_mov_b32_dpp v220, v84 row_ror:1 row_mask:0xf bank_mask:0xf
	v_add_f32_e32 v191, 1.0, v225
	v_rcp_f32_e32 v219, v191
	v_add_f32_e32 v225, 1.0, v190
	v_cndmask_b32_e64 v190, v220, v218, s[14:15]
	v_cndmask_b32_e64 v191, v221, v223, s[12:13]
	v_fma_f32 v218, v148, v190, v152
	v_mov_b32_e32 v208, v84
	v_mov_b32_e32 v190, v156
	v_pk_mul_f32 v[190:191], v[208:209], v[190:191]
	v_mov_b32_e32 v208, v160
	v_add_f32_e32 v190, v190, v218
; __device__ __forceinline__ float siluf(float x) { return x * __builtin_amdgcn_rcpf(1.f + __expf(-x)); }
; __device__ __forceinline__ float dpp_ror1(float v) { return __builtin_bit_cast(float, __builtin_amdgcn_update_dpp(0, __builtin_bit_cast(int, v), 0x121, 0xf, 0xf, false)); }
; __device__ __forceinline__ float dpp_ror15(float v) { return __builtin_bit_cast(float, __builtin_amdgcn_update_dpp(0, __builtin_bit_cast(int, v), 0x12F, 0xf, 0xf, false)); }
;     __device__ __forceinline__ void operator()(const f32x4 (&acc)[2][2][4][2], const pg8::Unit& u, int wr, int wc, int fr, int fq_in) const {
;     ...
;                     for (int ai = 0; ai < 2; ++ai) {
;                         f32x4 o[4][2];
; #pragma unroll
;                         for (int n = 0; n < 2; ++n)
; #pragma unroll
;                             for (int q = 0; q < 4; ++q) { float A[4], B[4];
; #pragma unroll
;                                 for (int m = 0; m < 4; ++m) { A[m] = dpp_ror1(acc[ai][bj][m][n][q]); B[m] = dpp_ror15(acc[ai][bj][m][n][q]); }
; #pragma unroll
;                                 for (int m = 0; m < 4; ++m) { const float pv = fr > 0 ? A[m] : (m > 0 ? A[m > 0 ? m - 1 : 0] : 0.f), nv = fr < 15 ? B[m] : (m < 3 ? B[m < 3 ? m + 1 : 3] : 0.f);
;                                     o[m][n][q] = siluf(bb[n][q] + w0[n][q] * pv + w1[n][q] * acc[ai][bj][m][n][q] + w2[n][q] * nv); } }
	v_add_f32_e32 v218, v190, v191
	v_mul_f32_e32 v190, 0xbfb8aa3b, v218
	v_cndmask_b32_e64 v191, v222, v220, s[14:15]
	v_exp_f32_e32 v221, v190
	v_cndmask_b32_e64 v190, v223, 0, s[12:13]
	v_fma_f32 v220, v148, v191, v152
	v_mov_b32_e32 v209, v72
	v_mov_b32_e32 v191, v156
	v_pk_mul_f32 v[190:191], v[208:209], v[190:191]
	v_rcp_f32_e32 v208, v225
	v_add_f32_e32 v191, v191, v220
	v_add_f32_e32 v190, v190, v191
	v_mul_f32_e32 v191, 0xbfb8aa3b, v190
	v_exp_f32_e32 v191, v191
	v_add_f32_e32 v209, 1.0, v221
	v_rcp_f32_e32 v209, v209
	v_mul_f32_e32 v220, v189, v208
	v_add_f32_e32 v191, 1.0, v191
	v_rcp_f32_e32 v191, v191
	v_mov_b32_e32 v189, v171
	v_mov_b32_e32 v223, v171
	v_mul_f32_e32 v218, v218, v209
	v_mul_f32_e32 v221, v190, v191
	v_mov_b32_dpp v189, v117 row_ror:1 row_mask:0xf bank_mask:0xf
	v_mov_b32_e32 v190, v171
	v_mov_b32_dpp v223, v101 row_ror:15 row_mask:0xf bank_mask:0xf
	v_cndmask_b32_e64 v208, v189, 0, s[14:15]
	v_mov_b32_dpp v190, v117 row_ror:15 row_mask:0xf bank_mask:0xf
	v_cndmask_b32_e64 v191, v190, v223, s[12:13]
	v_fma_f32 v228, v149, v208, v153
	v_mov_b32_e32 v208, v117
	v_mov_b32_e32 v209, v161
	v_mov_b32_e32 v190, v157
	v_pk_mul_f32 v[190:191], v[208:209], v[190:191]
	v_mov_b32_e32 v222, v171
	v_add_f32_e32 v190, v190, v228
	v_mov_b32_e32 v225, v171
	v_add_f32_e32 v228, v190, v191
	v_mov_b32_dpp v222, v101 row_ror:1 row_mask:0xf bank_mask:0xf
	v_mov_b32_dpp v225, v85 row_ror:15 row_mask:0xf bank_mask:0xf
	v_mul_f32_e32 v190, 0xbfb8aa3b, v228
	v_exp_f32_e32 v229, v190
	v_cndmask_b32_e64 v189, v222, v189, s[14:15]
	v_cndmask_b32_e64 v191, v223, v225, s[12:13]
	v_mov_b32_e32 v208, v101
	v_mov_b32_e32 v190, v157
	v_fma_f32 v189, v149, v189, v153
	v_pk_mul_f32 v[190:191], v[208:209], v[190:191]
	v_mul_f32_e32 v219, v224, v219
	v_add_f32_e32 v189, v190, v189
	v_add_f32_e32 v189, v189, v191
	v_mul_f32_e32 v190, 0xbfb8aa3b, v189
	v_exp_f32_e32 v190, v190
	v_mov_b32_e32 v224, v171
	v_add_f32_e32 v191, 1.0, v229
	v_rcp_f32_e32 v223, v191
	v_mov_b32_dpp v224, v85 row_ror:1 row_mask:0xf bank_mask:0xf
	v_add_f32_e32 v229, 1.0, v190
	v_cndmask_b32_e64 v190, v224, v222, s[14:15]
	v_cndmask_b32_e64 v191, v225, v227, s[12:13]
	v_fma_f32 v222, v149, v190, v153
	v_mov_b32_e32 v208, v85
	v_mov_b32_e32 v190, v157
	v_pk_mul_f32 v[190:191], v[208:209], v[190:191]
	v_mov_b32_e32 v208, v161
	v_add_f32_e32 v190, v190, v222
	v_add_f32_e32 v222, v190, v191
	v_mul_f32_e32 v190, 0xbfb8aa3b, v222
	v_cndmask_b32_e64 v191, v226, v224, s[14:15]
	v_exp_f32_e32 v225, v190
	v_cndmask_b32_e64 v190, v227, 0, s[12:13]
	v_fma_f32 v224, v149, v191, v153
	v_mov_b32_e32 v209, v73
	v_mov_b32_e32 v191, v157
	v_pk_mul_f32 v[190:191], v[208:209], v[190:191]
	v_rcp_f32_e32 v208, v229
	v_add_f32_e32 v191, v191, v224
	v_add_f32_e32 v190, v190, v191
	v_mul_f32_e32 v191, 0xbfb8aa3b, v190
	v_exp_f32_e32 v191, v191
	v_add_f32_e32 v209, 1.0, v225
	v_rcp_f32_e32 v209, v209
	v_mul_f32_e32 v224, v189, v208
	v_add_f32_e32 v191, 1.0, v191
	v_rcp_f32_e32 v191, v191
	v_mov_b32_e32 v189, v171
	v_mov_b32_e32 v227, v171
	v_mul_f32_e32 v222, v222, v209
	v_mul_f32_e32 v225, v190, v191
	v_mov_b32_dpp v189, v106 row_ror:1 row_mask:0xf bank_mask:0xf
	v_mov_b32_e32 v190, v171
	v_mov_b32_dpp v227, v90 row_ror:15 row_mask:0xf bank_mask:0xf
	v_cndmask_b32_e64 v208, v189, 0, s[14:15]
	v_mov_b32_dpp v190, v106 row_ror:15 row_mask:0xf bank_mask:0xf
	v_cndmask_b32_e64 v191, v190, v227, s[12:13]
	s_waitcnt vmcnt(0)
	v_fma_f32 v232, v138, v208, v134
	v_mov_b32_e32 v208, v106
	v_mov_b32_e32 v209, v142
	v_mov_b32_e32 v190, v130
	v_pk_mul_f32 v[190:191], v[208:209], v[190:191]
	v_mov_b32_e32 v226, v171
	v_add_f32_e32 v190, v190, v232
	v_mov_b32_e32 v229, v171
	v_add_f32_e32 v232, v190, v191
	v_mov_b32_dpp v226, v90 row_ror:1 row_mask:0xf bank_mask:0xf
	v_mov_b32_dpp v229, v74 row_ror:15 row_mask:0xf bank_mask:0xf
	v_mul_f32_e32 v190, 0xbfb8aa3b, v232
	v_exp_f32_e32 v233, v190
	v_cndmask_b32_e64 v189, v226, v189, s[14:15]
	v_cndmask_b32_e64 v191, v227, v229, s[12:13]
	v_mov_b32_e32 v208, v90
	v_mov_b32_e32 v190, v130
	v_fma_f32 v189, v138, v189, v134
	v_pk_mul_f32 v[190:191], v[208:209], v[190:191]
	v_mul_f32_e32 v223, v228, v223
	v_add_f32_e32 v189, v190, v189
	v_add_f32_e32 v189, v189, v191
	v_mul_f32_e32 v190, 0xbfb8aa3b, v189
	v_exp_f32_e32 v190, v190
	v_mov_b32_e32 v228, v171
	v_add_f32_e32 v191, 1.0, v233
	v_rcp_f32_e32 v227, v191
	v_mov_b32_dpp v228, v74 row_ror:1 row_mask:0xf bank_mask:0xf
	v_add_f32_e32 v233, 1.0, v190
	v_cndmask_b32_e64 v190, v228, v226, s[14:15]
	v_cndmask_b32_e64 v191, v229, v231, s[12:13]
	v_fma_f32 v226, v138, v190, v134
	v_mov_b32_e32 v208, v74
	v_mov_b32_e32 v190, v130
	v_pk_mul_f32 v[190:191], v[208:209], v[190:191]
	v_mov_b32_e32 v208, v142
	v_add_f32_e32 v190, v190, v226
	v_add_f32_e32 v226, v190, v191
	v_mul_f32_e32 v190, 0xbfb8aa3b, v226
	v_cndmask_b32_e64 v191, v230, v228, s[14:15]
	v_exp_f32_e32 v229, v190
	v_cndmask_b32_e64 v190, v231, 0, s[12:13]
	v_fma_f32 v228, v138, v191, v134
	v_mov_b32_e32 v209, v66
	v_mov_b32_e32 v191, v130
	v_pk_mul_f32 v[190:191], v[208:209], v[190:191]
	v_rcp_f32_e32 v208, v233
	v_add_f32_e32 v191, v191, v228
	v_add_f32_e32 v190, v190, v191
	v_mul_f32_e32 v191, 0xbfb8aa3b, v190
	v_exp_f32_e32 v191, v191
	v_add_f32_e32 v209, 1.0, v229
	v_rcp_f32_e32 v209, v209
	v_mul_f32_e32 v228, v189, v208
	v_add_f32_e32 v191, 1.0, v191
	v_rcp_f32_e32 v191, v191
	v_mov_b32_e32 v189, v171
	v_mov_b32_e32 v231, v171
	v_mul_f32_e32 v226, v226, v209
	v_mul_f32_e32 v229, v190, v191
	v_mov_b32_dpp v189, v107 row_ror:1 row_mask:0xf bank_mask:0xf
	v_mov_b32_e32 v190, v171
	v_mov_b32_dpp v231, v91 row_ror:15 row_mask:0xf bank_mask:0xf
	v_cndmask_b32_e64 v208, v189, 0, s[14:15]
; __device__ __forceinline__ float siluf(float x) { return x * __builtin_amdgcn_rcpf(1.f + __expf(-x)); }
; __device__ __forceinline__ float dpp_ror1(float v) { return __builtin_bit_cast(float, __builtin_amdgcn_update_dpp(0, __builtin_bit_cast(int, v), 0x121, 0xf, 0xf, false)); }
; __device__ __forceinline__ float dpp_ror15(float v) { return __builtin_bit_cast(float, __builtin_amdgcn_update_dpp(0, __builtin_bit_cast(int, v), 0x12F, 0xf, 0xf, false)); }
;     __device__ __forceinline__ void operator()(const f32x4 (&acc)[2][2][4][2], const pg8::Unit& u, int wr, int wc, int fr, int fq_in) const {
;     ...
;                     for (int ai = 0; ai < 2; ++ai) {
;                         f32x4 o[4][2];
; #pragma unroll
;                         for (int n = 0; n < 2; ++n)
; #pragma unroll
;                             for (int q = 0; q < 4; ++q) { float A[4], B[4];
; #pragma unroll
;                                 for (int m = 0; m < 4; ++m) { A[m] = dpp_ror1(acc[ai][bj][m][n][q]); B[m] = dpp_ror15(acc[ai][bj][m][n][q]); }
; #pragma unroll
;                                 for (int m = 0; m < 4; ++m) { const float pv = fr > 0 ? A[m] : (m > 0 ? A[m > 0 ? m - 1 : 0] : 0.f), nv = fr < 15 ? B[m] : (m < 3 ? B[m < 3 ? m + 1 : 3] : 0.f);
;                                     o[m][n][q] = siluf(bb[n][q] + w0[n][q] * pv + w1[n][q] * acc[ai][bj][m][n][q] + w2[n][q] * nv); } }
	v_mov_b32_dpp v190, v107 row_ror:15 row_mask:0xf bank_mask:0xf
	v_cndmask_b32_e64 v191, v190, v231, s[12:13]
	v_fma_f32 v236, v139, v208, v135
	v_mov_b32_e32 v208, v107
	v_mov_b32_e32 v209, v143
	v_mov_b32_e32 v190, v131
	v_pk_mul_f32 v[190:191], v[208:209], v[190:191]
	v_mov_b32_e32 v230, v171
	v_add_f32_e32 v190, v190, v236
	v_mov_b32_e32 v233, v171
	v_add_f32_e32 v236, v190, v191
	v_mov_b32_dpp v230, v91 row_ror:1 row_mask:0xf bank_mask:0xf
	v_mov_b32_dpp v233, v75 row_ror:15 row_mask:0xf bank_mask:0xf
	v_mul_f32_e32 v190, 0xbfb8aa3b, v236
	v_exp_f32_e32 v237, v190
	v_cndmask_b32_e64 v189, v230, v189, s[14:15]
	v_cndmask_b32_e64 v191, v231, v233, s[12:13]
	v_mov_b32_e32 v208, v91
	v_mov_b32_e32 v190, v131
	v_fma_f32 v189, v139, v189, v135
	v_pk_mul_f32 v[190:191], v[208:209], v[190:191]
	v_mul_f32_e32 v227, v232, v227
	v_add_f32_e32 v189, v190, v189
	v_add_f32_e32 v189, v189, v191
	v_mul_f32_e32 v190, 0xbfb8aa3b, v189
	v_exp_f32_e32 v190, v190
	v_mov_b32_e32 v232, v171
	v_add_f32_e32 v191, 1.0, v237
	v_rcp_f32_e32 v231, v191
	v_mov_b32_dpp v232, v75 row_ror:1 row_mask:0xf bank_mask:0xf
	v_add_f32_e32 v237, 1.0, v190
	v_cndmask_b32_e64 v190, v232, v230, s[14:15]
	v_cndmask_b32_e64 v191, v233, v235, s[12:13]
	v_fma_f32 v230, v139, v190, v135
	v_mov_b32_e32 v208, v75
	v_mov_b32_e32 v190, v131
	v_pk_mul_f32 v[190:191], v[208:209], v[190:191]
	v_mov_b32_e32 v208, v143
	v_add_f32_e32 v190, v190, v230
	v_add_f32_e32 v230, v190, v191
	v_mul_f32_e32 v190, 0xbfb8aa3b, v230
	v_cndmask_b32_e64 v191, v234, v232, s[14:15]
	v_exp_f32_e32 v233, v190
	v_cndmask_b32_e64 v190, v235, 0, s[12:13]
	v_fma_f32 v232, v139, v191, v135
	v_mov_b32_e32 v209, v67
	v_mov_b32_e32 v191, v131
	v_pk_mul_f32 v[190:191], v[208:209], v[190:191]
	v_rcp_f32_e32 v208, v237
	v_add_f32_e32 v191, v191, v232
	v_add_f32_e32 v190, v190, v191
	v_mul_f32_e32 v191, 0xbfb8aa3b, v190
	v_exp_f32_e32 v191, v191
	v_add_f32_e32 v209, 1.0, v233
	v_rcp_f32_e32 v209, v209
	v_mul_f32_e32 v232, v189, v208
	v_add_f32_e32 v191, 1.0, v191
	v_rcp_f32_e32 v191, v191
	v_mov_b32_e32 v189, v171
	v_mov_b32_e32 v235, v171
	v_mul_f32_e32 v230, v230, v209
	v_mul_f32_e32 v233, v190, v191
	v_mov_b32_dpp v189, v108 row_ror:1 row_mask:0xf bank_mask:0xf
	v_mov_b32_e32 v190, v171
	v_mov_b32_dpp v235, v92 row_ror:15 row_mask:0xf bank_mask:0xf
	v_cndmask_b32_e64 v208, v189, 0, s[14:15]
	v_mov_b32_dpp v190, v108 row_ror:15 row_mask:0xf bank_mask:0xf
	v_cndmask_b32_e64 v191, v190, v235, s[12:13]
	v_fma_f32 v240, v140, v208, v136
	v_mov_b32_e32 v208, v108
	v_mov_b32_e32 v209, v144
	v_mov_b32_e32 v190, v132
	v_pk_mul_f32 v[190:191], v[208:209], v[190:191]
	v_mov_b32_e32 v234, v171
	v_add_f32_e32 v190, v190, v240
	v_mov_b32_e32 v237, v171
	v_add_f32_e32 v240, v190, v191
	v_mov_b32_dpp v234, v92 row_ror:1 row_mask:0xf bank_mask:0xf
	v_mov_b32_dpp v237, v76 row_ror:15 row_mask:0xf bank_mask:0xf
	v_mul_f32_e32 v190, 0xbfb8aa3b, v240
	v_exp_f32_e32 v241, v190
	v_cndmask_b32_e64 v189, v234, v189, s[14:15]
	v_cndmask_b32_e64 v191, v235, v237, s[12:13]
	v_mov_b32_e32 v208, v92
	v_mov_b32_e32 v190, v132
	v_fma_f32 v189, v140, v189, v136
	v_pk_mul_f32 v[190:191], v[208:209], v[190:191]
	v_mul_f32_e32 v231, v236, v231
	v_add_f32_e32 v189, v190, v189
	v_add_f32_e32 v189, v189, v191
	v_mul_f32_e32 v190, 0xbfb8aa3b, v189
	v_exp_f32_e32 v190, v190
	v_mov_b32_e32 v236, v171
	v_add_f32_e32 v191, 1.0, v241
	v_rcp_f32_e32 v235, v191
	v_mov_b32_dpp v236, v76 row_ror:1 row_mask:0xf bank_mask:0xf
	v_add_f32_e32 v241, 1.0, v190
	v_cndmask_b32_e64 v190, v236, v234, s[14:15]
	v_cndmask_b32_e64 v191, v237, v239, s[12:13]
	v_fma_f32 v234, v140, v190, v136
	v_mov_b32_e32 v208, v76
	v_mov_b32_e32 v190, v132
	v_pk_mul_f32 v[190:191], v[208:209], v[190:191]
	v_mov_b32_e32 v208, v144
	v_add_f32_e32 v190, v190, v234
	v_add_f32_e32 v234, v190, v191
	v_mul_f32_e32 v190, 0xbfb8aa3b, v234
	v_cndmask_b32_e64 v191, v238, v236, s[14:15]
	v_exp_f32_e32 v237, v190
	v_cndmask_b32_e64 v190, v239, 0, s[12:13]
	v_fma_f32 v236, v140, v191, v136
	v_mov_b32_e32 v209, v68
	v_mov_b32_e32 v191, v132
	v_pk_mul_f32 v[190:191], v[208:209], v[190:191]
	v_rcp_f32_e32 v208, v241
	v_add_f32_e32 v191, v191, v236
	v_add_f32_e32 v190, v190, v191
	v_mul_f32_e32 v191, 0xbfb8aa3b, v190
	v_exp_f32_e32 v191, v191
	v_add_f32_e32 v209, 1.0, v237
	v_rcp_f32_e32 v209, v209
	v_mul_f32_e32 v236, v189, v208
	v_add_f32_e32 v191, 1.0, v191
	v_rcp_f32_e32 v191, v191
	v_mov_b32_e32 v189, v171
	v_mov_b32_e32 v239, v171
	v_mul_f32_e32 v234, v234, v209
	v_mul_f32_e32 v237, v190, v191
	v_mov_b32_dpp v189, v109 row_ror:1 row_mask:0xf bank_mask:0xf
	v_mov_b32_e32 v190, v171
	v_mov_b32_dpp v239, v93 row_ror:15 row_mask:0xf bank_mask:0xf
	v_cndmask_b32_e64 v208, v189, 0, s[14:15]
	v_mov_b32_dpp v190, v109 row_ror:15 row_mask:0xf bank_mask:0xf
	v_cndmask_b32_e64 v191, v190, v239, s[12:13]
	v_fma_f32 v244, v141, v208, v137
	v_mov_b32_e32 v208, v109
	v_mov_b32_e32 v209, v145
	v_mov_b32_e32 v190, v133
	v_pk_mul_f32 v[190:191], v[208:209], v[190:191]
	v_mov_b32_e32 v238, v171
	v_add_f32_e32 v190, v190, v244
	v_mov_b32_e32 v241, v171
	v_add_f32_e32 v244, v190, v191
	v_mov_b32_dpp v238, v93 row_ror:1 row_mask:0xf bank_mask:0xf
	v_mov_b32_dpp v241, v77 row_ror:15 row_mask:0xf bank_mask:0xf
	v_mul_f32_e32 v190, 0xbfb8aa3b, v244
	v_exp_f32_e32 v245, v190
	v_cndmask_b32_e64 v189, v238, v189, s[14:15]
	v_cndmask_b32_e64 v191, v239, v241, s[12:13]
	v_mov_b32_e32 v208, v93
	v_mov_b32_e32 v190, v133
	v_fma_f32 v189, v141, v189, v137
	v_pk_mul_f32 v[190:191], v[208:209], v[190:191]
	v_mul_f32_e32 v235, v240, v235
	v_add_f32_e32 v189, v190, v189
	v_add_f32_e32 v189, v189, v191
	v_mul_f32_e32 v190, 0xbfb8aa3b, v189
; __device__ __forceinline__ unsigned cvt_pk_bf16(float lo, float hi) { unsigned r; asm volatile("v_cvt_pk_bf16_f32 %0, %1, %2" : "=v"(r) : "v"(lo), "v"(hi)); return r; }
; __device__ __forceinline__ float siluf(float x) { return x * __builtin_amdgcn_rcpf(1.f + __expf(-x)); }
; __device__ __forceinline__ float dpp_ror1(float v) { return __builtin_bit_cast(float, __builtin_amdgcn_update_dpp(0, __builtin_bit_cast(int, v), 0x121, 0xf, 0xf, false)); }
; __device__ __forceinline__ float dpp_ror15(float v) { return __builtin_bit_cast(float, __builtin_amdgcn_update_dpp(0, __builtin_bit_cast(int, v), 0x12F, 0xf, 0xf, false)); }
;     __device__ __forceinline__ void operator()(const f32x4 (&acc)[2][2][4][2], const pg8::Unit& u, int wr, int wc, int fr, int fq_in) const {
;     ...
;                     for (int ai = 0; ai < 2; ++ai) {
;                         f32x4 o[4][2];
; #pragma unroll
;                         for (int n = 0; n < 2; ++n)
; #pragma unroll
;                             for (int q = 0; q < 4; ++q) { float A[4], B[4];
; #pragma unroll
;                                 for (int m = 0; m < 4; ++m) { A[m] = dpp_ror1(acc[ai][bj][m][n][q]); B[m] = dpp_ror15(acc[ai][bj][m][n][q]); }
; #pragma unroll
;                                 for (int m = 0; m < 4; ++m) { const float pv = fr > 0 ? A[m] : (m > 0 ? A[m > 0 ? m - 1 : 0] : 0.f), nv = fr < 15 ? B[m] : (m < 3 ? B[m < 3 ? m + 1 : 3] : 0.f);
;                                     o[m][n][q] = siluf(bb[n][q] + w0[n][q] * pv + w1[n][q] * acc[ai][bj][m][n][q] + w2[n][q] * nv); } }
; #pragma unroll
;                         for (int m = 0; m < 4; ++m) { u32x4 w; w.x = pg8::cvt_pk_bf16(o[m][0][0], o[m][0][1]); w.y = pg8::cvt_pk_bf16(o[m][0][2], o[m][0][3]); w.z = pg8::cvt_pk_bf16(o[m][1][0], o[m][1][1]); w.w = pg8::cvt_pk_bf16(o[m][1][2], o[m][1][3]);
;                             *(u32x4*)(XBC + (size_t)(row0 + ai * 128 + m * 16) * XBCW + col) = w; }
	v_exp_f32_e32 v190, v190
	v_mov_b32_e32 v240, v171
	v_add_f32_e32 v191, 1.0, v245
	v_rcp_f32_e32 v239, v191
	v_mov_b32_dpp v240, v77 row_ror:1 row_mask:0xf bank_mask:0xf
	v_add_f32_e32 v245, 1.0, v190
	v_cndmask_b32_e64 v190, v240, v238, s[14:15]
	v_cndmask_b32_e64 v191, v241, v243, s[12:13]
	v_fma_f32 v238, v141, v190, v137
	v_mov_b32_e32 v208, v77
	v_mov_b32_e32 v190, v133
	v_pk_mul_f32 v[190:191], v[208:209], v[190:191]
	v_mov_b32_e32 v208, v145
	v_add_f32_e32 v190, v190, v238
	v_add_f32_e32 v238, v190, v191
	v_mul_f32_e32 v190, 0xbfb8aa3b, v238
	v_cndmask_b32_e64 v191, v242, v240, s[14:15]
	v_exp_f32_e32 v241, v190
	v_cndmask_b32_e64 v190, v243, 0, s[12:13]
	v_fma_f32 v240, v141, v191, v137
	v_mov_b32_e32 v209, v69
	v_mov_b32_e32 v191, v133
	v_pk_mul_f32 v[190:191], v[208:209], v[190:191]
	v_add_f32_e32 v209, 1.0, v241
	v_add_f32_e32 v191, v191, v240
	v_add_f32_e32 v190, v190, v191
	v_mul_f32_e32 v191, 0xbfb8aa3b, v190
	v_exp_f32_e32 v191, v191
	v_rcp_f32_e32 v208, v245
	v_rcp_f32_e32 v209, v209
	v_mul_f32_e32 v239, v244, v239
	v_add_f32_e32 v191, 1.0, v191
	v_rcp_f32_e32 v191, v191
	v_mul_f32_e32 v208, v189, v208
	v_mul_f32_e32 v209, v238, v209
	v_cvt_pk_bf16_f32 v188, v182, v188
	v_mul_f32_e32 v238, v190, v191
	v_cvt_pk_bf16_f32 v189, v219, v223
	v_cvt_pk_bf16_f32 v190, v227, v231
	v_cvt_pk_bf16_f32 v191, v235, v239
	global_store_dwordx4 v[192:193], v[188:191], off offset:256
	v_mov_b32_e32 v192, v171
	s_nop 0
	v_cvt_pk_bf16_f32 v188, v179, v185
	v_cvt_pk_bf16_f32 v189, v220, v224
	v_cvt_pk_bf16_f32 v190, v228, v232
	v_cvt_pk_bf16_f32 v191, v236, v208
	global_store_dwordx4 v[194:195], v[188:191], off offset:256
	v_mov_b32_e32 v179, v171
	v_mov_b32_dpp v192, v6 row_ror:15 row_mask:0xf bank_mask:0xf
	v_cvt_pk_bf16_f32 v188, v177, v184
	v_cvt_pk_bf16_f32 v189, v218, v222
	v_cvt_pk_bf16_f32 v190, v226, v230
	v_cvt_pk_bf16_f32 v191, v234, v209
	global_store_dwordx4 v[196:197], v[188:191], off offset:256
	v_cvt_pk_bf16_f32 v182, v170, v183
	v_mov_b32_e32 v170, v171
	v_mov_b32_e32 v177, v171
	v_mov_b32_e32 v188, v171
	v_mov_b32_dpp v170, v50 row_ror:1 row_mask:0xf bank_mask:0xf
	v_cvt_pk_bf16_f32 v183, v221, v225
	v_cvt_pk_bf16_f32 v184, v229, v233
	v_cvt_pk_bf16_f32 v185, v237, v238
	global_store_dwordx4 v[198:199], v[182:185], off offset:256
	v_mov_b32_dpp v177, v50 row_ror:15 row_mask:0xf bank_mask:0xf
	v_mov_b32_dpp v188, v34 row_ror:15 row_mask:0xf bank_mask:0xf
	v_cndmask_b32_e64 v182, v170, 0, s[14:15]
	v_cndmask_b32_e64 v183, v177, v188, s[12:13]
	v_fma_f32 v177, v146, v182, v150
	v_mov_b32_e32 v184, v50
	v_mov_b32_e32 v185, v158
	v_mov_b32_e32 v182, v154
	v_pk_mul_f32 v[182:183], v[184:185], v[182:183]
	v_mov_b32_e32 v190, v171
	v_add_f32_e32 v177, v182, v177
	v_add_f32_e32 v177, v177, v183
	v_mov_b32_dpp v179, v34 row_ror:1 row_mask:0xf bank_mask:0xf
	v_mov_b32_dpp v190, v18 row_ror:15 row_mask:0xf bank_mask:0xf
	v_mul_f32_e32 v182, 0xbfb8aa3b, v177
	v_exp_f32_e32 v193, v182
	v_cndmask_b32_e64 v170, v179, v170, s[14:15]
	v_cndmask_b32_e64 v183, v188, v190, s[12:13]
	v_mov_b32_e32 v184, v34
	v_mov_b32_e32 v182, v154
	v_fma_f32 v170, v146, v170, v150
	v_pk_mul_f32 v[182:183], v[184:185], v[182:183]
	v_mov_b32_e32 v189, v171
	v_add_f32_e32 v170, v182, v170
	v_add_f32_e32 v170, v170, v183
	v_mul_f32_e32 v182, 0xbfb8aa3b, v170
	v_exp_f32_e32 v182, v182
	v_mov_b32_dpp v189, v18 row_ror:1 row_mask:0xf bank_mask:0xf
	v_add_f32_e32 v183, 1.0, v193
	v_rcp_f32_e32 v188, v183
	v_add_f32_e32 v193, 1.0, v182
	v_cndmask_b32_e64 v179, v189, v179, s[14:15]
	v_cndmask_b32_e64 v183, v190, v192, s[12:13]
	v_mov_b32_e32 v184, v18
	v_mov_b32_e32 v182, v154
	v_fma_f32 v179, v146, v179, v150
	v_pk_mul_f32 v[182:183], v[184:185], v[182:183]
	v_mov_b32_e32 v191, v171
	v_add_f32_e32 v179, v182, v179
	v_add_f32_e32 v179, v179, v183
	v_mov_b32_dpp v191, v6 row_ror:1 row_mask:0xf bank_mask:0xf
	v_mul_f32_e32 v182, 0xbfb8aa3b, v179
	v_cndmask_b32_e64 v183, v191, v189, s[14:15]
	v_exp_f32_e32 v190, v182
	v_cndmask_b32_e64 v182, v192, 0, s[12:13]
	v_fma_f32 v146, v146, v183, v150
	v_mov_b32_e32 v184, v158
	v_mov_b32_e32 v185, v6
	v_mov_b32_e32 v183, v154
	v_pk_mul_f32 v[182:183], v[184:185], v[182:183]
	v_rcp_f32_e32 v154, v193
	v_add_f32_e32 v146, v183, v146
	v_add_f32_e32 v146, v182, v146
	v_mul_f32_e32 v150, 0xbfb8aa3b, v146
	v_exp_f32_e32 v150, v150
	v_add_f32_e32 v158, 1.0, v190
	v_rcp_f32_e32 v158, v158
	v_mul_f32_e32 v170, v170, v154
	v_add_f32_e32 v150, 1.0, v150
	v_rcp_f32_e32 v182, v150
	v_mov_b32_e32 v154, v171
	v_mul_f32_e32 v150, v179, v158
	v_mov_b32_e32 v158, v171
	v_mov_b32_dpp v154, v51 row_ror:1 row_mask:0xf bank_mask:0xf
	v_mov_b32_e32 v184, v171
	v_mul_f32_e32 v146, v146, v182
	v_mov_b32_dpp v158, v51 row_ror:15 row_mask:0xf bank_mask:0xf
	v_mov_b32_dpp v184, v35 row_ror:15 row_mask:0xf bank_mask:0xf
	v_cndmask_b32_e64 v182, v154, 0, s[14:15]
	v_cndmask_b32_e64 v183, v158, v184, s[12:13]
	v_fma_f32 v191, v147, v182, v151
	v_mov_b32_e32 v158, v51
	v_mov_b32_e32 v182, v155
	v_pk_mul_f32 v[182:183], v[158:159], v[182:183]
	v_mul_f32_e32 v177, v177, v188
	v_add_f32_e32 v158, v182, v191
	v_mov_b32_e32 v179, v171
	v_mov_b32_e32 v188, v171
	v_add_f32_e32 v191, v158, v183
	v_mov_b32_dpp v179, v35 row_ror:1 row_mask:0xf bank_mask:0xf
	v_mov_b32_dpp v188, v19 row_ror:15 row_mask:0xf bank_mask:0xf
	v_mul_f32_e32 v158, 0xbfb8aa3b, v191
	v_exp_f32_e32 v192, v158
	v_cndmask_b32_e64 v154, v179, v154, s[14:15]
	v_cndmask_b32_e64 v183, v184, v188, s[12:13]
	v_mov_b32_e32 v158, v35
	v_mov_b32_e32 v182, v155
	v_fma_f32 v154, v147, v154, v151
	v_pk_mul_f32 v[182:183], v[158:159], v[182:183]
	v_mov_b32_e32 v185, v171
	v_add_f32_e32 v154, v182, v154
; __device__ __forceinline__ float siluf(float x) { return x * __builtin_amdgcn_rcpf(1.f + __expf(-x)); }
; __device__ __forceinline__ float dpp_ror1(float v) { return __builtin_bit_cast(float, __builtin_amdgcn_update_dpp(0, __builtin_bit_cast(int, v), 0x121, 0xf, 0xf, false)); }
; __device__ __forceinline__ float dpp_ror15(float v) { return __builtin_bit_cast(float, __builtin_amdgcn_update_dpp(0, __builtin_bit_cast(int, v), 0x12F, 0xf, 0xf, false)); }
;     __device__ __forceinline__ void operator()(const f32x4 (&acc)[2][2][4][2], const pg8::Unit& u, int wr, int wc, int fr, int fq_in) const {
;     ...
;                     for (int ai = 0; ai < 2; ++ai) {
;                         f32x4 o[4][2];
; #pragma unroll
;                         for (int n = 0; n < 2; ++n)
; #pragma unroll
;                             for (int q = 0; q < 4; ++q) { float A[4], B[4];
; #pragma unroll
;                                 for (int m = 0; m < 4; ++m) { A[m] = dpp_ror1(acc[ai][bj][m][n][q]); B[m] = dpp_ror15(acc[ai][bj][m][n][q]); }
; #pragma unroll
;                                 for (int m = 0; m < 4; ++m) { const float pv = fr > 0 ? A[m] : (m > 0 ? A[m > 0 ? m - 1 : 0] : 0.f), nv = fr < 15 ? B[m] : (m < 3 ? B[m < 3 ? m + 1 : 3] : 0.f);
;                                     o[m][n][q] = siluf(bb[n][q] + w0[n][q] * pv + w1[n][q] * acc[ai][bj][m][n][q] + w2[n][q] * nv); } }
	v_add_f32_e32 v184, v154, v183
	v_mul_f32_e32 v154, 0xbfb8aa3b, v184
	v_exp_f32_e32 v154, v154
	v_mov_b32_e32 v190, v171
	v_mov_b32_dpp v185, v19 row_ror:1 row_mask:0xf bank_mask:0xf
	v_add_f32_e32 v158, 1.0, v192
	v_mov_b32_dpp v190, v7 row_ror:15 row_mask:0xf bank_mask:0xf
	v_rcp_f32_e32 v192, v158
	v_add_f32_e32 v193, 1.0, v154
	v_cndmask_b32_e64 v154, v185, v179, s[14:15]
	v_cndmask_b32_e64 v183, v188, v190, s[12:13]
	v_mov_b32_e32 v158, v19
	v_mov_b32_e32 v182, v155
	v_fma_f32 v154, v147, v154, v151
	v_pk_mul_f32 v[182:183], v[158:159], v[182:183]
	v_mov_b32_e32 v189, v171
	v_add_f32_e32 v154, v182, v154
	v_add_f32_e32 v179, v154, v183
	v_mov_b32_dpp v189, v7 row_ror:1 row_mask:0xf bank_mask:0xf
	v_mul_f32_e32 v154, 0xbfb8aa3b, v179
	v_cndmask_b32_e64 v158, v189, v185, s[14:15]
	v_exp_f32_e32 v182, v154
	v_cndmask_b32_e64 v154, v190, 0, s[12:13]
	v_fma_f32 v147, v147, v158, v151
	v_mov_b32_e32 v158, v159
	v_mov_b32_e32 v159, v7
	v_pk_mul_f32 v[154:155], v[158:159], v[154:155]
	v_mov_b32_e32 v185, v171
	v_add_f32_e32 v147, v155, v147
	v_add_f32_e32 v147, v154, v147
	v_mul_f32_e32 v151, 0xbfb8aa3b, v147
	v_exp_f32_e32 v151, v151
	v_add_f32_e32 v155, 1.0, v182
	v_rcp_f32_e32 v158, v155
	v_rcp_f32_e32 v154, v193
	v_add_f32_e32 v151, 1.0, v151
	v_rcp_f32_e32 v159, v151
	v_mul_f32_e32 v151, v179, v158
	v_mov_b32_e32 v179, v171
	v_mov_b32_e32 v158, v171
	v_mov_b32_dpp v185, v36 row_ror:15 row_mask:0xf bank_mask:0xf
	v_mov_b32_dpp v179, v52 row_ror:1 row_mask:0xf bank_mask:0xf
	v_mov_b32_dpp v158, v52 row_ror:15 row_mask:0xf bank_mask:0xf
	v_cndmask_b32_e64 v182, v179, 0, s[14:15]
	v_mul_f32_e32 v155, v191, v192
	v_mul_f32_e32 v147, v147, v159
	v_cndmask_b32_e64 v159, v158, v185, s[12:13]
	v_fma_f32 v192, v148, v182, v152
	v_mov_b32_e32 v182, v52
	v_mov_b32_e32 v183, v160
	v_mov_b32_e32 v158, v156
	v_pk_mul_f32 v[158:159], v[182:183], v[158:159]
	v_mul_f32_e32 v154, v184, v154
	v_add_f32_e32 v158, v158, v192
	v_mov_b32_e32 v184, v171
	v_add_f32_e32 v192, v158, v159
	v_mov_b32_e32 v189, v171
	v_mov_b32_dpp v184, v36 row_ror:1 row_mask:0xf bank_mask:0xf
	v_mul_f32_e32 v158, 0xbfb8aa3b, v192
	v_mov_b32_dpp v189, v20 row_ror:15 row_mask:0xf bank_mask:0xf
	v_exp_f32_e32 v193, v158
	v_cndmask_b32_e64 v158, v184, v179, s[14:15]
	v_cndmask_b32_e64 v159, v185, v189, s[12:13]
	v_fma_f32 v179, v148, v158, v152
	v_mov_b32_e32 v182, v36
	v_mov_b32_e32 v158, v156
	v_pk_mul_f32 v[158:159], v[182:183], v[158:159]
	v_mov_b32_e32 v188, v171
	v_add_f32_e32 v158, v158, v179
	v_add_f32_e32 v179, v158, v159
	v_mul_f32_e32 v158, 0xbfb8aa3b, v179
	v_exp_f32_e32 v158, v158
	v_mov_b32_dpp v188, v20 row_ror:1 row_mask:0xf bank_mask:0xf
	v_mov_b32_e32 v191, v171
	v_add_f32_e32 v159, 1.0, v193
	v_add_f32_e32 v193, 1.0, v158
	v_mov_b32_dpp v191, v8 row_ror:15 row_mask:0xf bank_mask:0xf
	v_cndmask_b32_e64 v158, v188, v184, s[14:15]
	v_rcp_f32_e32 v185, v159
	v_cndmask_b32_e64 v159, v189, v191, s[12:13]
	v_fma_f32 v184, v148, v158, v152
	v_mov_b32_e32 v182, v20
	v_mov_b32_e32 v158, v156
	v_pk_mul_f32 v[158:159], v[182:183], v[158:159]
	v_mov_b32_e32 v190, v171
	v_add_f32_e32 v158, v158, v184
	v_add_f32_e32 v184, v158, v159
	v_mov_b32_dpp v190, v8 row_ror:1 row_mask:0xf bank_mask:0xf
	v_mul_f32_e32 v158, 0xbfb8aa3b, v184
	v_cndmask_b32_e64 v159, v190, v188, s[14:15]
	v_exp_f32_e32 v189, v158
	v_cndmask_b32_e64 v158, v191, 0, s[12:13]
	v_fma_f32 v148, v148, v159, v152
	v_mov_b32_e32 v182, v160
	v_mov_b32_e32 v183, v8
	v_mov_b32_e32 v159, v156
	v_pk_mul_f32 v[158:159], v[182:183], v[158:159]
	v_mul_f32_e32 v182, v192, v185
	v_add_f32_e32 v148, v159, v148
	v_add_f32_e32 v148, v158, v148
	v_mul_f32_e32 v152, 0xbfb8aa3b, v148
	v_exp_f32_e32 v152, v152
	v_add_f32_e32 v158, 1.0, v189
	v_rcp_f32_e32 v158, v158
	v_mov_b32_e32 v185, v171
	v_add_f32_e32 v152, 1.0, v152
	v_rcp_f32_e32 v152, v152
	v_mul_f32_e32 v183, v184, v158
	v_rcp_f32_e32 v156, v193
	v_mov_b32_dpp v185, v37 row_ror:15 row_mask:0xf bank_mask:0xf
	v_mul_f32_e32 v184, v148, v152
	v_mov_b32_e32 v148, v171
	v_mov_b32_e32 v152, v171
	v_mov_b32_e32 v160, v53
	v_mov_b32_dpp v148, v53 row_ror:1 row_mask:0xf bank_mask:0xf
	v_mov_b32_dpp v152, v53 row_ror:15 row_mask:0xf bank_mask:0xf
	v_cndmask_b32_e64 v158, v148, 0, s[14:15]
	v_cndmask_b32_e64 v159, v152, v185, s[12:13]
	v_fma_f32 v152, v149, v158, v153
	v_mov_b32_e32 v158, v157
	v_pk_mul_f32 v[158:159], v[160:161], v[158:159]
	v_mul_f32_e32 v179, v179, v156
	v_add_f32_e32 v152, v158, v152
	v_mov_b32_e32 v156, v171
	v_mov_b32_e32 v189, v171
	v_add_f32_e32 v152, v152, v159
	v_mov_b32_dpp v156, v37 row_ror:1 row_mask:0xf bank_mask:0xf
	v_mov_b32_dpp v189, v21 row_ror:15 row_mask:0xf bank_mask:0xf
	v_mul_f32_e32 v158, 0xbfb8aa3b, v152
	v_exp_f32_e32 v192, v158
	v_cndmask_b32_e64 v148, v156, v148, s[14:15]
	v_cndmask_b32_e64 v159, v185, v189, s[12:13]
	v_mov_b32_e32 v160, v37
	v_mov_b32_e32 v158, v157
	v_fma_f32 v148, v149, v148, v153
	v_pk_mul_f32 v[158:159], v[160:161], v[158:159]
	v_mov_b32_e32 v188, v171
	v_add_f32_e32 v148, v158, v148
	v_add_f32_e32 v185, v148, v159
	v_mul_f32_e32 v148, 0xbfb8aa3b, v185
	v_exp_f32_e32 v148, v148
	v_mov_b32_e32 v191, v171
	v_mov_b32_dpp v188, v21 row_ror:1 row_mask:0xf bank_mask:0xf
	v_add_f32_e32 v158, 1.0, v192
	v_mov_b32_dpp v191, v9 row_ror:15 row_mask:0xf bank_mask:0xf
	v_rcp_f32_e32 v192, v158
	v_add_f32_e32 v193, 1.0, v148
	v_cndmask_b32_e64 v148, v188, v156, s[14:15]
	v_cndmask_b32_e64 v159, v189, v191, s[12:13]
	v_mov_b32_e32 v160, v21
	v_mov_b32_e32 v158, v157
	v_fma_f32 v148, v149, v148, v153
	v_pk_mul_f32 v[158:159], v[160:161], v[158:159]
	v_mov_b32_e32 v190, v171
	v_add_f32_e32 v148, v158, v148
	v_add_f32_e32 v158, v148, v159
; __device__ __forceinline__ float siluf(float x) { return x * __builtin_amdgcn_rcpf(1.f + __expf(-x)); }
; __device__ __forceinline__ float dpp_ror1(float v) { return __builtin_bit_cast(float, __builtin_amdgcn_update_dpp(0, __builtin_bit_cast(int, v), 0x121, 0xf, 0xf, false)); }
; __device__ __forceinline__ float dpp_ror15(float v) { return __builtin_bit_cast(float, __builtin_amdgcn_update_dpp(0, __builtin_bit_cast(int, v), 0x12F, 0xf, 0xf, false)); }
;     __device__ __forceinline__ void operator()(const f32x4 (&acc)[2][2][4][2], const pg8::Unit& u, int wr, int wc, int fr, int fq_in) const {
;     ...
;                     for (int ai = 0; ai < 2; ++ai) {
;                         f32x4 o[4][2];
; #pragma unroll
;                         for (int n = 0; n < 2; ++n)
; #pragma unroll
;                             for (int q = 0; q < 4; ++q) { float A[4], B[4];
; #pragma unroll
;                                 for (int m = 0; m < 4; ++m) { A[m] = dpp_ror1(acc[ai][bj][m][n][q]); B[m] = dpp_ror15(acc[ai][bj][m][n][q]); }
; #pragma unroll
;                                 for (int m = 0; m < 4; ++m) { const float pv = fr > 0 ? A[m] : (m > 0 ? A[m > 0 ? m - 1 : 0] : 0.f), nv = fr < 15 ? B[m] : (m < 3 ? B[m < 3 ? m + 1 : 3] : 0.f);
;                                     o[m][n][q] = siluf(bb[n][q] + w0[n][q] * pv + w1[n][q] * acc[ai][bj][m][n][q] + w2[n][q] * nv); } }
	v_mov_b32_dpp v190, v9 row_ror:1 row_mask:0xf bank_mask:0xf
	v_mul_f32_e32 v148, 0xbfb8aa3b, v158
	v_exp_f32_e32 v159, v148
	v_cndmask_b32_e64 v148, v190, v188, s[14:15]
	v_cndmask_b32_e64 v156, v191, 0, s[12:13]
	v_fmac_f32_e32 v153, v149, v148
	v_mov_b32_e32 v148, v161
	v_mov_b32_e32 v149, v9
	v_pk_mul_f32 v[148:149], v[148:149], v[156:157]
	v_add_f32_e32 v156, 1.0, v159
	v_add_f32_e32 v149, v149, v153
	v_add_f32_e32 v148, v148, v149
	v_mul_f32_e32 v149, 0xbfb8aa3b, v148
	v_exp_f32_e32 v149, v149
	v_rcp_f32_e32 v153, v193
	v_rcp_f32_e32 v156, v156
	v_mov_b32_e32 v160, v171
	v_add_f32_e32 v149, 1.0, v149
	v_rcp_f32_e32 v149, v149
	v_mul_f32_e32 v159, v185, v153
	v_mul_f32_e32 v156, v158, v156
	v_mov_b32_dpp v160, v42 row_ror:1 row_mask:0xf bank_mask:0xf
	v_mul_f32_e32 v158, v148, v149
	v_mov_b32_e32 v148, v171
	v_mov_b32_e32 v185, v171
	v_mul_f32_e32 v157, v152, v192
	v_mov_b32_dpp v148, v42 row_ror:15 row_mask:0xf bank_mask:0xf
	v_mov_b32_dpp v185, v26 row_ror:15 row_mask:0xf bank_mask:0xf
	v_cndmask_b32_e64 v152, v160, 0, s[14:15]
	v_cndmask_b32_e64 v149, v148, v185, s[12:13]
	v_fma_f32 v192, v138, v152, v134
	v_mov_b32_e32 v152, v42
	v_mov_b32_e32 v153, v142
	v_mov_b32_e32 v148, v130
	v_pk_mul_f32 v[148:149], v[152:153], v[148:149]
	v_mov_b32_e32 v161, v171
	v_add_f32_e32 v148, v148, v192
	v_add_f32_e32 v192, v148, v149
	v_mov_b32_dpp v161, v26 row_ror:1 row_mask:0xf bank_mask:0xf
	v_mov_b32_e32 v189, v171
	v_mul_f32_e32 v148, 0xbfb8aa3b, v192
	v_exp_f32_e32 v193, v148
	v_mov_b32_dpp v189, v10 row_ror:15 row_mask:0xf bank_mask:0xf
	v_cndmask_b32_e64 v148, v161, v160, s[14:15]
	v_cndmask_b32_e64 v149, v185, v189, s[12:13]
	v_fma_f32 v160, v138, v148, v134
	v_mov_b32_e32 v152, v26
	v_mov_b32_e32 v148, v130
	v_pk_mul_f32 v[148:149], v[152:153], v[148:149]
	v_mov_b32_e32 v188, v171
	v_add_f32_e32 v148, v148, v160
	v_add_f32_e32 v160, v148, v149
	v_mul_f32_e32 v148, 0xbfb8aa3b, v160
	v_exp_f32_e32 v148, v148
	v_mov_b32_dpp v188, v10 row_ror:1 row_mask:0xf bank_mask:0xf
	v_mov_b32_e32 v191, v171
	v_add_f32_e32 v149, 1.0, v193
	v_add_f32_e32 v193, 1.0, v148
	v_mov_b32_dpp v191, v2 row_ror:15 row_mask:0xf bank_mask:0xf
	v_cndmask_b32_e64 v148, v188, v161, s[14:15]
	v_rcp_f32_e32 v185, v149
	v_cndmask_b32_e64 v149, v189, v191, s[12:13]
	v_fma_f32 v161, v138, v148, v134
	v_mov_b32_e32 v152, v10
	v_mov_b32_e32 v148, v130
	v_pk_mul_f32 v[148:149], v[152:153], v[148:149]
	v_mov_b32_e32 v190, v171
	v_add_f32_e32 v148, v148, v161
	v_add_f32_e32 v161, v148, v149
	v_mov_b32_dpp v190, v2 row_ror:1 row_mask:0xf bank_mask:0xf
	v_mul_f32_e32 v148, 0xbfb8aa3b, v161
	v_cndmask_b32_e64 v149, v190, v188, s[14:15]
	v_exp_f32_e32 v189, v148
	v_cndmask_b32_e64 v148, v191, 0, s[12:13]
	v_fma_f32 v134, v138, v149, v134
	v_mov_b32_e32 v152, v142
	v_mov_b32_e32 v153, v2
	v_mov_b32_e32 v149, v130
	v_pk_mul_f32 v[148:149], v[152:153], v[148:149]
	v_rcp_f32_e32 v138, v193
	v_add_f32_e32 v130, v149, v134
	v_add_f32_e32 v130, v148, v130
	v_mul_f32_e32 v134, 0xbfb8aa3b, v130
	v_exp_f32_e32 v134, v134
	v_add_f32_e32 v142, 1.0, v189
	v_rcp_f32_e32 v142, v142
	v_mul_f32_e32 v138, v160, v138
	v_add_f32_e32 v134, 1.0, v134
	v_rcp_f32_e32 v134, v134
	v_mul_f32_e32 v152, v192, v185
	v_mov_b32_e32 v185, v171
	v_mul_f32_e32 v153, v161, v142
	v_mul_f32_e32 v160, v130, v134
	v_mov_b32_e32 v130, v171
	v_mov_b32_e32 v134, v171
	v_mov_b32_dpp v185, v27 row_ror:15 row_mask:0xf bank_mask:0xf
	v_mov_b32_dpp v130, v43 row_ror:1 row_mask:0xf bank_mask:0xf
	v_mov_b32_dpp v134, v43 row_ror:15 row_mask:0xf bank_mask:0xf
	v_cndmask_b32_e64 v142, v130, 0, s[14:15]
	v_cndmask_b32_e64 v149, v134, v185, s[12:13]
	v_fma_f32 v134, v139, v142, v135
	v_mov_b32_e32 v142, v43
	v_mov_b32_e32 v148, v131
	v_mov_b32_e32 v161, v171
	v_mov_b32_e32 v189, v171
	v_pk_mul_f32 v[148:149], v[142:143], v[148:149]
	v_mov_b32_dpp v161, v27 row_ror:1 row_mask:0xf bank_mask:0xf
	v_mov_b32_dpp v189, v11 row_ror:15 row_mask:0xf bank_mask:0xf
	v_add_f32_e32 v134, v148, v134
	v_add_f32_e32 v192, v134, v149
	v_cndmask_b32_e64 v130, v161, v130, s[14:15]
	v_cndmask_b32_e64 v149, v185, v189, s[12:13]
	v_mov_b32_e32 v142, v27
	v_mov_b32_e32 v148, v131
	v_fma_f32 v130, v139, v130, v135
	v_pk_mul_f32 v[148:149], v[142:143], v[148:149]
	v_mov_b32_e32 v188, v171
	v_add_f32_e32 v130, v148, v130
	v_add_f32_e32 v185, v130, v149
	v_mul_f32_e32 v130, 0xbfb8aa3b, v185
	v_exp_f32_e32 v130, v130
	v_mov_b32_e32 v191, v171
	v_mul_f32_e32 v134, 0xbfb8aa3b, v192
	v_mov_b32_dpp v188, v11 row_ror:1 row_mask:0xf bank_mask:0xf
	v_exp_f32_e32 v134, v134
	v_mov_b32_dpp v191, v3 row_ror:15 row_mask:0xf bank_mask:0xf
	v_add_f32_e32 v194, 1.0, v130
	v_cndmask_b32_e64 v130, v188, v161, s[14:15]
	v_cndmask_b32_e64 v149, v189, v191, s[12:13]
	v_mov_b32_e32 v142, v11
	v_mov_b32_e32 v148, v131
	v_fma_f32 v130, v139, v130, v135
	v_pk_mul_f32 v[148:149], v[142:143], v[148:149]
	v_mov_b32_e32 v190, v171
	v_add_f32_e32 v130, v148, v130
	v_add_f32_e32 v134, 1.0, v134
	v_mov_b32_dpp v190, v3 row_ror:1 row_mask:0xf bank_mask:0xf
	v_add_f32_e32 v142, v130, v149
	v_rcp_f32_e32 v193, v134
	v_mul_f32_e32 v130, 0xbfb8aa3b, v142
	v_cndmask_b32_e64 v134, v190, v188, s[14:15]
	v_exp_f32_e32 v148, v130
	v_cndmask_b32_e64 v130, v191, 0, s[12:13]
	v_fma_f32 v139, v139, v134, v135
	v_mov_b32_e32 v134, v143
	v_mov_b32_e32 v135, v3
	v_pk_mul_f32 v[130:131], v[134:135], v[130:131]
	v_rcp_f32_e32 v134, v194
	v_add_f32_e32 v131, v131, v139
	v_add_f32_e32 v130, v130, v131
	v_mul_f32_e32 v131, 0xbfb8aa3b, v130
	v_exp_f32_e32 v131, v131
	v_add_f32_e32 v135, 1.0, v148
	v_rcp_f32_e32 v135, v135
	v_mov_b32_e32 v149, v171
	v_add_f32_e32 v131, 1.0, v131
	v_rcp_f32_e32 v131, v131
; __device__ __forceinline__ unsigned cvt_pk_bf16(float lo, float hi) { unsigned r; asm volatile("v_cvt_pk_bf16_f32 %0, %1, %2" : "=v"(r) : "v"(lo), "v"(hi)); return r; }
; __device__ __forceinline__ float siluf(float x) { return x * __builtin_amdgcn_rcpf(1.f + __expf(-x)); }
; __device__ __forceinline__ float dpp_ror1(float v) { return __builtin_bit_cast(float, __builtin_amdgcn_update_dpp(0, __builtin_bit_cast(int, v), 0x121, 0xf, 0xf, false)); }
; __device__ __forceinline__ float dpp_ror15(float v) { return __builtin_bit_cast(float, __builtin_amdgcn_update_dpp(0, __builtin_bit_cast(int, v), 0x12F, 0xf, 0xf, false)); }
;     __device__ __forceinline__ void operator()(const f32x4 (&acc)[2][2][4][2], const pg8::Unit& u, int wr, int wc, int fr, int fq_in) const {
;     ...
;                     for (int ai = 0; ai < 2; ++ai) {
;                         f32x4 o[4][2];
; #pragma unroll
;                         for (int n = 0; n < 2; ++n)
; #pragma unroll
;                             for (int q = 0; q < 4; ++q) { float A[4], B[4];
; #pragma unroll
;                                 for (int m = 0; m < 4; ++m) { A[m] = dpp_ror1(acc[ai][bj][m][n][q]); B[m] = dpp_ror15(acc[ai][bj][m][n][q]); }
; #pragma unroll
;                                 for (int m = 0; m < 4; ++m) { const float pv = fr > 0 ? A[m] : (m > 0 ? A[m > 0 ? m - 1 : 0] : 0.f), nv = fr < 15 ? B[m] : (m < 3 ? B[m < 3 ? m + 1 : 3] : 0.f);
;                                     o[m][n][q] = siluf(bb[n][q] + w0[n][q] * pv + w1[n][q] * acc[ai][bj][m][n][q] + w2[n][q] * nv); } }
; #pragma unroll
;                         for (int m = 0; m < 4; ++m) { u32x4 w; w.x = pg8::cvt_pk_bf16(o[m][0][0], o[m][0][1]); w.y = pg8::cvt_pk_bf16(o[m][0][2], o[m][0][3]); w.z = pg8::cvt_pk_bf16(o[m][1][0], o[m][1][1]); w.w = pg8::cvt_pk_bf16(o[m][1][2], o[m][1][3]);
;                             *(u32x4*)(XBC + (size_t)(row0 + ai * 128 + m * 16) * XBCW + col) = w; }
	v_mul_f32_e32 v143, v185, v134
	v_mov_b32_dpp v149, v44 row_ror:1 row_mask:0xf bank_mask:0xf
	v_mov_b32_e32 v185, v171
	v_mul_f32_e32 v148, v130, v131
	v_mov_b32_e32 v130, v171
	v_mov_b32_dpp v185, v28 row_ror:15 row_mask:0xf bank_mask:0xf
	v_cndmask_b32_e64 v134, v149, 0, s[14:15]
	v_mov_b32_dpp v130, v44 row_ror:15 row_mask:0xf bank_mask:0xf
	v_mul_f32_e32 v139, v192, v193
	v_mul_f32_e32 v142, v142, v135
	v_cndmask_b32_e64 v131, v130, v185, s[12:13]
	v_fma_f32 v192, v140, v134, v136
	v_mov_b32_e32 v134, v44
	v_mov_b32_e32 v135, v144
	v_mov_b32_e32 v130, v132
	v_pk_mul_f32 v[130:131], v[134:135], v[130:131]
	v_mov_b32_e32 v161, v171
	v_add_f32_e32 v130, v130, v192
	v_add_f32_e32 v192, v130, v131
	v_mov_b32_dpp v161, v28 row_ror:1 row_mask:0xf bank_mask:0xf
	v_mov_b32_e32 v189, v171
	v_mul_f32_e32 v130, 0xbfb8aa3b, v192
	v_exp_f32_e32 v193, v130
	v_mov_b32_dpp v189, v12 row_ror:15 row_mask:0xf bank_mask:0xf
	v_cndmask_b32_e64 v130, v161, v149, s[14:15]
	v_cndmask_b32_e64 v131, v185, v189, s[12:13]
	v_fma_f32 v149, v140, v130, v136
	v_mov_b32_e32 v134, v28
	v_mov_b32_e32 v130, v132
	v_pk_mul_f32 v[130:131], v[134:135], v[130:131]
	v_mov_b32_e32 v188, v171
	v_add_f32_e32 v130, v130, v149
	v_add_f32_e32 v149, v130, v131
	v_mul_f32_e32 v130, 0xbfb8aa3b, v149
	v_exp_f32_e32 v130, v130
	v_mov_b32_dpp v188, v12 row_ror:1 row_mask:0xf bank_mask:0xf
	v_mov_b32_e32 v191, v171
	v_add_f32_e32 v131, 1.0, v193
	v_add_f32_e32 v193, 1.0, v130
	v_mov_b32_dpp v191, v4 row_ror:15 row_mask:0xf bank_mask:0xf
	v_cndmask_b32_e64 v130, v188, v161, s[14:15]
	v_rcp_f32_e32 v185, v131
	v_cndmask_b32_e64 v131, v189, v191, s[12:13]
	v_fma_f32 v161, v140, v130, v136
	v_mov_b32_e32 v134, v12
	v_mov_b32_e32 v130, v132
	v_pk_mul_f32 v[130:131], v[134:135], v[130:131]
	v_mov_b32_e32 v190, v171
	v_add_f32_e32 v130, v130, v161
	v_add_f32_e32 v161, v130, v131
	v_mov_b32_dpp v190, v4 row_ror:1 row_mask:0xf bank_mask:0xf
	v_mul_f32_e32 v130, 0xbfb8aa3b, v161
	v_cndmask_b32_e64 v131, v190, v188, s[14:15]
	v_exp_f32_e32 v189, v130
	v_cndmask_b32_e64 v130, v191, 0, s[12:13]
	v_fma_f32 v136, v140, v131, v136
	v_mov_b32_e32 v134, v144
	v_mov_b32_e32 v135, v4
	v_mov_b32_e32 v131, v132
	v_pk_mul_f32 v[130:131], v[134:135], v[130:131]
	v_rcp_f32_e32 v132, v193
	v_add_f32_e32 v131, v131, v136
	v_add_f32_e32 v130, v130, v131
	v_mul_f32_e32 v131, 0xbfb8aa3b, v130
	v_exp_f32_e32 v131, v131
	v_add_f32_e32 v134, 1.0, v189
	v_rcp_f32_e32 v134, v134
	v_mul_f32_e32 v136, v149, v132
	v_add_f32_e32 v131, 1.0, v131
	v_rcp_f32_e32 v131, v131
	v_mov_b32_e32 v132, v171
	v_mul_f32_e32 v134, v161, v134
	v_mov_b32_e32 v161, v171
	v_mul_f32_e32 v140, v130, v131
	v_mov_b32_dpp v132, v45 row_ror:1 row_mask:0xf bank_mask:0xf
	v_mov_b32_e32 v130, v171
	v_mov_b32_dpp v161, v29 row_ror:15 row_mask:0xf bank_mask:0xf
	v_cndmask_b32_e64 v144, v132, 0, s[14:15]
	v_mov_b32_dpp v130, v45 row_ror:15 row_mask:0xf bank_mask:0xf
	v_cndmask_b32_e64 v131, v130, v161, s[12:13]
	v_fma_f32 v191, v141, v144, v137
	v_mov_b32_e32 v144, v45
	v_mov_b32_e32 v130, v133
	v_pk_mul_f32 v[130:131], v[144:145], v[130:131]
	v_mov_b32_e32 v149, v171
	v_add_f32_e32 v130, v130, v191
	v_add_f32_e32 v191, v130, v131
	v_mov_b32_dpp v149, v29 row_ror:1 row_mask:0xf bank_mask:0xf
	v_mov_b32_e32 v188, v171
	v_mul_f32_e32 v130, 0xbfb8aa3b, v191
	v_mul_f32_e32 v135, v192, v185
	v_mov_b32_dpp v188, v13 row_ror:15 row_mask:0xf bank_mask:0xf
	v_exp_f32_e32 v192, v130
	v_cndmask_b32_e64 v130, v149, v132, s[14:15]
	v_cndmask_b32_e64 v131, v161, v188, s[12:13]
	v_fma_f32 v132, v141, v130, v137
	v_mov_b32_e32 v144, v29
	v_mov_b32_e32 v130, v133
	v_pk_mul_f32 v[130:131], v[144:145], v[130:131]
	v_mov_b32_e32 v185, v171
	v_add_f32_e32 v130, v130, v132
	v_add_f32_e32 v161, v130, v131
	v_mul_f32_e32 v130, 0xbfb8aa3b, v161
	v_exp_f32_e32 v130, v130
	v_mov_b32_dpp v185, v13 row_ror:1 row_mask:0xf bank_mask:0xf
	v_mov_b32_e32 v190, v171
	v_add_f32_e32 v131, 1.0, v192
	v_add_f32_e32 v193, 1.0, v130
	v_mov_b32_dpp v190, v5 row_ror:15 row_mask:0xf bank_mask:0xf
	v_cndmask_b32_e64 v130, v185, v149, s[14:15]
	v_rcp_f32_e32 v192, v131
	v_cndmask_b32_e64 v131, v188, v190, s[12:13]
	v_fma_f32 v132, v141, v130, v137
	v_mov_b32_e32 v144, v13
	v_mov_b32_e32 v130, v133
	v_pk_mul_f32 v[130:131], v[144:145], v[130:131]
	v_mov_b32_e32 v189, v171
	v_add_f32_e32 v130, v130, v132
	v_add_f32_e32 v144, v130, v131
	v_mov_b32_dpp v189, v5 row_ror:1 row_mask:0xf bank_mask:0xf
	v_mul_f32_e32 v130, 0xbfb8aa3b, v144
	v_exp_f32_e32 v149, v130
	v_cndmask_b32_e64 v130, v189, v185, s[14:15]
	v_cndmask_b32_e64 v132, v190, 0, s[12:13]
	v_fmac_f32_e32 v137, v141, v130
	v_mov_b32_e32 v130, v145
	v_mov_b32_e32 v131, v5
	v_pk_mul_f32 v[130:131], v[130:131], v[132:133]
	v_add_f32_e32 v133, 1.0, v149
	v_add_f32_e32 v131, v131, v137
	v_add_f32_e32 v130, v130, v131
	v_mul_f32_e32 v131, 0xbfb8aa3b, v130
	v_exp_f32_e32 v131, v131
	v_rcp_f32_e32 v132, v193
	v_rcp_f32_e32 v133, v133
	v_mul_f32_e32 v137, v191, v192
	v_add_f32_e32 v131, 1.0, v131
	v_rcp_f32_e32 v131, v131
	v_mul_f32_e32 v141, v161, v132
	v_mul_f32_e32 v144, v144, v133
	v_mul_f32_e32 v145, v130, v131
	v_cvt_pk_bf16_f32 v130, v177, v155
	v_cvt_pk_bf16_f32 v131, v182, v157
	v_cvt_pk_bf16_f32 v132, v152, v139
	v_cvt_pk_bf16_f32 v133, v135, v137
	global_store_dwordx4 v[200:201], v[130:133], off offset:256
	s_nop 1
	v_cvt_pk_bf16_f32 v130, v170, v154
	v_cvt_pk_bf16_f32 v131, v179, v159
	v_cvt_pk_bf16_f32 v132, v138, v143
	v_cvt_pk_bf16_f32 v133, v136, v141
	global_store_dwordx4 v[202:203], v[130:133], off offset:256
	s_nop 1
	v_cvt_pk_bf16_f32 v130, v150, v151
	v_cvt_pk_bf16_f32 v131, v183, v156
	v_cvt_pk_bf16_f32 v132, v153, v142
	v_cvt_pk_bf16_f32 v133, v134, v144
	global_store_dwordx4 v[204:205], v[130:133], off offset:256
	s_nop 1
	v_cvt_pk_bf16_f32 v130, v146, v147
	v_cvt_pk_bf16_f32 v131, v184, v158
	v_cvt_pk_bf16_f32 v132, v160, v148
	v_cvt_pk_bf16_f32 v133, v140, v145
	s_mov_b32 s98, 1
	global_store_dwordx4 v[206:207], v[130:133], off offset:256
; __device__ __forceinline__ unsigned cvt_pk_bf16(float lo, float hi) { unsigned r; asm volatile("v_cvt_pk_bf16_f32 %0, %1, %2" : "=v"(r) : "v"(lo), "v"(hi)); return r; }
;     __device__ __forceinline__ void operator()(const f32x4 (&acc)[2][2][4][2], const pg8::Unit& u, int wr, int wc, int fr, int fq_in) const {
;     ...
;             if (u.pm >= 64) {
; #pragma unroll
;                 for (int ai = 0; ai < 2; ++ai)
; #pragma unroll
;                     for (int m = 0; m < 4; ++m) { bf16* rowp = XBCR + (size_t)(row0 - M + ai * 128 + m * 16) * XBCW + col0;
; #pragma unroll
;                         for (int bj = 0; bj < 2; ++bj) { const f32x4 v0 = acc[ai][bj][m][0], v1 = acc[ai][bj][m][1];
;                             u32x4 w; w.x = pg8::cvt_pk_bf16(v0[0], v0[1]); w.y = pg8::cvt_pk_bf16(v0[2], v0[3]); w.z = pg8::cvt_pk_bf16(v1[0], v1[1]); w.w = pg8::cvt_pk_bf16(v1[2], v1[3]);
;                             *(u32x4*)(rowp + bj * 128) = w; } }
.LBB0_480:
	s_andn2_b64 vcc, exec, s[0:1]
	s_cbranch_vccnz .LBB0_482
	v_add_u32_e32 v132, 0xffffc000, v178
	v_mov_b64_e32 v[130:131], s[30:31]
	v_mad_i64_i32 v[134:135], s[0:1], v132, s93, v[130:131]
	v_lshlrev_b64 v[132:133], 1, v[180:181]
	v_lshl_add_u64 v[134:135], v[134:135], 0, v[132:133]
	v_cvt_pk_bf16_f32 v126, v126, v127
	v_cvt_pk_bf16_f32 v127, v128, v129
	v_cvt_pk_bf16_f32 v128, v122, v123
	v_cvt_pk_bf16_f32 v129, v124, v125
	global_store_dwordx4 v[134:135], v[126:129], off
	v_cvt_pk_bf16_f32 v114, v114, v115
	v_cvt_pk_bf16_f32 v115, v116, v117
	v_cvt_pk_bf16_f32 v116, v106, v107
	v_add_u32_e32 v106, 0xffffc010, v178
	v_mad_i64_i32 v[106:107], s[0:1], v106, s93, v[130:131]
	v_cvt_pk_bf16_f32 v117, v108, v109
	global_store_dwordx4 v[134:135], v[114:117], off offset:256
	s_nop 1
	v_lshl_add_u64 v[114:115], v[106:107], 0, v[132:133]
	v_cvt_pk_bf16_f32 v106, v118, v119
	v_cvt_pk_bf16_f32 v107, v120, v121
	v_cvt_pk_bf16_f32 v108, v110, v111
	v_cvt_pk_bf16_f32 v109, v112, v113
	global_store_dwordx4 v[114:115], v[106:109], off
	v_cvt_pk_bf16_f32 v98, v98, v99
	v_cvt_pk_bf16_f32 v99, v100, v101
	v_cvt_pk_bf16_f32 v100, v90, v91
	v_add_u32_e32 v90, 0xffffc020, v178
	v_mad_i64_i32 v[90:91], s[0:1], v90, s93, v[130:131]
	v_cvt_pk_bf16_f32 v101, v92, v93
	global_store_dwordx4 v[114:115], v[98:101], off offset:256
	s_nop 1
	v_lshl_add_u64 v[98:99], v[90:91], 0, v[132:133]
	v_cvt_pk_bf16_f32 v90, v102, v103
	v_cvt_pk_bf16_f32 v91, v104, v105
	v_cvt_pk_bf16_f32 v92, v94, v95
	v_cvt_pk_bf16_f32 v93, v96, v97
	global_store_dwordx4 v[98:99], v[90:93], off
	v_cvt_pk_bf16_f32 v82, v82, v83
	v_cvt_pk_bf16_f32 v83, v84, v85
	v_cvt_pk_bf16_f32 v84, v74, v75
	v_add_u32_e32 v74, 0xffffc030, v178
	v_mad_i64_i32 v[74:75], s[0:1], v74, s93, v[130:131]
	v_cvt_pk_bf16_f32 v85, v76, v77
	global_store_dwordx4 v[98:99], v[82:85], off offset:256
	s_nop 1
	v_lshl_add_u64 v[82:83], v[74:75], 0, v[132:133]
	v_cvt_pk_bf16_f32 v74, v86, v87
	v_cvt_pk_bf16_f32 v75, v88, v89
	v_cvt_pk_bf16_f32 v76, v78, v79
	v_cvt_pk_bf16_f32 v77, v80, v81
	global_store_dwordx4 v[82:83], v[74:77], off
	v_cvt_pk_bf16_f32 v70, v70, v71
	v_cvt_pk_bf16_f32 v71, v72, v73
	v_cvt_pk_bf16_f32 v72, v66, v67
	v_add_u32_e32 v66, 0xffffc080, v178
	v_mad_i64_i32 v[66:67], s[0:1], v66, s93, v[130:131]
	v_lshl_add_u64 v[66:67], v[66:67], 0, v[132:133]
	v_cvt_pk_bf16_f32 v73, v68, v69
	global_store_dwordx4 v[82:83], v[70:73], off offset:256
	v_cvt_pk_bf16_f32 v62, v62, v63
	v_cvt_pk_bf16_f32 v63, v64, v65
	v_cvt_pk_bf16_f32 v64, v58, v59
	v_cvt_pk_bf16_f32 v65, v60, v61
	global_store_dwordx4 v[66:67], v[62:65], off
	v_cvt_pk_bf16_f32 v50, v50, v51
	v_cvt_pk_bf16_f32 v51, v52, v53
	v_cvt_pk_bf16_f32 v52, v42, v43
	v_add_u32_e32 v42, 0xffffc090, v178
	v_mad_i64_i32 v[42:43], s[0:1], v42, s93, v[130:131]
	v_cvt_pk_bf16_f32 v53, v44, v45
	global_store_dwordx4 v[66:67], v[50:53], off offset:256
	s_nop 1
	v_lshl_add_u64 v[50:51], v[42:43], 0, v[132:133]
	v_cvt_pk_bf16_f32 v42, v54, v55
	v_cvt_pk_bf16_f32 v43, v56, v57
	v_cvt_pk_bf16_f32 v44, v46, v47
	v_cvt_pk_bf16_f32 v45, v48, v49
	global_store_dwordx4 v[50:51], v[42:45], off
	v_cvt_pk_bf16_f32 v34, v34, v35
	v_cvt_pk_bf16_f32 v35, v36, v37
	v_cvt_pk_bf16_f32 v36, v26, v27
	v_add_u32_e32 v26, 0xffffc0a0, v178
	v_mad_i64_i32 v[26:27], s[0:1], v26, s93, v[130:131]
	v_cvt_pk_bf16_f32 v37, v28, v29
	global_store_dwordx4 v[50:51], v[34:37], off offset:256
	s_nop 1
	v_lshl_add_u64 v[34:35], v[26:27], 0, v[132:133]
	v_cvt_pk_bf16_f32 v26, v38, v39
	v_cvt_pk_bf16_f32 v27, v40, v41
	v_cvt_pk_bf16_f32 v28, v30, v31
	v_cvt_pk_bf16_f32 v29, v32, v33
	global_store_dwordx4 v[34:35], v[26:29], off
	v_cvt_pk_bf16_f32 v18, v18, v19
	v_cvt_pk_bf16_f32 v19, v20, v21
	v_cvt_pk_bf16_f32 v20, v10, v11
	v_add_u32_e32 v10, 0xffffc0b0, v178
	v_mad_i64_i32 v[10:11], s[0:1], v10, s93, v[130:131]
	v_cvt_pk_bf16_f32 v21, v12, v13
	global_store_dwordx4 v[34:35], v[18:21], off offset:256
	s_nop 1
	v_lshl_add_u64 v[18:19], v[10:11], 0, v[132:133]
	v_cvt_pk_bf16_f32 v10, v22, v23
	v_cvt_pk_bf16_f32 v11, v24, v25
	v_cvt_pk_bf16_f32 v12, v14, v15
	v_cvt_pk_bf16_f32 v13, v16, v17
	global_store_dwordx4 v[18:19], v[10:13], off
	v_cvt_pk_bf16_f32 v6, v6, v7
	v_cvt_pk_bf16_f32 v7, v8, v9
	v_cvt_pk_bf16_f32 v8, v2, v3
	v_cvt_pk_bf16_f32 v9, v4, v5
	s_mov_b32 s98, 1
	global_store_dwordx4 v[18:19], v[6:9], off offset:256
